# dead-instruction removal (redundant priority toggles, XNACK-only pads between back-to-back loads across the file) stacked with stage K fragment reads three ahead over four register quads
# baseline (speedup 1.0000x reference)
;     const int nblk = ncols / 32, kb = item / nblk, nb = item % nblk, k0 = 64 * kb, n0 = 32 * nb;
; #pragma unroll 8
;     for (int i = 0; i < 32; ++i) { const int kk = 2 * i + (lane >> 5); scr[kk * 33 + (lane & 31)] = W[(size_t)(k0 + kk) * ldw + n0 + (lane & 31)]; }
;     asm volatile("s_waitcnt lgkmcnt(0)" ::: "memory");
.LBB0_31:
	v_add_u32_e32 v47, s20, v4
	v_add_u32_e32 v56, 0xffffe700, v47
	v_add_u32_e32 v58, 0xffffe702, v47
	v_add_u32_e32 v60, 0xffffe704, v47
	v_add_u32_e32 v62, 0xffffe706, v47
	v_add_u32_e32 v76, 0xffffe708, v47
	v_add_u32_e32 v78, 0xffffe70a, v47
	v_add_u32_e32 v80, 0xffffe70c, v47
	v_add_u32_e32 v82, 0xffffe70e, v47
	v_ashrrev_i32_e32 v57, 31, v56
	v_ashrrev_i32_e32 v59, 31, v58
	v_ashrrev_i32_e32 v61, 31, v60
	v_ashrrev_i32_e32 v63, 31, v62
	v_ashrrev_i32_e32 v77, 31, v76
	v_ashrrev_i32_e32 v79, 31, v78
	v_ashrrev_i32_e32 v81, 31, v80
	v_ashrrev_i32_e32 v83, 31, v82
	v_lshlrev_b64 v[56:57], 12, v[56:57]
	v_lshlrev_b64 v[58:59], 12, v[58:59]
	v_lshlrev_b64 v[60:61], 12, v[60:61]
	v_lshlrev_b64 v[62:63], 12, v[62:63]
	v_lshlrev_b64 v[76:77], 12, v[76:77]
	v_lshlrev_b64 v[78:79], 12, v[78:79]
	v_lshlrev_b64 v[80:81], 12, v[80:81]
	v_lshlrev_b64 v[82:83], 12, v[82:83]
	v_lshl_add_u64 v[56:57], v[54:55], 0, v[56:57]
	v_lshl_add_u64 v[58:59], v[54:55], 0, v[58:59]
	v_lshl_add_u64 v[60:61], v[54:55], 0, v[60:61]
	v_lshl_add_u64 v[62:63], v[54:55], 0, v[62:63]
	v_lshl_add_u64 v[76:77], v[54:55], 0, v[76:77]
	v_lshl_add_u64 v[78:79], v[54:55], 0, v[78:79]
	v_lshl_add_u64 v[80:81], v[54:55], 0, v[80:81]
	v_lshl_add_u64 v[82:83], v[54:55], 0, v[82:83]
	global_load_dword v47, v[56:57], off
	global_load_dword v49, v[58:59], off
	global_load_dword v51, v[60:61], off
	global_load_dword v56, v[62:63], off
	global_load_dword v57, v[76:77], off
	global_load_dword v58, v[78:79], off
	global_load_dword v59, v[80:81], off
	global_load_dword v60, v[82:83], off
	s_add_i32 s20, s20, 16
	v_add_u32_e32 v61, 0x400, v45
	s_cmp_eq_u32 s20, 64
	s_waitcnt vmcnt(6)
	ds_write2_b32 v45, v47, v49 offset1:66
	s_waitcnt vmcnt(4)
	ds_write2_b32 v45, v51, v56 offset0:132 offset1:198
	s_waitcnt vmcnt(2)
	ds_write2_b32 v61, v57, v58 offset0:8 offset1:74
	s_waitcnt vmcnt(0)
	ds_write2_b32 v61, v59, v60 offset0:140 offset1:206
	v_add_u32_e32 v45, 0x840, v45
	s_cbranch_scc0 .LBB0_31

; __device__ __forceinline__ u32x4 pk8(const f32x4 a, const f32x4 b) { u32x4 w; w.x = cvt_pk_bf16(a[0], a[1]); w.y = cvt_pk_bf16(a[2], a[3]); w.z = cvt_pk_bf16(b[0], b[1]); w.w = cvt_pk_bf16(b[2], b[3]); return w; }
; __device__ __forceinline__ void cvt_chunk(const float* src, bf16* dst, size_t chunk, int lane) {
;     const f32x4* s = (const f32x4*)(src + chunk * 512) + lane * 2; const f32x4 a = s[0], b = s[1];
;     *(v4u*)(dst + chunk * 512 + lane * 8) = pk8(a, b);
; }
; __device__ __forceinline__ void prep_phase(Frame& F, const Args& a, int layer, int blk, int nblk_, int part) {
;     ...
;         for (int it = gw; it < ntot; it += NGW) {
;             int r = it;
;             if (r < n2) { cvt8_chunk(ut, (unsigned char*)(db + DB_U), r, lane, 256.f); continue; } r -= n2;
;             if (r < n2) { cvt8_chunk(vt, (unsigned char*)(db + DB_V), r, lane, 64.f); continue; } r -= n2;
;             if (r < n4) { cvt_chunk(pin, (bf16*)(db + DB_PB), r, lane); continue; } r -= n4;
;             if (r < n1) { cvt_chunk(keys, (bf16*)(db + DB_KEYS), r, lane); continue; } r -= n1;
;             {
;                 const int e0 = r * 512 + lane * 8, tq = (e0 >> 7) & 127, p0 = e0 & 127;
;                 const f32x4* s = (const f32x4*)(gws + e0); f32x4 x0 = s[0], x1 = s[1];
; #pragma unroll
;                 for (int j = 0; j < 4; ++j) { if (p0 + j > tq) x0[j] = 0.f; if (p0 + 4 + j > tq) x1[j] = 0.f; }
;                 *(v4u*)((bf16*)(db + DB_GMW) + e0) = pk8(x0, x1);
;             }
.LBB0_95:
	s_cmp_gt_i32 s14, -1
	s_mov_b64 s[12:13], -1
	s_cbranch_scc0 .LBB0_105
	s_cmpk_gt_u32 s14, 0x3fff
	s_cbranch_scc0 .LBB0_102
	s_add_i32 s12, s14, 0xffffc000
	s_cmpk_gt_u32 s12, 0x1ff
	s_mov_b64 s[12:13], -1
	s_cbranch_scc0 .LBB0_99
	v_add_u32_e32 v36, s4, v23
	v_readlane_b32 s36, v251, 34
	v_ashrrev_i32_e32 v37, 31, v36
	v_readlane_b32 s46, v251, 44
	v_readlane_b32 s47, v251, 45
	v_bfe_u32 v3, v36, 7, 7
	v_mov_b32_e32 v32, s5
	v_lshl_add_u64 v[28:29], v[36:37], 2, s[46:47]
	global_load_dwordx4 v[24:27], v[28:29], off
	global_load_dwordx4 v[28:31], v[28:29], off offset:16
	v_cmp_gt_u32_e32 vcc, v1, v3
	v_mov_b32_e32 v34, s5
	v_lshl_add_u64 v[36:37], v[36:37], 1, s[0:1]
	v_readlane_b32 s37, v251, 35
	v_readlane_b32 s38, v251, 36
	v_readlane_b32 s39, v251, 37
	v_readlane_b32 s40, v251, 38
	v_readlane_b32 s41, v251, 39
	v_readlane_b32 s42, v251, 40
	v_readlane_b32 s43, v251, 41
	v_readlane_b32 s44, v251, 42
	v_readlane_b32 s45, v251, 43
	v_readlane_b32 s48, v251, 46
	v_readlane_b32 s49, v251, 47
	v_readlane_b32 s50, v251, 48
	v_readlane_b32 s51, v251, 49
	s_mov_b64 s[12:13], 0
	s_waitcnt vmcnt(1)
	v_cndmask_b32_e32 v33, v26, v26, vcc
	v_cndmask_b32_e32 v35, v27, v27, vcc
	v_cndmask_b32_e32 v32, v24, v32, vcc
	v_cmp_gt_u32_e32 vcc, v17, v3
	s_waitcnt vmcnt(0)
	s_nop 0
	v_cndmask_b32_e32 v28, v28, v34, vcc
	v_cndmask_b32_e32 v31, v31, v31, vcc
	v_cndmask_b32_e32 v30, v30, v30, vcc
	v_cndmask_b32_e32 v29, v29, v29, vcc
	v_cmp_lt_u32_e32 vcc, v1, v3
	s_nop 1
	v_cndmask_b32_e32 v24, v32, v24, vcc
	v_cndmask_b32_e32 v27, v35, v27, vcc
	v_cndmask_b32_e32 v26, v33, v26, vcc
	v_cndmask_b32_e32 v25, 0, v25, vcc
	v_cmp_le_u32_e32 vcc, v18, v3
	v_cvt_pk_bf16_f32 v24, v24, v25
	s_nop 1
	v_cndmask_b32_e32 v29, 0, v29, vcc
	v_cmp_le_u32_e32 vcc, v20, v3
	s_nop 1
	v_cndmask_b32_e32 v30, 0, v30, vcc
	v_cmp_le_u32_e32 vcc, v22, v3
	s_nop 1
	v_cndmask_b32_e32 v31, 0, v31, vcc
	v_cmp_le_u32_e32 vcc, v19, v3
	s_nop 1
	v_cndmask_b32_e32 v26, 0, v26, vcc
	v_cmp_le_u32_e32 vcc, v21, v3
	s_nop 1
	v_cndmask_b32_e32 v3, 0, v27, vcc
	v_cvt_pk_bf16_f32 v25, v26, v3
	v_cvt_pk_bf16_f32 v26, v28, v29
	v_cvt_pk_bf16_f32 v27, v30, v31
	global_store_dwordx4 v[36:37], v[24:27], off
.LBB0_99:
	s_andn2_b64 vcc, exec, s[12:13]
	s_cbranch_vccnz .LBB0_101
	s_add_i32 s12, s4, 0xff800000
	s_mov_b32 s13, s5
	v_lshl_add_u64 v[28:29], s[12:13], 2, v[4:5]
	global_load_dwordx4 v[24:27], v[28:29], off
	global_load_dwordx4 v[28:31], v[28:29], off offset:16
	s_waitcnt vmcnt(1)
	v_cvt_pk_bf16_f32 v24, v24, v25
	v_cvt_pk_bf16_f32 v25, v26, v27
	s_waitcnt vmcnt(0)
	v_cvt_pk_bf16_f32 v26, v28, v29
	v_lshl_add_u64 v[28:29], s[12:13], 1, v[6:7]
	v_cvt_pk_bf16_f32 v27, v30, v31
	global_store_dwordx4 v[28:29], v[24:27], off

; __device__ __forceinline__ u32x4 pk8(const f32x4 a, const f32x4 b) { u32x4 w; w.x = cvt_pk_bf16(a[0], a[1]); w.y = cvt_pk_bf16(a[2], a[3]); w.z = cvt_pk_bf16(b[0], b[1]); w.w = cvt_pk_bf16(b[2], b[3]); return w; }
; __device__ __forceinline__ void cvt_chunk(const float* src, bf16* dst, size_t chunk, int lane) {
;     const f32x4* s = (const f32x4*)(src + chunk * 512) + lane * 2; const f32x4 a = s[0], b = s[1];
;     *(v4u*)(dst + chunk * 512 + lane * 8) = pk8(a, b);
; }
; __device__ __forceinline__ void prep_phase(Frame& F, const Args& a, int layer, int blk, int nblk_, int part) {
;     ...
;             if (r < n4) { cvt_chunk(pin, (bf16*)(db + DB_PB), r, lane); continue; } r -= n4;
.LBB0_102:
	s_andn2_b64 vcc, exec, s[12:13]
	s_cbranch_vccnz .LBB0_104
	v_lshl_add_u64 v[28:29], s[4:5], 2, v[8:9]
	global_load_dwordx4 v[24:27], v[28:29], off
	global_load_dwordx4 v[28:31], v[28:29], off offset:16
	s_waitcnt vmcnt(1)
	v_cvt_pk_bf16_f32 v24, v24, v25
	v_cvt_pk_bf16_f32 v25, v26, v27
	s_waitcnt vmcnt(0)
	v_cvt_pk_bf16_f32 v26, v28, v29
	v_lshl_add_u64 v[28:29], s[4:5], 1, v[10:11]
	v_cvt_pk_bf16_f32 v27, v30, v31
	global_store_dwordx4 v[28:29], v[24:27], off

; __device__ __forceinline__ void norm_row_nx(const float* hrow, float* hcopy, const float* g, bf16* NX, int t, int lane) {
;     const f32x4* xr = (const f32x4*)hrow + lane; f32x4 v[4]; float s = 0.f;
; #pragma unroll
;     for (int j = 0; j < 4; ++j) { v[j] = xr[64 * j]; s += (v[j].x * v[j].x + v[j].y * v[j].y) + (v[j].z * v[j].z + v[j].w * v[j].w); }
;     if (hcopy) {
; #pragma unroll
;         for (int j = 0; j < 4; ++j) ((f32x4*)hcopy)[lane + 64 * j] = v[j]; }
.LBB0_112:
	v_readlane_b32 s36, v251, 2
	v_readlane_b32 s37, v251, 3
	s_and_b64 vcc, exec, s[0:1]
	v_readlane_b32 s38, v251, 4
	v_lshl_add_u64 v[0:1], s[36:37], 0, v[26:27]
	global_load_dwordx4 v[12:15], v[0:1], off
	global_load_dwordx4 v[8:11], v[0:1], off offset:1024
	global_load_dwordx4 v[4:7], v[0:1], off offset:2048
	global_load_dwordx4 v[0:3], v[0:1], off offset:3072
	v_readlane_b32 s39, v251, 5
	v_readlane_b32 s40, v251, 6
	v_readlane_b32 s41, v251, 7
	v_readlane_b32 s42, v251, 8
	v_readlane_b32 s43, v251, 9
	v_readlane_b32 s44, v251, 10
	v_readlane_b32 s45, v251, 11
	v_readlane_b32 s46, v251, 12
	v_readlane_b32 s47, v251, 13
	v_readlane_b32 s48, v251, 14
	v_readlane_b32 s49, v251, 15
	v_readlane_b32 s50, v251, 16
	v_readlane_b32 s51, v251, 17
	s_cbranch_vccnz .LBB0_111
	v_lshl_add_u64 v[30:31], s[24:25], 0, v[26:27]
	s_waitcnt vmcnt(3)
	global_store_dwordx4 v[30:31], v[12:15], off
	s_waitcnt vmcnt(3)
	global_store_dwordx4 v[30:31], v[8:11], off offset:1024
	s_waitcnt vmcnt(3)
	global_store_dwordx4 v[30:31], v[4:7], off offset:2048
	s_waitcnt vmcnt(3)
	global_store_dwordx4 v[30:31], v[0:3], off offset:3072
	s_branch .LBB0_111

; __device__ __forceinline__ void unpk8(const u32x4 w, f32x4& a, f32x4& b) { a = (f32x4){bflo(w.x), bfhi(w.x), bflo(w.y), bfhi(w.y)}; b = (f32x4){bflo(w.z), bfhi(w.z), bflo(w.w), bfhi(w.w)}; }
; __device__ __forceinline__ u32x4 pk8(const f32x4 a, const f32x4 b) { u32x4 w; w.x = cvt_pk_bf16(a[0], a[1]); w.y = cvt_pk_bf16(a[2], a[3]); w.z = cvt_pk_bf16(b[0], b[1]); w.w = cvt_pk_bf16(b[2], b[3]); return w; }
; __device__ __forceinline__ float fsig(float x) { return __builtin_amdgcn_rcpf(1.f + __builtin_amdgcn_exp2f(-1.44269504f * x)); }
;     __device__ __forceinline__ void operator()(const f32x4 (&acc)[2][2][4][2], const Unit& u, int wr, int wc, int fr, int fq) const {
;         const int row0 = u.pm * BM + wr * 64 + fr, col0 = u.pn * 256 + wc * 32 + 8 * fq;
;         f32x4 bv[2][2];
; #pragma unroll
;         for (int bj = 0; bj < 2; ++bj)
; #pragma unroll
;             for (int n = 0; n < 2; ++n) bv[bj][n] = *(const f32x4*)(v0b + col0 + bj * HALF + 4 * n);
;         EPI_ROWS_BEGIN
; #pragma unroll
;             for (int bj = 0; bj < 2; ++bj) { bf16_t* zp = zrkv + row * 3072 + 2048 + col0 + bj * HALF;
;                 f32x4 z0, z1, f0, f1; unpk8(*(const u32x4*)zp, z0, z1); unpk8(*(const u32x4*)(vf + row * 1024 + col0 + bj * HALF), f0, f1);
;                 const f32x4 m0 = act4(acc[ai][bj][m][0] + bv[bj][0], 2), m1 = act4(acc[ai][bj][m][1] + bv[bj][1], 2);
;                 *(u32x4*)zp = pk8(z0 + (f0 - z0) * m0, z1 + (f1 - z1) * m1); }
.LBB0_767:
	v_lshl_or_b32 v158, s82, 8, v177
	v_ashrrev_i32_e32 v159, 31, v158
	v_lshl_add_u64 v[22:23], v[158:159], 2, s[52:53]
	global_load_dwordx4 v[34:37], v[22:23], off offset:16
	global_load_dwordx4 v[42:45], v[22:23], off
	global_load_dwordx4 v[18:21], v[22:23], off offset:528
	global_load_dwordx4 v[22:25], v[22:23], off offset:512
	v_lshl_add_u32 v162, s48, 8, v1
	v_mov_b64_e32 v[160:161], s[54:55]
	s_movk_i32 s27, 0x1800
	v_ashrrev_i32_e32 v163, 31, v162
	v_mad_i64_i32 v[164:165], s[60:61], v162, s27, v[160:161]
	v_lshlrev_b64 v[158:159], 1, v[158:159]
	v_lshlrev_b64 v[166:167], 11, v[162:163]
	v_lshl_add_u64 v[164:165], v[164:165], 0, v[158:159]
	v_add_co_u32_e32 v164, vcc, s9, v164
	v_lshl_add_u64 v[166:167], s[56:57], 0, v[166:167]
	s_nop 0
	v_addc_co_u32_e32 v165, vcc, 0, v165, vcc
	v_lshl_add_u64 v[166:167], v[166:167], 0, v[158:159]
	global_load_dwordx4 v[168:171], v[164:165], off
	global_load_dwordx4 v[180:183], v[166:167], off
	global_load_dwordx4 v[190:193], v[164:165], off offset:256
	global_load_dwordx4 v[194:197], v[166:167], off offset:256
	s_waitcnt vmcnt(0)
	v_pk_add_f32 v[140:141], v[140:141], v[36:37]
	v_pk_add_f32 v[144:145], v[144:145], v[44:45]
	v_pk_add_f32 v[142:143], v[142:143], v[42:43]
	v_mul_f32_e32 v144, 0xbfb8aa3b, v144
	v_mul_f32_e32 v142, 0xbfb8aa3b, v142
	v_mul_f32_e32 v143, 0xbfb8aa3b, v143
	v_mul_f32_e32 v145, 0xbfb8aa3b, v145
	v_pk_add_f32 v[138:139], v[138:139], v[34:35]
	v_exp_f32_e32 v142, v142
	v_exp_f32_e32 v143, v143
	v_exp_f32_e32 v144, v144
	v_exp_f32_e32 v145, v145
	v_mul_f32_e32 v138, 0xbfb8aa3b, v138
	v_mul_f32_e32 v139, 0xbfb8aa3b, v139
	v_mul_f32_e32 v140, 0xbfb8aa3b, v140
	v_mul_f32_e32 v141, 0xbfb8aa3b, v141
	v_exp_f32_e32 v138, v138
	v_exp_f32_e32 v139, v139
	v_exp_f32_e32 v140, v140
	v_exp_f32_e32 v141, v141
	v_add_f32_e32 v142, 1.0, v142
	v_add_f32_e32 v143, 1.0, v143
	v_add_f32_e32 v144, 1.0, v144
	v_add_f32_e32 v145, 1.0, v145
	v_rcp_f32_e32 v142, v142
	v_rcp_f32_e32 v143, v143
	v_rcp_f32_e32 v144, v144
	v_rcp_f32_e32 v145, v145
	v_add_f32_e32 v138, 1.0, v138
	v_add_f32_e32 v139, 1.0, v139
	v_add_f32_e32 v140, 1.0, v140
	v_add_f32_e32 v141, 1.0, v141
	v_rcp_f32_e32 v138, v138
	v_rcp_f32_e32 v139, v139
	v_rcp_f32_e32 v140, v140
	v_rcp_f32_e32 v141, v141
	v_lshlrev_b32_e32 v172, 16, v168
	v_and_b32_e32 v173, 0xffff0000, v168
	v_lshlrev_b32_e32 v174, 16, v169
	v_and_b32_e32 v175, 0xffff0000, v169
	v_lshlrev_b32_e32 v163, 16, v180
	v_and_b32_e32 v179, 0xffff0000, v180
	v_lshlrev_b32_e32 v184, 16, v181
	v_and_b32_e32 v185, 0xffff0000, v181
	v_lshlrev_b32_e32 v168, 16, v170
	v_and_b32_e32 v169, 0xffff0000, v170
	v_lshlrev_b32_e32 v170, 16, v171
	v_and_b32_e32 v171, 0xffff0000, v171
	v_lshlrev_b32_e32 v186, 16, v182
	v_and_b32_e32 v187, 0xffff0000, v182
	v_lshlrev_b32_e32 v188, 16, v183
	v_and_b32_e32 v189, 0xffff0000, v183
	v_sub_f32_e32 v181, v179, v173
	v_sub_f32_e32 v180, v163, v172
	v_sub_f32_e32 v183, v185, v175
	v_sub_f32_e32 v182, v184, v174
	v_pk_fma_f32 v[144:145], v[144:145], v[182:183], v[174:175]
	v_pk_fma_f32 v[142:143], v[142:143], v[180:181], v[172:173]
	v_sub_f32_e32 v173, v187, v169
	v_sub_f32_e32 v172, v186, v168
	v_sub_f32_e32 v175, v189, v171
	v_sub_f32_e32 v174, v188, v170
	v_pk_fma_f32 v[170:171], v[140:141], v[174:175], v[170:171]
	v_pk_fma_f32 v[140:141], v[138:139], v[172:173], v[168:169]
	v_cvt_pk_bf16_f32 v138, v142, v143
	v_cvt_pk_bf16_f32 v139, v144, v145
	v_pk_add_f32 v[136:137], v[136:137], v[24:25]
	v_cvt_pk_bf16_f32 v140, v140, v141
	v_cvt_pk_bf16_f32 v141, v170, v171
	global_store_dwordx4 v[164:165], v[138:141], off
	v_pk_add_f32 v[134:135], v[134:135], v[22:23]
	v_mul_f32_e32 v136, 0xbfb8aa3b, v136
	v_mul_f32_e32 v134, 0xbfb8aa3b, v134
	v_mul_f32_e32 v135, 0xbfb8aa3b, v135
	v_mul_f32_e32 v137, 0xbfb8aa3b, v137
	v_pk_add_f32 v[132:133], v[132:133], v[20:21]
	v_pk_add_f32 v[130:131], v[130:131], v[18:19]
	v_exp_f32_e32 v134, v134
	v_exp_f32_e32 v135, v135
	v_exp_f32_e32 v136, v136
	v_exp_f32_e32 v137, v137
	v_mul_f32_e32 v130, 0xbfb8aa3b, v130
	v_mul_f32_e32 v131, 0xbfb8aa3b, v131
	v_mul_f32_e32 v132, 0xbfb8aa3b, v132
	v_mul_f32_e32 v133, 0xbfb8aa3b, v133
	v_exp_f32_e32 v130, v130
	v_exp_f32_e32 v131, v131
	v_exp_f32_e32 v132, v132
	v_exp_f32_e32 v133, v133
	v_add_f32_e32 v134, 1.0, v134
	v_add_f32_e32 v135, 1.0, v135
	v_add_f32_e32 v136, 1.0, v136
	v_add_f32_e32 v137, 1.0, v137
	v_rcp_f32_e32 v134, v134
	v_rcp_f32_e32 v135, v135
	v_rcp_f32_e32 v136, v136
	v_rcp_f32_e32 v137, v137
	v_add_f32_e32 v130, 1.0, v130
	v_add_f32_e32 v131, 1.0, v131
	v_add_f32_e32 v132, 1.0, v132
	v_add_f32_e32 v133, 1.0, v133
	v_rcp_f32_e32 v130, v130
	v_rcp_f32_e32 v131, v131
	v_rcp_f32_e32 v132, v132
	v_rcp_f32_e32 v133, v133
	v_pk_add_f32 v[128:129], v[128:129], v[44:45]
	v_pk_add_f32 v[126:127], v[126:127], v[42:43]
	v_mul_f32_e32 v128, 0xbfb8aa3b, v128
	v_mul_f32_e32 v126, 0xbfb8aa3b, v126
	v_mul_f32_e32 v127, 0xbfb8aa3b, v127
	v_mul_f32_e32 v129, 0xbfb8aa3b, v129
	v_pk_add_f32 v[124:125], v[124:125], v[36:37]
	v_pk_add_f32 v[122:123], v[122:123], v[34:35]
	v_exp_f32_e32 v126, v126
	v_exp_f32_e32 v127, v127
	v_exp_f32_e32 v128, v128
	v_exp_f32_e32 v129, v129
	v_mul_f32_e32 v122, 0xbfb8aa3b, v122
	v_mul_f32_e32 v123, 0xbfb8aa3b, v123
	v_mul_f32_e32 v124, 0xbfb8aa3b, v124
	v_mul_f32_e32 v125, 0xbfb8aa3b, v125
	v_exp_f32_e32 v122, v122
	v_exp_f32_e32 v123, v123
	v_exp_f32_e32 v124, v124
	v_exp_f32_e32 v125, v125
	v_add_f32_e32 v126, 1.0, v126
	v_add_f32_e32 v127, 1.0, v127
	v_add_f32_e32 v128, 1.0, v128
	v_add_f32_e32 v129, 1.0, v129
	v_rcp_f32_e32 v126, v126
	v_rcp_f32_e32 v127, v127
	v_rcp_f32_e32 v128, v128
	v_rcp_f32_e32 v129, v129
	v_add_f32_e32 v122, 1.0, v122
; __device__ __forceinline__ void unpk8(const u32x4 w, f32x4& a, f32x4& b) { a = (f32x4){bflo(w.x), bfhi(w.x), bflo(w.y), bfhi(w.y)}; b = (f32x4){bflo(w.z), bfhi(w.z), bflo(w.w), bfhi(w.w)}; }
; __device__ __forceinline__ u32x4 pk8(const f32x4 a, const f32x4 b) { u32x4 w; w.x = cvt_pk_bf16(a[0], a[1]); w.y = cvt_pk_bf16(a[2], a[3]); w.z = cvt_pk_bf16(b[0], b[1]); w.w = cvt_pk_bf16(b[2], b[3]); return w; }
; __device__ __forceinline__ float fsig(float x) { return __builtin_amdgcn_rcpf(1.f + __builtin_amdgcn_exp2f(-1.44269504f * x)); }
;     __device__ __forceinline__ void operator()(const f32x4 (&acc)[2][2][4][2], const Unit& u, int wr, int wc, int fr, int fq) const {
;     ...
;         EPI_ROWS_BEGIN
; #pragma unroll
;             for (int bj = 0; bj < 2; ++bj) { bf16_t* zp = zrkv + row * 3072 + 2048 + col0 + bj * HALF;
;                 f32x4 z0, z1, f0, f1; unpk8(*(const u32x4*)zp, z0, z1); unpk8(*(const u32x4*)(vf + row * 1024 + col0 + bj * HALF), f0, f1);
;                 const f32x4 m0 = act4(acc[ai][bj][m][0] + bv[bj][0], 2), m1 = act4(acc[ai][bj][m][1] + bv[bj][1], 2);
;                 *(u32x4*)zp = pk8(z0 + (f0 - z0) * m0, z1 + (f1 - z1) * m1); }
	v_add_f32_e32 v123, 1.0, v123
	v_add_f32_e32 v124, 1.0, v124
	v_add_f32_e32 v125, 1.0, v125
	v_rcp_f32_e32 v122, v122
	v_rcp_f32_e32 v123, v123
	v_rcp_f32_e32 v124, v124
	v_rcp_f32_e32 v125, v125
	v_pk_add_f32 v[120:121], v[120:121], v[24:25]
	v_pk_add_f32 v[118:119], v[118:119], v[22:23]
	v_mul_f32_e32 v120, 0xbfb8aa3b, v120
	v_mul_f32_e32 v118, 0xbfb8aa3b, v118
	v_mul_f32_e32 v119, 0xbfb8aa3b, v119
	v_mul_f32_e32 v121, 0xbfb8aa3b, v121
	v_pk_add_f32 v[116:117], v[116:117], v[20:21]
	v_pk_add_f32 v[114:115], v[114:115], v[18:19]
	v_lshlrev_b32_e32 v142, 16, v190
	v_and_b32_e32 v143, 0xffff0000, v190
	v_lshlrev_b32_e32 v144, 16, v191
	v_and_b32_e32 v145, 0xffff0000, v191
	v_lshlrev_b32_e32 v168, 16, v192
	v_and_b32_e32 v169, 0xffff0000, v192
	v_lshlrev_b32_e32 v170, 16, v193
	v_and_b32_e32 v171, 0xffff0000, v193
	v_exp_f32_e32 v118, v118
	v_exp_f32_e32 v119, v119
	v_exp_f32_e32 v120, v120
	v_exp_f32_e32 v121, v121
	v_mul_f32_e32 v114, 0xbfb8aa3b, v114
	v_mul_f32_e32 v115, 0xbfb8aa3b, v115
	v_mul_f32_e32 v116, 0xbfb8aa3b, v116
	v_mul_f32_e32 v117, 0xbfb8aa3b, v117
	v_exp_f32_e32 v114, v114
	v_exp_f32_e32 v115, v115
	v_exp_f32_e32 v116, v116
	v_exp_f32_e32 v117, v117
	v_add_f32_e32 v118, 1.0, v118
	v_add_f32_e32 v119, 1.0, v119
	v_add_f32_e32 v120, 1.0, v120
	v_add_f32_e32 v121, 1.0, v121
	v_rcp_f32_e32 v118, v118
	v_rcp_f32_e32 v119, v119
	v_rcp_f32_e32 v120, v120
	v_rcp_f32_e32 v121, v121
	v_add_f32_e32 v114, 1.0, v114
	v_add_f32_e32 v115, 1.0, v115
	v_add_f32_e32 v116, 1.0, v116
	v_add_f32_e32 v117, 1.0, v117
	v_rcp_f32_e32 v114, v114
	v_rcp_f32_e32 v115, v115
	v_rcp_f32_e32 v116, v116
	v_rcp_f32_e32 v117, v117
	v_pk_add_f32 v[112:113], v[112:113], v[44:45]
	v_pk_add_f32 v[110:111], v[110:111], v[42:43]
	v_mul_f32_e32 v112, 0xbfb8aa3b, v112
	v_mul_f32_e32 v110, 0xbfb8aa3b, v110
	v_mul_f32_e32 v111, 0xbfb8aa3b, v111
	v_mul_f32_e32 v113, 0xbfb8aa3b, v113
	v_pk_add_f32 v[108:109], v[108:109], v[36:37]
	v_pk_add_f32 v[106:107], v[106:107], v[34:35]
	v_exp_f32_e32 v110, v110
	v_exp_f32_e32 v111, v111
	v_exp_f32_e32 v112, v112
	v_exp_f32_e32 v113, v113
	v_mul_f32_e32 v106, 0xbfb8aa3b, v106
	v_mul_f32_e32 v107, 0xbfb8aa3b, v107
	v_mul_f32_e32 v108, 0xbfb8aa3b, v108
	v_mul_f32_e32 v109, 0xbfb8aa3b, v109
	v_exp_f32_e32 v106, v106
	v_exp_f32_e32 v107, v107
	v_exp_f32_e32 v108, v108
	v_exp_f32_e32 v109, v109
	v_add_f32_e32 v110, 1.0, v110
	v_add_f32_e32 v111, 1.0, v111
	v_add_f32_e32 v112, 1.0, v112
	v_add_f32_e32 v113, 1.0, v113
	v_rcp_f32_e32 v110, v110
	v_rcp_f32_e32 v111, v111
	v_rcp_f32_e32 v112, v112
	v_rcp_f32_e32 v113, v113
	v_add_f32_e32 v106, 1.0, v106
	v_add_f32_e32 v107, 1.0, v107
	v_add_f32_e32 v108, 1.0, v108
	v_add_f32_e32 v109, 1.0, v109
	v_rcp_f32_e32 v106, v106
	v_rcp_f32_e32 v107, v107
	v_rcp_f32_e32 v108, v108
	v_rcp_f32_e32 v109, v109
	v_pk_add_f32 v[104:105], v[104:105], v[24:25]
	v_pk_add_f32 v[102:103], v[102:103], v[22:23]
	v_mul_f32_e32 v104, 0xbfb8aa3b, v104
	v_mul_f32_e32 v102, 0xbfb8aa3b, v102
	v_mul_f32_e32 v103, 0xbfb8aa3b, v103
	v_mul_f32_e32 v105, 0xbfb8aa3b, v105
	v_pk_add_f32 v[100:101], v[100:101], v[20:21]
	v_pk_add_f32 v[98:99], v[98:99], v[18:19]
	v_exp_f32_e32 v102, v102
	v_exp_f32_e32 v103, v103
	v_exp_f32_e32 v104, v104
	v_exp_f32_e32 v105, v105
	v_mul_f32_e32 v98, 0xbfb8aa3b, v98
	v_mul_f32_e32 v99, 0xbfb8aa3b, v99
	v_mul_f32_e32 v100, 0xbfb8aa3b, v100
	v_lshlrev_b32_e32 v163, 16, v194
	v_and_b32_e32 v138, 0xffff0000, v194
	v_lshlrev_b32_e32 v166, 16, v195
	v_and_b32_e32 v167, 0xffff0000, v195
	v_lshlrev_b32_e32 v172, 16, v196
	v_and_b32_e32 v173, 0xffff0000, v196
	v_lshlrev_b32_e32 v174, 16, v197
	v_and_b32_e32 v175, 0xffff0000, v197
	v_sub_f32_e32 v139, v138, v143
	v_sub_f32_e32 v138, v163, v142
	v_sub_f32_e32 v141, v167, v145
	v_sub_f32_e32 v140, v166, v144
	v_pk_fma_f32 v[136:137], v[136:137], v[140:141], v[144:145]
	v_pk_fma_f32 v[134:135], v[134:135], v[138:139], v[142:143]
	v_sub_f32_e32 v139, v173, v169
	v_sub_f32_e32 v138, v172, v168
	v_sub_f32_e32 v141, v175, v171
	v_sub_f32_e32 v140, v174, v170
	v_pk_fma_f32 v[140:141], v[132:133], v[140:141], v[170:171]
	v_pk_fma_f32 v[132:133], v[130:131], v[138:139], v[168:169]
	v_cvt_pk_bf16_f32 v130, v134, v135
	v_cvt_pk_bf16_f32 v131, v136, v137
	v_mul_f32_e32 v101, 0xbfb8aa3b, v101
	v_cvt_pk_bf16_f32 v132, v132, v133
	v_cvt_pk_bf16_f32 v133, v140, v141
	global_store_dwordx4 v[164:165], v[130:133], off offset:256
	v_exp_f32_e32 v98, v98
	v_exp_f32_e32 v99, v99
	v_or_b32_e32 v130, 16, v162
	v_ashrrev_i32_e32 v131, 31, v130
	v_lshlrev_b64 v[132:133], 11, v[130:131]
	v_mad_i64_i32 v[130:131], s[60:61], v130, s27, v[160:161]
	v_lshl_add_u64 v[130:131], v[130:131], 0, v[158:159]
	v_add_co_u32_e32 v130, vcc, s9, v130
	v_lshl_add_u64 v[132:133], s[56:57], 0, v[132:133]
	s_nop 0
	v_addc_co_u32_e32 v131, vcc, 0, v131, vcc
	v_lshl_add_u64 v[132:133], v[132:133], 0, v[158:159]
	global_load_dwordx4 v[134:137], v[130:131], off
	global_load_dwordx4 v[142:145], v[132:133], off
	global_load_dwordx4 v[190:193], v[130:131], off offset:256
	global_load_dwordx4 v[194:197], v[132:133], off offset:256
	v_exp_f32_e32 v100, v100
	v_exp_f32_e32 v101, v101
	v_add_f32_e32 v102, 1.0, v102
	v_add_f32_e32 v103, 1.0, v103
	v_add_f32_e32 v104, 1.0, v104
	v_add_f32_e32 v105, 1.0, v105
	v_rcp_f32_e32 v102, v102
	v_rcp_f32_e32 v103, v103
	v_rcp_f32_e32 v104, v104
	v_rcp_f32_e32 v105, v105
	v_add_f32_e32 v98, 1.0, v98
	v_add_f32_e32 v99, 1.0, v99
	v_add_f32_e32 v100, 1.0, v100
	v_add_f32_e32 v101, 1.0, v101
	v_rcp_f32_e32 v98, v98
	v_rcp_f32_e32 v99, v99
	v_rcp_f32_e32 v100, v100
	v_rcp_f32_e32 v101, v101
	v_pk_add_f32 v[96:97], v[96:97], v[44:45]
	v_pk_add_f32 v[94:95], v[94:95], v[42:43]
; __device__ __forceinline__ void unpk8(const u32x4 w, f32x4& a, f32x4& b) { a = (f32x4){bflo(w.x), bfhi(w.x), bflo(w.y), bfhi(w.y)}; b = (f32x4){bflo(w.z), bfhi(w.z), bflo(w.w), bfhi(w.w)}; }
; __device__ __forceinline__ u32x4 pk8(const f32x4 a, const f32x4 b) { u32x4 w; w.x = cvt_pk_bf16(a[0], a[1]); w.y = cvt_pk_bf16(a[2], a[3]); w.z = cvt_pk_bf16(b[0], b[1]); w.w = cvt_pk_bf16(b[2], b[3]); return w; }
; __device__ __forceinline__ float fsig(float x) { return __builtin_amdgcn_rcpf(1.f + __builtin_amdgcn_exp2f(-1.44269504f * x)); }
;     __device__ __forceinline__ void operator()(const f32x4 (&acc)[2][2][4][2], const Unit& u, int wr, int wc, int fr, int fq) const {
;     ...
;         EPI_ROWS_BEGIN
; #pragma unroll
;             for (int bj = 0; bj < 2; ++bj) { bf16_t* zp = zrkv + row * 3072 + 2048 + col0 + bj * HALF;
;                 f32x4 z0, z1, f0, f1; unpk8(*(const u32x4*)zp, z0, z1); unpk8(*(const u32x4*)(vf + row * 1024 + col0 + bj * HALF), f0, f1);
;                 const f32x4 m0 = act4(acc[ai][bj][m][0] + bv[bj][0], 2), m1 = act4(acc[ai][bj][m][1] + bv[bj][1], 2);
;                 *(u32x4*)zp = pk8(z0 + (f0 - z0) * m0, z1 + (f1 - z1) * m1); }
	v_mul_f32_e32 v96, 0xbfb8aa3b, v96
	v_mul_f32_e32 v94, 0xbfb8aa3b, v94
	v_mul_f32_e32 v95, 0xbfb8aa3b, v95
	v_mul_f32_e32 v97, 0xbfb8aa3b, v97
	v_pk_add_f32 v[92:93], v[92:93], v[36:37]
	v_pk_add_f32 v[90:91], v[90:91], v[34:35]
	v_exp_f32_e32 v94, v94
	v_exp_f32_e32 v95, v95
	v_exp_f32_e32 v96, v96
	v_exp_f32_e32 v97, v97
	v_mul_f32_e32 v90, 0xbfb8aa3b, v90
	v_mul_f32_e32 v91, 0xbfb8aa3b, v91
	v_mul_f32_e32 v92, 0xbfb8aa3b, v92
	v_mul_f32_e32 v93, 0xbfb8aa3b, v93
	v_exp_f32_e32 v90, v90
	v_exp_f32_e32 v91, v91
	v_exp_f32_e32 v92, v92
	v_exp_f32_e32 v93, v93
	v_add_f32_e32 v94, 1.0, v94
	v_add_f32_e32 v95, 1.0, v95
	v_add_f32_e32 v96, 1.0, v96
	v_add_f32_e32 v97, 1.0, v97
	v_rcp_f32_e32 v94, v94
	v_rcp_f32_e32 v95, v95
	v_rcp_f32_e32 v96, v96
	v_rcp_f32_e32 v97, v97
	v_add_f32_e32 v90, 1.0, v90
	v_add_f32_e32 v91, 1.0, v91
	v_add_f32_e32 v92, 1.0, v92
	v_add_f32_e32 v93, 1.0, v93
	v_rcp_f32_e32 v90, v90
	v_rcp_f32_e32 v91, v91
	v_rcp_f32_e32 v92, v92
	v_rcp_f32_e32 v93, v93
	v_pk_add_f32 v[88:89], v[88:89], v[24:25]
	v_pk_add_f32 v[86:87], v[86:87], v[22:23]
	v_mul_f32_e32 v88, 0xbfb8aa3b, v88
	v_mul_f32_e32 v86, 0xbfb8aa3b, v86
	v_mul_f32_e32 v87, 0xbfb8aa3b, v87
	v_mul_f32_e32 v89, 0xbfb8aa3b, v89
	v_pk_add_f32 v[84:85], v[84:85], v[20:21]
	v_pk_add_f32 v[82:83], v[82:83], v[18:19]
	v_exp_f32_e32 v86, v86
	v_exp_f32_e32 v87, v87
	v_exp_f32_e32 v88, v88
	v_exp_f32_e32 v89, v89
	v_mul_f32_e32 v82, 0xbfb8aa3b, v82
	v_mul_f32_e32 v83, 0xbfb8aa3b, v83
	v_mul_f32_e32 v84, 0xbfb8aa3b, v84
	v_mul_f32_e32 v85, 0xbfb8aa3b, v85
	v_exp_f32_e32 v82, v82
	v_exp_f32_e32 v83, v83
	v_exp_f32_e32 v84, v84
	v_exp_f32_e32 v85, v85
	v_add_f32_e32 v86, 1.0, v86
	v_add_f32_e32 v87, 1.0, v87
	v_add_f32_e32 v88, 1.0, v88
	v_add_f32_e32 v89, 1.0, v89
	s_waitcnt vmcnt(0)
	v_lshlrev_b32_e32 v138, 16, v134
	v_and_b32_e32 v139, 0xffff0000, v134
	v_lshlrev_b32_e32 v140, 16, v135
	v_and_b32_e32 v141, 0xffff0000, v135
	v_lshlrev_b32_e32 v163, 16, v142
	v_and_b32_e32 v142, 0xffff0000, v142
	v_lshlrev_b32_e32 v164, 16, v143
	v_and_b32_e32 v165, 0xffff0000, v143
	v_lshlrev_b32_e32 v134, 16, v136
	v_and_b32_e32 v135, 0xffff0000, v136
	v_lshlrev_b32_e32 v136, 16, v137
	v_and_b32_e32 v137, 0xffff0000, v137
	v_lshlrev_b32_e32 v166, 16, v144
	v_and_b32_e32 v167, 0xffff0000, v144
	v_lshlrev_b32_e32 v168, 16, v145
	v_and_b32_e32 v169, 0xffff0000, v145
	v_sub_f32_e32 v143, v142, v139
	v_sub_f32_e32 v142, v163, v138
	v_sub_f32_e32 v145, v165, v141
	v_sub_f32_e32 v144, v164, v140
	v_pk_fma_f32 v[128:129], v[128:129], v[144:145], v[140:141]
	v_pk_fma_f32 v[126:127], v[126:127], v[142:143], v[138:139]
	v_sub_f32_e32 v139, v167, v135
	v_sub_f32_e32 v138, v166, v134
	v_sub_f32_e32 v141, v169, v137
	v_sub_f32_e32 v140, v168, v136
	v_pk_fma_f32 v[136:137], v[124:125], v[140:141], v[136:137]
	v_pk_fma_f32 v[124:125], v[122:123], v[138:139], v[134:135]
	v_cvt_pk_bf16_f32 v122, v126, v127
	v_cvt_pk_bf16_f32 v123, v128, v129
	v_rcp_f32_e32 v86, v86
	v_cvt_pk_bf16_f32 v124, v124, v125
	v_cvt_pk_bf16_f32 v125, v136, v137
	global_store_dwordx4 v[130:131], v[122:125], off
	v_rcp_f32_e32 v87, v87
	v_rcp_f32_e32 v88, v88
	v_rcp_f32_e32 v89, v89
	v_add_f32_e32 v82, 1.0, v82
	v_add_f32_e32 v83, 1.0, v83
	v_add_f32_e32 v84, 1.0, v84
	v_add_f32_e32 v85, 1.0, v85
	v_rcp_f32_e32 v82, v82
	v_rcp_f32_e32 v83, v83
	v_rcp_f32_e32 v84, v84
	v_rcp_f32_e32 v85, v85
	v_pk_add_f32 v[80:81], v[80:81], v[44:45]
	v_pk_add_f32 v[78:79], v[78:79], v[42:43]
	v_mul_f32_e32 v80, 0xbfb8aa3b, v80
	v_mul_f32_e32 v78, 0xbfb8aa3b, v78
	v_mul_f32_e32 v79, 0xbfb8aa3b, v79
	v_mul_f32_e32 v81, 0xbfb8aa3b, v81
	v_pk_add_f32 v[76:77], v[76:77], v[36:37]
	v_pk_add_f32 v[74:75], v[74:75], v[34:35]
	v_exp_f32_e32 v78, v78
	v_exp_f32_e32 v79, v79
	v_exp_f32_e32 v80, v80
	v_exp_f32_e32 v81, v81
	v_mul_f32_e32 v74, 0xbfb8aa3b, v74
	v_mul_f32_e32 v75, 0xbfb8aa3b, v75
	v_mul_f32_e32 v76, 0xbfb8aa3b, v76
	v_mul_f32_e32 v77, 0xbfb8aa3b, v77
	v_exp_f32_e32 v74, v74
	v_exp_f32_e32 v75, v75
	v_exp_f32_e32 v76, v76
	v_exp_f32_e32 v77, v77
	v_add_f32_e32 v78, 1.0, v78
	v_add_f32_e32 v79, 1.0, v79
	v_add_f32_e32 v80, 1.0, v80
	v_add_f32_e32 v81, 1.0, v81
	v_rcp_f32_e32 v78, v78
	v_rcp_f32_e32 v79, v79
	v_rcp_f32_e32 v80, v80
	v_rcp_f32_e32 v81, v81
	v_add_f32_e32 v74, 1.0, v74
	v_add_f32_e32 v75, 1.0, v75
	v_add_f32_e32 v76, 1.0, v76
	v_add_f32_e32 v77, 1.0, v77
	v_rcp_f32_e32 v74, v74
	v_rcp_f32_e32 v75, v75
	v_rcp_f32_e32 v76, v76
	v_rcp_f32_e32 v77, v77
	v_pk_add_f32 v[72:73], v[72:73], v[24:25]
	v_pk_add_f32 v[70:71], v[70:71], v[22:23]
	v_mul_f32_e32 v72, 0xbfb8aa3b, v72
	v_mul_f32_e32 v70, 0xbfb8aa3b, v70
	v_mul_f32_e32 v71, 0xbfb8aa3b, v71
	v_mul_f32_e32 v73, 0xbfb8aa3b, v73
	v_pk_add_f32 v[68:69], v[68:69], v[20:21]
	v_pk_add_f32 v[66:67], v[66:67], v[18:19]
	v_exp_f32_e32 v70, v70
	v_exp_f32_e32 v71, v71
	v_exp_f32_e32 v72, v72
	v_exp_f32_e32 v73, v73
	v_mul_f32_e32 v66, 0xbfb8aa3b, v66
	v_mul_f32_e32 v67, 0xbfb8aa3b, v67
	v_mul_f32_e32 v68, 0xbfb8aa3b, v68
	v_mul_f32_e32 v69, 0xbfb8aa3b, v69
	v_exp_f32_e32 v66, v66
	v_exp_f32_e32 v67, v67
	v_exp_f32_e32 v68, v68
	v_exp_f32_e32 v69, v69
	v_add_f32_e32 v70, 1.0, v70
	v_add_f32_e32 v71, 1.0, v71
	v_add_f32_e32 v72, 1.0, v72
	v_add_f32_e32 v73, 1.0, v73
	v_rcp_f32_e32 v70, v70
	v_rcp_f32_e32 v71, v71
	v_rcp_f32_e32 v72, v72
	v_rcp_f32_e32 v73, v73
	v_add_f32_e32 v66, 1.0, v66
	v_add_f32_e32 v67, 1.0, v67
	v_add_f32_e32 v68, 1.0, v68
	v_add_f32_e32 v69, 1.0, v69
	v_lshlrev_b32_e32 v126, 16, v190
	v_and_b32_e32 v127, 0xffff0000, v190
	v_lshlrev_b32_e32 v128, 16, v191
	v_and_b32_e32 v129, 0xffff0000, v191
	v_lshlrev_b32_e32 v134, 16, v192
	v_and_b32_e32 v135, 0xffff0000, v192
; __device__ __forceinline__ void unpk8(const u32x4 w, f32x4& a, f32x4& b) { a = (f32x4){bflo(w.x), bfhi(w.x), bflo(w.y), bfhi(w.y)}; b = (f32x4){bflo(w.z), bfhi(w.z), bflo(w.w), bfhi(w.w)}; }
; __device__ __forceinline__ u32x4 pk8(const f32x4 a, const f32x4 b) { u32x4 w; w.x = cvt_pk_bf16(a[0], a[1]); w.y = cvt_pk_bf16(a[2], a[3]); w.z = cvt_pk_bf16(b[0], b[1]); w.w = cvt_pk_bf16(b[2], b[3]); return w; }
; __device__ __forceinline__ float fsig(float x) { return __builtin_amdgcn_rcpf(1.f + __builtin_amdgcn_exp2f(-1.44269504f * x)); }
;     __device__ __forceinline__ void operator()(const f32x4 (&acc)[2][2][4][2], const Unit& u, int wr, int wc, int fr, int fq) const {
;     ...
;         EPI_ROWS_BEGIN
; #pragma unroll
;             for (int bj = 0; bj < 2; ++bj) { bf16_t* zp = zrkv + row * 3072 + 2048 + col0 + bj * HALF;
;                 f32x4 z0, z1, f0, f1; unpk8(*(const u32x4*)zp, z0, z1); unpk8(*(const u32x4*)(vf + row * 1024 + col0 + bj * HALF), f0, f1);
;                 const f32x4 m0 = act4(acc[ai][bj][m][0] + bv[bj][0], 2), m1 = act4(acc[ai][bj][m][1] + bv[bj][1], 2);
;                 *(u32x4*)zp = pk8(z0 + (f0 - z0) * m0, z1 + (f1 - z1) * m1); }
	v_lshlrev_b32_e32 v136, 16, v193
	v_and_b32_e32 v137, 0xffff0000, v193
	v_rcp_f32_e32 v66, v66
	v_rcp_f32_e32 v67, v67
	v_rcp_f32_e32 v68, v68
	v_rcp_f32_e32 v69, v69
	v_pk_add_f32 v[64:65], v[64:65], v[44:45]
	v_pk_add_f32 v[62:63], v[62:63], v[42:43]
	v_mul_f32_e32 v64, 0xbfb8aa3b, v64
	v_mul_f32_e32 v62, 0xbfb8aa3b, v62
	v_mul_f32_e32 v63, 0xbfb8aa3b, v63
	v_mul_f32_e32 v65, 0xbfb8aa3b, v65
	v_pk_add_f32 v[60:61], v[60:61], v[36:37]
	v_pk_add_f32 v[58:59], v[58:59], v[34:35]
	v_exp_f32_e32 v62, v62
	v_exp_f32_e32 v63, v63
	v_exp_f32_e32 v64, v64
	v_exp_f32_e32 v65, v65
	v_mul_f32_e32 v58, 0xbfb8aa3b, v58
	v_mul_f32_e32 v59, 0xbfb8aa3b, v59
	v_mul_f32_e32 v60, 0xbfb8aa3b, v60
	v_mul_f32_e32 v61, 0xbfb8aa3b, v61
	v_exp_f32_e32 v58, v58
	v_exp_f32_e32 v59, v59
	v_exp_f32_e32 v60, v60
	v_exp_f32_e32 v61, v61
	v_add_f32_e32 v62, 1.0, v62
	v_add_f32_e32 v63, 1.0, v63
	v_add_f32_e32 v64, 1.0, v64
	v_add_f32_e32 v65, 1.0, v65
	v_rcp_f32_e32 v62, v62
	v_rcp_f32_e32 v63, v63
	v_rcp_f32_e32 v64, v64
	v_rcp_f32_e32 v65, v65
	v_add_f32_e32 v58, 1.0, v58
	v_add_f32_e32 v59, 1.0, v59
	v_add_f32_e32 v60, 1.0, v60
	v_add_f32_e32 v61, 1.0, v61
	v_rcp_f32_e32 v58, v58
	v_rcp_f32_e32 v59, v59
	v_rcp_f32_e32 v60, v60
	v_rcp_f32_e32 v61, v61
	v_pk_add_f32 v[56:57], v[56:57], v[24:25]
	v_pk_add_f32 v[54:55], v[54:55], v[22:23]
	v_mul_f32_e32 v56, 0xbfb8aa3b, v56
	v_mul_f32_e32 v54, 0xbfb8aa3b, v54
	v_mul_f32_e32 v55, 0xbfb8aa3b, v55
	v_mul_f32_e32 v57, 0xbfb8aa3b, v57
	v_pk_add_f32 v[52:53], v[52:53], v[20:21]
	v_pk_add_f32 v[50:51], v[50:51], v[18:19]
	v_exp_f32_e32 v54, v54
	v_exp_f32_e32 v55, v55
	v_exp_f32_e32 v56, v56
	v_exp_f32_e32 v57, v57
	v_mul_f32_e32 v50, 0xbfb8aa3b, v50
	v_mul_f32_e32 v51, 0xbfb8aa3b, v51
	v_mul_f32_e32 v52, 0xbfb8aa3b, v52
	v_mul_f32_e32 v53, 0xbfb8aa3b, v53
	v_exp_f32_e32 v50, v50
	v_exp_f32_e32 v51, v51
	v_exp_f32_e32 v52, v52
	v_exp_f32_e32 v53, v53
	v_add_f32_e32 v54, 1.0, v54
	v_add_f32_e32 v55, 1.0, v55
	v_add_f32_e32 v56, 1.0, v56
	v_add_f32_e32 v57, 1.0, v57
	v_rcp_f32_e32 v54, v54
	v_rcp_f32_e32 v55, v55
	v_rcp_f32_e32 v56, v56
	v_rcp_f32_e32 v57, v57
	v_add_f32_e32 v50, 1.0, v50
	v_add_f32_e32 v51, 1.0, v51
	v_add_f32_e32 v52, 1.0, v52
	v_add_f32_e32 v53, 1.0, v53
	v_rcp_f32_e32 v50, v50
	v_rcp_f32_e32 v51, v51
	v_rcp_f32_e32 v52, v52
	v_rcp_f32_e32 v53, v53
	v_pk_add_f32 v[48:49], v[48:49], v[44:45]
	v_pk_add_f32 v[46:47], v[46:47], v[42:43]
	v_mul_f32_e32 v48, 0xbfb8aa3b, v48
	v_lshlrev_b32_e32 v132, 16, v194
	v_and_b32_e32 v122, 0xffff0000, v194
	v_lshlrev_b32_e32 v133, 16, v195
	v_and_b32_e32 v138, 0xffff0000, v195
	v_lshlrev_b32_e32 v139, 16, v196
	v_and_b32_e32 v140, 0xffff0000, v196
	v_lshlrev_b32_e32 v141, 16, v197
	v_and_b32_e32 v142, 0xffff0000, v197
	v_sub_f32_e32 v123, v122, v127
	v_sub_f32_e32 v122, v132, v126
	v_sub_f32_e32 v125, v138, v129
	v_sub_f32_e32 v124, v133, v128
	v_pk_fma_f32 v[120:121], v[120:121], v[124:125], v[128:129]
	v_pk_fma_f32 v[118:119], v[118:119], v[122:123], v[126:127]
	v_sub_f32_e32 v123, v140, v135
	v_sub_f32_e32 v122, v139, v134
	v_sub_f32_e32 v125, v142, v137
	v_sub_f32_e32 v124, v141, v136
	v_pk_fma_f32 v[124:125], v[116:117], v[124:125], v[136:137]
	v_pk_fma_f32 v[116:117], v[114:115], v[122:123], v[134:135]
	v_cvt_pk_bf16_f32 v114, v118, v119
	v_cvt_pk_bf16_f32 v115, v120, v121
	v_mul_f32_e32 v46, 0xbfb8aa3b, v46
	v_cvt_pk_bf16_f32 v116, v116, v117
	v_cvt_pk_bf16_f32 v117, v124, v125
	global_store_dwordx4 v[130:131], v[114:117], off offset:256
	v_mul_f32_e32 v47, 0xbfb8aa3b, v47
	v_mul_f32_e32 v49, 0xbfb8aa3b, v49
	v_or_b32_e32 v114, 32, v162
	v_ashrrev_i32_e32 v115, 31, v114
	v_lshlrev_b64 v[116:117], 11, v[114:115]
	v_mad_i64_i32 v[114:115], s[60:61], v114, s27, v[160:161]
	v_lshl_add_u64 v[114:115], v[114:115], 0, v[158:159]
	v_add_co_u32_e32 v114, vcc, s9, v114
	v_lshl_add_u64 v[116:117], s[56:57], 0, v[116:117]
	s_nop 0
	v_addc_co_u32_e32 v115, vcc, 0, v115, vcc
	v_lshl_add_u64 v[116:117], v[116:117], 0, v[158:159]
	global_load_dwordx4 v[118:121], v[114:115], off
	global_load_dwordx4 v[126:129], v[116:117], off
	global_load_dwordx4 v[190:193], v[114:115], off offset:256
	global_load_dwordx4 v[194:197], v[116:117], off offset:256
	v_pk_add_f32 v[40:41], v[40:41], v[36:37]
	v_pk_add_f32 v[38:39], v[38:39], v[34:35]
	v_exp_f32_e32 v46, v46
	v_exp_f32_e32 v47, v47
	v_exp_f32_e32 v48, v48
	v_exp_f32_e32 v49, v49
	v_mul_f32_e32 v38, 0xbfb8aa3b, v38
	v_mul_f32_e32 v39, 0xbfb8aa3b, v39
	v_mul_f32_e32 v40, 0xbfb8aa3b, v40
	v_mul_f32_e32 v41, 0xbfb8aa3b, v41
	v_exp_f32_e32 v38, v38
	v_exp_f32_e32 v39, v39
	v_exp_f32_e32 v40, v40
	v_exp_f32_e32 v41, v41
	v_add_f32_e32 v46, 1.0, v46
	v_add_f32_e32 v47, 1.0, v47
	v_add_f32_e32 v48, 1.0, v48
	v_add_f32_e32 v49, 1.0, v49
	v_rcp_f32_e32 v46, v46
	v_rcp_f32_e32 v47, v47
	v_rcp_f32_e32 v48, v48
	v_rcp_f32_e32 v49, v49
	v_add_f32_e32 v38, 1.0, v38
	v_add_f32_e32 v39, 1.0, v39
	v_add_f32_e32 v40, 1.0, v40
	v_add_f32_e32 v41, 1.0, v41
	v_rcp_f32_e32 v38, v38
	v_rcp_f32_e32 v39, v39
	v_rcp_f32_e32 v40, v40
	v_rcp_f32_e32 v41, v41
	v_pk_add_f32 v[32:33], v[32:33], v[24:25]
	v_pk_add_f32 v[30:31], v[30:31], v[22:23]
	v_mul_f32_e32 v32, 0xbfb8aa3b, v32
	v_mul_f32_e32 v30, 0xbfb8aa3b, v30
	v_mul_f32_e32 v31, 0xbfb8aa3b, v31
	v_mul_f32_e32 v33, 0xbfb8aa3b, v33
	v_pk_add_f32 v[28:29], v[28:29], v[20:21]
	v_pk_add_f32 v[26:27], v[26:27], v[18:19]
	v_exp_f32_e32 v30, v30
	v_exp_f32_e32 v31, v31
	v_exp_f32_e32 v32, v32
	v_exp_f32_e32 v33, v33
	v_mul_f32_e32 v26, 0xbfb8aa3b, v26
	v_mul_f32_e32 v27, 0xbfb8aa3b, v27
	v_mul_f32_e32 v28, 0xbfb8aa3b, v28
	v_mul_f32_e32 v29, 0xbfb8aa3b, v29
	v_exp_f32_e32 v26, v26
	v_exp_f32_e32 v27, v27
	v_exp_f32_e32 v28, v28
	v_exp_f32_e32 v29, v29
	v_add_f32_e32 v30, 1.0, v30
	v_add_f32_e32 v31, 1.0, v31
	v_add_f32_e32 v32, 1.0, v32
	v_add_f32_e32 v33, 1.0, v33
	v_rcp_f32_e32 v30, v30
	v_rcp_f32_e32 v31, v31
	v_rcp_f32_e32 v32, v32
	v_rcp_f32_e32 v33, v33
	v_add_f32_e32 v26, 1.0, v26
	v_add_f32_e32 v27, 1.0, v27
	v_add_f32_e32 v28, 1.0, v28
	v_add_f32_e32 v29, 1.0, v29
	v_rcp_f32_e32 v26, v26
	v_rcp_f32_e32 v27, v27
	v_rcp_f32_e32 v28, v28
	v_rcp_f32_e32 v29, v29
	v_pk_add_f32 v[16:17], v[16:17], v[44:45]
	v_pk_add_f32 v[14:15], v[14:15], v[42:43]
	v_mul_f32_e32 v16, 0xbfb8aa3b, v16
	v_mul_f32_e32 v14, 0xbfb8aa3b, v14
	v_mul_f32_e32 v15, 0xbfb8aa3b, v15
	v_mul_f32_e32 v17, 0xbfb8aa3b, v17
	v_pk_add_f32 v[12:13], v[12:13], v[36:37]
	v_pk_add_f32 v[10:11], v[10:11], v[34:35]
	v_exp_f32_e32 v14, v14
	v_exp_f32_e32 v15, v15
	v_exp_f32_e32 v16, v16
	v_exp_f32_e32 v17, v17
	s_waitcnt vmcnt(0)
; __device__ __forceinline__ void unpk8(const u32x4 w, f32x4& a, f32x4& b) { a = (f32x4){bflo(w.x), bfhi(w.x), bflo(w.y), bfhi(w.y)}; b = (f32x4){bflo(w.z), bfhi(w.z), bflo(w.w), bfhi(w.w)}; }
; __device__ __forceinline__ u32x4 pk8(const f32x4 a, const f32x4 b) { u32x4 w; w.x = cvt_pk_bf16(a[0], a[1]); w.y = cvt_pk_bf16(a[2], a[3]); w.z = cvt_pk_bf16(b[0], b[1]); w.w = cvt_pk_bf16(b[2], b[3]); return w; }
;     __device__ __forceinline__ void operator()(const f32x4 (&acc)[2][2][4][2], const Unit& u, int wr, int wc, int fr, int fq) const {
;     ...
;         EPI_ROWS_BEGIN
; #pragma unroll
;             for (int bj = 0; bj < 2; ++bj) { bf16_t* zp = zrkv + row * 3072 + 2048 + col0 + bj * HALF;
;                 f32x4 z0, z1, f0, f1; unpk8(*(const u32x4*)zp, z0, z1); unpk8(*(const u32x4*)(vf + row * 1024 + col0 + bj * HALF), f0, f1);
;                 const f32x4 m0 = act4(acc[ai][bj][m][0] + bv[bj][0], 2), m1 = act4(acc[ai][bj][m][1] + bv[bj][1], 2);
;                 *(u32x4*)zp = pk8(z0 + (f0 - z0) * m0, z1 + (f1 - z1) * m1); }
	v_lshlrev_b32_e32 v122, 16, v118
	v_and_b32_e32 v123, 0xffff0000, v118
	v_lshlrev_b32_e32 v124, 16, v119
	v_and_b32_e32 v125, 0xffff0000, v119
	v_lshlrev_b32_e32 v130, 16, v126
	v_and_b32_e32 v126, 0xffff0000, v126
	v_lshlrev_b32_e32 v131, 16, v127
	v_and_b32_e32 v132, 0xffff0000, v127
	v_lshlrev_b32_e32 v118, 16, v120
	v_and_b32_e32 v119, 0xffff0000, v120
	v_lshlrev_b32_e32 v120, 16, v121
	v_and_b32_e32 v121, 0xffff0000, v121
	v_lshlrev_b32_e32 v133, 16, v128
	v_and_b32_e32 v134, 0xffff0000, v128
	v_lshlrev_b32_e32 v135, 16, v129
	v_and_b32_e32 v136, 0xffff0000, v129
	v_sub_f32_e32 v127, v126, v123
	v_sub_f32_e32 v126, v130, v122
	v_sub_f32_e32 v129, v132, v125
	v_sub_f32_e32 v128, v131, v124
	v_pk_fma_f32 v[112:113], v[112:113], v[128:129], v[124:125]
	v_pk_fma_f32 v[110:111], v[110:111], v[126:127], v[122:123]
	v_sub_f32_e32 v123, v134, v119
	v_sub_f32_e32 v122, v133, v118
	v_sub_f32_e32 v125, v136, v121
	v_sub_f32_e32 v124, v135, v120
	v_pk_fma_f32 v[120:121], v[108:109], v[124:125], v[120:121]
	v_pk_fma_f32 v[108:109], v[106:107], v[122:123], v[118:119]
	v_cvt_pk_bf16_f32 v106, v110, v111
	v_cvt_pk_bf16_f32 v107, v112, v113
	v_mul_f32_e32 v10, 0xbfb8aa3b, v10
	v_cvt_pk_bf16_f32 v108, v108, v109
	v_cvt_pk_bf16_f32 v109, v120, v121
	global_store_dwordx4 v[114:115], v[106:109], off
	v_mul_f32_e32 v11, 0xbfb8aa3b, v11
	v_mul_f32_e32 v12, 0xbfb8aa3b, v12
	v_mul_f32_e32 v13, 0xbfb8aa3b, v13
	v_exp_f32_e32 v10, v10
	v_exp_f32_e32 v11, v11
	v_exp_f32_e32 v12, v12
	v_exp_f32_e32 v13, v13
	v_add_f32_e32 v14, 1.0, v14
	v_add_f32_e32 v15, 1.0, v15
	v_add_f32_e32 v16, 1.0, v16
	v_add_f32_e32 v17, 1.0, v17
	v_rcp_f32_e32 v14, v14
	v_rcp_f32_e32 v15, v15
	v_rcp_f32_e32 v16, v16
	v_rcp_f32_e32 v17, v17
	v_add_f32_e32 v10, 1.0, v10
	v_add_f32_e32 v11, 1.0, v11
	v_add_f32_e32 v12, 1.0, v12
	v_add_f32_e32 v13, 1.0, v13
	v_rcp_f32_e32 v10, v10
	v_rcp_f32_e32 v11, v11
	v_rcp_f32_e32 v12, v12
	v_rcp_f32_e32 v13, v13
	v_pk_add_f32 v[8:9], v[8:9], v[24:25]
	v_pk_add_f32 v[6:7], v[6:7], v[22:23]
	v_mul_f32_e32 v8, 0xbfb8aa3b, v8
	v_mul_f32_e32 v6, 0xbfb8aa3b, v6
	v_mul_f32_e32 v7, 0xbfb8aa3b, v7
	v_mul_f32_e32 v9, 0xbfb8aa3b, v9
	v_pk_add_f32 v[4:5], v[4:5], v[20:21]
	v_pk_add_f32 v[2:3], v[2:3], v[18:19]
	v_exp_f32_e32 v6, v6
	v_exp_f32_e32 v7, v7
	v_exp_f32_e32 v8, v8
	v_exp_f32_e32 v9, v9
	v_mul_f32_e32 v2, 0xbfb8aa3b, v2
	v_mul_f32_e32 v3, 0xbfb8aa3b, v3
	v_mul_f32_e32 v4, 0xbfb8aa3b, v4
	v_mul_f32_e32 v5, 0xbfb8aa3b, v5
	v_exp_f32_e32 v2, v2
	v_exp_f32_e32 v3, v3
	v_exp_f32_e32 v4, v4
	v_exp_f32_e32 v5, v5
	v_add_f32_e32 v6, 1.0, v6
	v_add_f32_e32 v7, 1.0, v7
	v_add_f32_e32 v8, 1.0, v8
	v_add_f32_e32 v9, 1.0, v9
	v_rcp_f32_e32 v6, v6
	v_rcp_f32_e32 v7, v7
	v_rcp_f32_e32 v8, v8
	v_rcp_f32_e32 v9, v9
	v_add_f32_e32 v2, 1.0, v2
	v_add_f32_e32 v3, 1.0, v3
	v_add_f32_e32 v4, 1.0, v4
	v_add_f32_e32 v5, 1.0, v5
	v_rcp_f32_e32 v2, v2
	v_rcp_f32_e32 v3, v3
	v_rcp_f32_e32 v4, v4
	v_rcp_f32_e32 v5, v5
	v_lshlrev_b32_e32 v110, 16, v190
	v_and_b32_e32 v111, 0xffff0000, v190
	v_lshlrev_b32_e32 v112, 16, v191
	v_and_b32_e32 v113, 0xffff0000, v191
	v_lshlrev_b32_e32 v118, 16, v192
	v_and_b32_e32 v119, 0xffff0000, v192
	v_lshlrev_b32_e32 v120, 16, v193
	v_and_b32_e32 v121, 0xffff0000, v193
	v_lshlrev_b32_e32 v116, 16, v194
	v_and_b32_e32 v106, 0xffff0000, v194
	v_lshlrev_b32_e32 v117, 16, v195
	v_and_b32_e32 v122, 0xffff0000, v195
	v_lshlrev_b32_e32 v123, 16, v196
	v_and_b32_e32 v124, 0xffff0000, v196
	v_lshlrev_b32_e32 v125, 16, v197
	v_and_b32_e32 v126, 0xffff0000, v197
	v_sub_f32_e32 v107, v106, v111
	v_sub_f32_e32 v106, v116, v110
	v_sub_f32_e32 v109, v122, v113
	v_sub_f32_e32 v108, v117, v112
	v_pk_fma_f32 v[104:105], v[104:105], v[108:109], v[112:113]
	v_pk_fma_f32 v[102:103], v[102:103], v[106:107], v[110:111]
	v_sub_f32_e32 v107, v124, v119
	v_sub_f32_e32 v106, v123, v118
	v_sub_f32_e32 v109, v126, v121
	v_sub_f32_e32 v108, v125, v120
	v_pk_fma_f32 v[108:109], v[100:101], v[108:109], v[120:121]
	v_pk_fma_f32 v[100:101], v[98:99], v[106:107], v[118:119]
	v_cvt_pk_bf16_f32 v98, v102, v103
	v_cvt_pk_bf16_f32 v99, v104, v105
	s_nop 0
	v_cvt_pk_bf16_f32 v100, v100, v101
	v_cvt_pk_bf16_f32 v101, v108, v109
	global_store_dwordx4 v[114:115], v[98:101], off offset:256
	s_nop 1
	v_or_b32_e32 v98, 48, v162
	v_ashrrev_i32_e32 v99, 31, v98
	v_lshlrev_b64 v[100:101], 11, v[98:99]
	v_mad_i64_i32 v[98:99], s[60:61], v98, s27, v[160:161]
	v_lshl_add_u64 v[98:99], v[98:99], 0, v[158:159]
	v_add_co_u32_e32 v98, vcc, s9, v98
	v_lshl_add_u64 v[100:101], s[56:57], 0, v[100:101]
	s_nop 0
	v_addc_co_u32_e32 v99, vcc, 0, v99, vcc
	v_lshl_add_u64 v[100:101], v[100:101], 0, v[158:159]
	global_load_dwordx4 v[102:105], v[98:99], off
	global_load_dwordx4 v[110:113], v[100:101], off
	global_load_dwordx4 v[190:193], v[98:99], off offset:256
	global_load_dwordx4 v[194:197], v[100:101], off offset:256
	s_waitcnt vmcnt(0)
; __device__ __forceinline__ void unpk8(const u32x4 w, f32x4& a, f32x4& b) { a = (f32x4){bflo(w.x), bfhi(w.x), bflo(w.y), bfhi(w.y)}; b = (f32x4){bflo(w.z), bfhi(w.z), bflo(w.w), bfhi(w.w)}; }
; __device__ __forceinline__ u32x4 pk8(const f32x4 a, const f32x4 b) { u32x4 w; w.x = cvt_pk_bf16(a[0], a[1]); w.y = cvt_pk_bf16(a[2], a[3]); w.z = cvt_pk_bf16(b[0], b[1]); w.w = cvt_pk_bf16(b[2], b[3]); return w; }
;     __device__ __forceinline__ void operator()(const f32x4 (&acc)[2][2][4][2], const Unit& u, int wr, int wc, int fr, int fq) const {
;     ...
;         EPI_ROWS_BEGIN
; #pragma unroll
;             for (int bj = 0; bj < 2; ++bj) { bf16_t* zp = zrkv + row * 3072 + 2048 + col0 + bj * HALF;
;                 f32x4 z0, z1, f0, f1; unpk8(*(const u32x4*)zp, z0, z1); unpk8(*(const u32x4*)(vf + row * 1024 + col0 + bj * HALF), f0, f1);
;                 const f32x4 m0 = act4(acc[ai][bj][m][0] + bv[bj][0], 2), m1 = act4(acc[ai][bj][m][1] + bv[bj][1], 2);
;                 *(u32x4*)zp = pk8(z0 + (f0 - z0) * m0, z1 + (f1 - z1) * m1); }
	v_lshlrev_b32_e32 v106, 16, v102
	v_and_b32_e32 v107, 0xffff0000, v102
	v_lshlrev_b32_e32 v108, 16, v103
	v_and_b32_e32 v109, 0xffff0000, v103
	v_lshlrev_b32_e32 v114, 16, v110
	v_and_b32_e32 v110, 0xffff0000, v110
	v_lshlrev_b32_e32 v115, 16, v111
	v_and_b32_e32 v116, 0xffff0000, v111
	v_lshlrev_b32_e32 v102, 16, v104
	v_and_b32_e32 v103, 0xffff0000, v104
	v_lshlrev_b32_e32 v104, 16, v105
	v_and_b32_e32 v105, 0xffff0000, v105
	v_lshlrev_b32_e32 v117, 16, v112
	v_and_b32_e32 v118, 0xffff0000, v112
	v_lshlrev_b32_e32 v119, 16, v113
	v_and_b32_e32 v120, 0xffff0000, v113
	v_sub_f32_e32 v111, v110, v107
	v_sub_f32_e32 v110, v114, v106
	v_sub_f32_e32 v113, v116, v109
	v_sub_f32_e32 v112, v115, v108
	v_pk_fma_f32 v[96:97], v[96:97], v[112:113], v[108:109]
	v_pk_fma_f32 v[94:95], v[94:95], v[110:111], v[106:107]
	v_sub_f32_e32 v107, v118, v103
	v_sub_f32_e32 v106, v117, v102
	v_sub_f32_e32 v109, v120, v105
	v_sub_f32_e32 v108, v119, v104
	v_pk_fma_f32 v[104:105], v[92:93], v[108:109], v[104:105]
	v_pk_fma_f32 v[92:93], v[90:91], v[106:107], v[102:103]
	v_cvt_pk_bf16_f32 v90, v94, v95
	v_cvt_pk_bf16_f32 v91, v96, v97
	s_nop 0
	v_cvt_pk_bf16_f32 v92, v92, v93
	v_cvt_pk_bf16_f32 v93, v104, v105
	global_store_dwordx4 v[98:99], v[90:93], off
	v_lshlrev_b32_e32 v94, 16, v190
	v_and_b32_e32 v95, 0xffff0000, v190
	v_lshlrev_b32_e32 v96, 16, v191
	v_and_b32_e32 v97, 0xffff0000, v191
	v_lshlrev_b32_e32 v102, 16, v192
	v_and_b32_e32 v103, 0xffff0000, v192
	v_lshlrev_b32_e32 v104, 16, v193
	v_and_b32_e32 v105, 0xffff0000, v193
	v_lshlrev_b32_e32 v100, 16, v194
	v_and_b32_e32 v90, 0xffff0000, v194
	v_lshlrev_b32_e32 v101, 16, v195
	v_and_b32_e32 v106, 0xffff0000, v195
	v_lshlrev_b32_e32 v107, 16, v196
	v_and_b32_e32 v108, 0xffff0000, v196
	v_lshlrev_b32_e32 v109, 16, v197
	v_and_b32_e32 v110, 0xffff0000, v197
	v_sub_f32_e32 v91, v90, v95
	v_sub_f32_e32 v90, v100, v94
	v_sub_f32_e32 v93, v106, v97
	v_sub_f32_e32 v92, v101, v96
	v_pk_fma_f32 v[88:89], v[88:89], v[92:93], v[96:97]
	v_pk_fma_f32 v[86:87], v[86:87], v[90:91], v[94:95]
	v_sub_f32_e32 v91, v108, v103
	v_sub_f32_e32 v90, v107, v102
	v_sub_f32_e32 v93, v110, v105
	v_sub_f32_e32 v92, v109, v104
	v_pk_fma_f32 v[92:93], v[84:85], v[92:93], v[104:105]
	v_pk_fma_f32 v[84:85], v[82:83], v[90:91], v[102:103]
	v_cvt_pk_bf16_f32 v82, v86, v87
	v_cvt_pk_bf16_f32 v83, v88, v89
	s_nop 0
	v_cvt_pk_bf16_f32 v84, v84, v85
	v_cvt_pk_bf16_f32 v85, v92, v93
	global_store_dwordx4 v[98:99], v[82:85], off offset:256
	s_nop 1
	v_add_u32_e32 v82, 0x80, v162
	v_ashrrev_i32_e32 v83, 31, v82
	v_lshlrev_b64 v[84:85], 11, v[82:83]
	v_mad_i64_i32 v[82:83], s[60:61], v82, s27, v[160:161]
	v_lshl_add_u64 v[82:83], v[82:83], 0, v[158:159]
	v_add_co_u32_e32 v82, vcc, s9, v82
	v_lshl_add_u64 v[84:85], s[56:57], 0, v[84:85]
	s_nop 0
	v_addc_co_u32_e32 v83, vcc, 0, v83, vcc
	v_lshl_add_u64 v[84:85], v[84:85], 0, v[158:159]
	global_load_dwordx4 v[86:89], v[82:83], off
	global_load_dwordx4 v[94:97], v[84:85], off
	global_load_dwordx4 v[190:193], v[82:83], off offset:256
	global_load_dwordx4 v[194:197], v[84:85], off offset:256
	s_waitcnt vmcnt(0)
	v_lshlrev_b32_e32 v90, 16, v86
	v_and_b32_e32 v91, 0xffff0000, v86
	v_lshlrev_b32_e32 v92, 16, v87
	v_and_b32_e32 v93, 0xffff0000, v87
	v_lshlrev_b32_e32 v98, 16, v94
	v_and_b32_e32 v94, 0xffff0000, v94
	v_lshlrev_b32_e32 v99, 16, v95
	v_and_b32_e32 v100, 0xffff0000, v95
	v_lshlrev_b32_e32 v86, 16, v88
	v_and_b32_e32 v87, 0xffff0000, v88
	v_lshlrev_b32_e32 v88, 16, v89
	v_and_b32_e32 v89, 0xffff0000, v89
	v_lshlrev_b32_e32 v101, 16, v96
	v_and_b32_e32 v102, 0xffff0000, v96
	v_lshlrev_b32_e32 v103, 16, v97
	v_and_b32_e32 v104, 0xffff0000, v97
	v_sub_f32_e32 v95, v94, v91
	v_sub_f32_e32 v94, v98, v90
	v_sub_f32_e32 v97, v100, v93
	v_sub_f32_e32 v96, v99, v92
	v_pk_fma_f32 v[80:81], v[80:81], v[96:97], v[92:93]
	v_pk_fma_f32 v[78:79], v[78:79], v[94:95], v[90:91]
	v_sub_f32_e32 v91, v102, v87
	v_sub_f32_e32 v90, v101, v86
	v_sub_f32_e32 v93, v104, v89
	v_sub_f32_e32 v92, v103, v88
	v_pk_fma_f32 v[88:89], v[76:77], v[92:93], v[88:89]
	v_pk_fma_f32 v[76:77], v[74:75], v[90:91], v[86:87]
	v_cvt_pk_bf16_f32 v74, v78, v79
	v_cvt_pk_bf16_f32 v75, v80, v81
	s_nop 0
	v_cvt_pk_bf16_f32 v76, v76, v77
	v_cvt_pk_bf16_f32 v77, v88, v89
	global_store_dwordx4 v[82:83], v[74:77], off
	v_lshlrev_b32_e32 v78, 16, v190
	v_and_b32_e32 v79, 0xffff0000, v190
	v_lshlrev_b32_e32 v80, 16, v191
	v_and_b32_e32 v81, 0xffff0000, v191
	v_lshlrev_b32_e32 v86, 16, v192
	v_and_b32_e32 v87, 0xffff0000, v192
	v_lshlrev_b32_e32 v88, 16, v193
	v_and_b32_e32 v89, 0xffff0000, v193
	v_lshlrev_b32_e32 v84, 16, v194
	v_and_b32_e32 v74, 0xffff0000, v194
	v_lshlrev_b32_e32 v85, 16, v195
	v_and_b32_e32 v90, 0xffff0000, v195
	v_lshlrev_b32_e32 v91, 16, v196
	v_and_b32_e32 v92, 0xffff0000, v196
	v_lshlrev_b32_e32 v93, 16, v197
	v_and_b32_e32 v94, 0xffff0000, v197
	v_sub_f32_e32 v75, v74, v79
	v_sub_f32_e32 v74, v84, v78
	v_sub_f32_e32 v77, v90, v81
	v_sub_f32_e32 v76, v85, v80
	v_pk_fma_f32 v[72:73], v[72:73], v[76:77], v[80:81]
	v_pk_fma_f32 v[70:71], v[70:71], v[74:75], v[78:79]
	v_sub_f32_e32 v75, v92, v87
	v_sub_f32_e32 v74, v91, v86
	v_sub_f32_e32 v77, v94, v89
	v_sub_f32_e32 v76, v93, v88
	v_pk_fma_f32 v[76:77], v[68:69], v[76:77], v[88:89]
	v_pk_fma_f32 v[68:69], v[66:67], v[74:75], v[86:87]
	v_cvt_pk_bf16_f32 v66, v70, v71
	v_cvt_pk_bf16_f32 v67, v72, v73
	s_nop 0
	v_cvt_pk_bf16_f32 v68, v68, v69
	v_cvt_pk_bf16_f32 v69, v76, v77
	global_store_dwordx4 v[82:83], v[66:69], off offset:256
	s_nop 1
	v_add_u32_e32 v66, 0x90, v162
	v_ashrrev_i32_e32 v67, 31, v66
	v_lshlrev_b64 v[68:69], 11, v[66:67]
	v_mad_i64_i32 v[66:67], s[60:61], v66, s27, v[160:161]
	v_lshl_add_u64 v[66:67], v[66:67], 0, v[158:159]
	v_add_co_u32_e32 v66, vcc, s9, v66
	v_lshl_add_u64 v[68:69], s[56:57], 0, v[68:69]
	s_nop 0
	v_addc_co_u32_e32 v67, vcc, 0, v67, vcc
	v_lshl_add_u64 v[68:69], v[68:69], 0, v[158:159]
	global_load_dwordx4 v[70:73], v[66:67], off
	global_load_dwordx4 v[78:81], v[68:69], off
	global_load_dwordx4 v[190:193], v[66:67], off offset:256
	global_load_dwordx4 v[194:197], v[68:69], off offset:256
	s_waitcnt vmcnt(0)
; __device__ __forceinline__ void unpk8(const u32x4 w, f32x4& a, f32x4& b) { a = (f32x4){bflo(w.x), bfhi(w.x), bflo(w.y), bfhi(w.y)}; b = (f32x4){bflo(w.z), bfhi(w.z), bflo(w.w), bfhi(w.w)}; }
; __device__ __forceinline__ u32x4 pk8(const f32x4 a, const f32x4 b) { u32x4 w; w.x = cvt_pk_bf16(a[0], a[1]); w.y = cvt_pk_bf16(a[2], a[3]); w.z = cvt_pk_bf16(b[0], b[1]); w.w = cvt_pk_bf16(b[2], b[3]); return w; }
;     __device__ __forceinline__ void operator()(const f32x4 (&acc)[2][2][4][2], const Unit& u, int wr, int wc, int fr, int fq) const {
;     ...
;         EPI_ROWS_BEGIN
; #pragma unroll
;             for (int bj = 0; bj < 2; ++bj) { bf16_t* zp = zrkv + row * 3072 + 2048 + col0 + bj * HALF;
;                 f32x4 z0, z1, f0, f1; unpk8(*(const u32x4*)zp, z0, z1); unpk8(*(const u32x4*)(vf + row * 1024 + col0 + bj * HALF), f0, f1);
;                 const f32x4 m0 = act4(acc[ai][bj][m][0] + bv[bj][0], 2), m1 = act4(acc[ai][bj][m][1] + bv[bj][1], 2);
;                 *(u32x4*)zp = pk8(z0 + (f0 - z0) * m0, z1 + (f1 - z1) * m1); }
;         EPI_ROWS_END
	v_lshlrev_b32_e32 v74, 16, v70
	v_and_b32_e32 v75, 0xffff0000, v70
	v_lshlrev_b32_e32 v76, 16, v71
	v_and_b32_e32 v77, 0xffff0000, v71
	v_lshlrev_b32_e32 v82, 16, v78
	v_and_b32_e32 v78, 0xffff0000, v78
	v_lshlrev_b32_e32 v83, 16, v79
	v_and_b32_e32 v84, 0xffff0000, v79
	v_lshlrev_b32_e32 v70, 16, v72
	v_and_b32_e32 v71, 0xffff0000, v72
	v_lshlrev_b32_e32 v72, 16, v73
	v_and_b32_e32 v73, 0xffff0000, v73
	v_lshlrev_b32_e32 v85, 16, v80
	v_and_b32_e32 v86, 0xffff0000, v80
	v_lshlrev_b32_e32 v87, 16, v81
	v_and_b32_e32 v88, 0xffff0000, v81
	v_sub_f32_e32 v79, v78, v75
	v_sub_f32_e32 v78, v82, v74
	v_sub_f32_e32 v81, v84, v77
	v_sub_f32_e32 v80, v83, v76
	v_pk_fma_f32 v[64:65], v[64:65], v[80:81], v[76:77]
	v_pk_fma_f32 v[62:63], v[62:63], v[78:79], v[74:75]
	v_sub_f32_e32 v75, v86, v71
	v_sub_f32_e32 v74, v85, v70
	v_sub_f32_e32 v77, v88, v73
	v_sub_f32_e32 v76, v87, v72
	v_pk_fma_f32 v[72:73], v[60:61], v[76:77], v[72:73]
	v_pk_fma_f32 v[60:61], v[58:59], v[74:75], v[70:71]
	v_cvt_pk_bf16_f32 v58, v62, v63
	v_cvt_pk_bf16_f32 v59, v64, v65
	s_nop 0
	v_cvt_pk_bf16_f32 v60, v60, v61
	v_cvt_pk_bf16_f32 v61, v72, v73
	global_store_dwordx4 v[66:67], v[58:61], off
	v_lshlrev_b32_e32 v62, 16, v190
	v_and_b32_e32 v63, 0xffff0000, v190
	v_lshlrev_b32_e32 v64, 16, v191
	v_and_b32_e32 v65, 0xffff0000, v191
	v_lshlrev_b32_e32 v70, 16, v192
	v_and_b32_e32 v71, 0xffff0000, v192
	v_lshlrev_b32_e32 v72, 16, v193
	v_and_b32_e32 v73, 0xffff0000, v193
	v_lshlrev_b32_e32 v68, 16, v194
	v_and_b32_e32 v58, 0xffff0000, v194
	v_lshlrev_b32_e32 v69, 16, v195
	v_and_b32_e32 v74, 0xffff0000, v195
	v_lshlrev_b32_e32 v75, 16, v196
	v_and_b32_e32 v76, 0xffff0000, v196
	v_lshlrev_b32_e32 v77, 16, v197
	v_and_b32_e32 v78, 0xffff0000, v197
	v_sub_f32_e32 v59, v58, v63
	v_sub_f32_e32 v58, v68, v62
	v_sub_f32_e32 v61, v74, v65
	v_sub_f32_e32 v60, v69, v64
	v_pk_fma_f32 v[56:57], v[56:57], v[60:61], v[64:65]
	v_pk_fma_f32 v[54:55], v[54:55], v[58:59], v[62:63]
	v_sub_f32_e32 v59, v76, v71
	v_sub_f32_e32 v58, v75, v70
	v_sub_f32_e32 v61, v78, v73
	v_sub_f32_e32 v60, v77, v72
	v_pk_fma_f32 v[60:61], v[52:53], v[60:61], v[72:73]
	v_pk_fma_f32 v[52:53], v[50:51], v[58:59], v[70:71]
	v_cvt_pk_bf16_f32 v50, v54, v55
	v_cvt_pk_bf16_f32 v51, v56, v57
	s_nop 0
	v_cvt_pk_bf16_f32 v52, v52, v53
	v_cvt_pk_bf16_f32 v53, v60, v61
	global_store_dwordx4 v[66:67], v[50:53], off offset:256
	s_nop 1
	v_add_u32_e32 v50, 0xa0, v162
	v_ashrrev_i32_e32 v51, 31, v50
	v_lshlrev_b64 v[52:53], 11, v[50:51]
	v_mad_i64_i32 v[50:51], s[60:61], v50, s27, v[160:161]
	v_lshl_add_u64 v[50:51], v[50:51], 0, v[158:159]
	v_add_co_u32_e32 v50, vcc, s9, v50
	v_lshl_add_u64 v[52:53], s[56:57], 0, v[52:53]
	s_nop 0
	v_addc_co_u32_e32 v51, vcc, 0, v51, vcc
	v_lshl_add_u64 v[52:53], v[52:53], 0, v[158:159]
	global_load_dwordx4 v[54:57], v[50:51], off
	global_load_dwordx4 v[62:65], v[52:53], off
	global_load_dwordx4 v[190:193], v[50:51], off offset:256
	global_load_dwordx4 v[194:197], v[52:53], off offset:256
	s_waitcnt vmcnt(0)
; __device__ __forceinline__ void unpk8(const u32x4 w, f32x4& a, f32x4& b) { a = (f32x4){bflo(w.x), bfhi(w.x), bflo(w.y), bfhi(w.y)}; b = (f32x4){bflo(w.z), bfhi(w.z), bflo(w.w), bfhi(w.w)}; }
; __device__ __forceinline__ u32x4 pk8(const f32x4 a, const f32x4 b) { u32x4 w; w.x = cvt_pk_bf16(a[0], a[1]); w.y = cvt_pk_bf16(a[2], a[3]); w.z = cvt_pk_bf16(b[0], b[1]); w.w = cvt_pk_bf16(b[2], b[3]); return w; }
; #define PG8_BAR __builtin_amdgcn_s_barrier()
;     __device__ __forceinline__ void operator()(const f32x4 (&acc)[2][2][4][2], const Unit& u, int wr, int wc, int fr, int fq) const {
;     ...
;         EPI_ROWS_BEGIN
; #pragma unroll
;             for (int bj = 0; bj < 2; ++bj) { bf16_t* zp = zrkv + row * 3072 + 2048 + col0 + bj * HALF;
;                 f32x4 z0, z1, f0, f1; unpk8(*(const u32x4*)zp, z0, z1); unpk8(*(const u32x4*)(vf + row * 1024 + col0 + bj * HALF), f0, f1);
;                 const f32x4 m0 = act4(acc[ai][bj][m][0] + bv[bj][0], 2), m1 = act4(acc[ai][bj][m][1] + bv[bj][1], 2);
;                 *(u32x4*)zp = pk8(z0 + (f0 - z0) * m0, z1 + (f1 - z1) * m1); }
;         EPI_ROWS_END
; template <class Epi, class Sched, bool ALIGN_EPI = false, bool SP2 = false>
; __device__ __forceinline__ void gemm_phase(PG8_LAS unsigned char* lds, const Gemm g, const Sched& S, const Epi& E, const int wave0) {
;     ...
;         if constexpr (ALIGN_EPI) { if (wr == 0) PG8_BAR; }
;         if constexpr (!Epi::AFTER_DRAIN) { E(acc, cur, wr, wc, fr, fq); S.done(cur); }
;         if (!has_next) break;
; #pragma unroll
;         for (int a = 0; a < 2; ++a)
; #pragma unroll
;             for (int b = 0; b < 2; ++b)
; #pragma unroll
;                 for (int m = 0; m < 4; ++m)
; #pragma unroll
;                     for (int n = 0; n < 2; ++n) acc[a][b][m][n] = (f32x4){0.f, 0.f, 0.f, 0.f};
;         cur = nxt; cA = nA; cB = nB; ++ui;
;         if constexpr (ALIGN_EPI) { if (wr == 1) PG8_BAR; }
	v_lshlrev_b32_e32 v58, 16, v54
	v_and_b32_e32 v59, 0xffff0000, v54
	v_lshlrev_b32_e32 v60, 16, v55
	v_and_b32_e32 v61, 0xffff0000, v55
	v_lshlrev_b32_e32 v66, 16, v62
	v_and_b32_e32 v62, 0xffff0000, v62
	v_lshlrev_b32_e32 v67, 16, v63
	v_and_b32_e32 v68, 0xffff0000, v63
	v_lshlrev_b32_e32 v54, 16, v56
	v_and_b32_e32 v55, 0xffff0000, v56
	v_lshlrev_b32_e32 v56, 16, v57
	v_and_b32_e32 v57, 0xffff0000, v57
	v_lshlrev_b32_e32 v69, 16, v64
	v_and_b32_e32 v70, 0xffff0000, v64
	v_lshlrev_b32_e32 v71, 16, v65
	v_and_b32_e32 v72, 0xffff0000, v65
	v_sub_f32_e32 v63, v62, v59
	v_sub_f32_e32 v62, v66, v58
	v_sub_f32_e32 v65, v68, v61
	v_sub_f32_e32 v64, v67, v60
	v_pk_fma_f32 v[48:49], v[48:49], v[64:65], v[60:61]
	v_pk_fma_f32 v[46:47], v[46:47], v[62:63], v[58:59]
	v_sub_f32_e32 v59, v70, v55
	v_sub_f32_e32 v58, v69, v54
	v_sub_f32_e32 v61, v72, v57
	v_sub_f32_e32 v60, v71, v56
	v_pk_fma_f32 v[56:57], v[40:41], v[60:61], v[56:57]
	v_pk_fma_f32 v[40:41], v[38:39], v[58:59], v[54:55]
	v_cvt_pk_bf16_f32 v38, v46, v47
	v_cvt_pk_bf16_f32 v39, v48, v49
	s_nop 0
	v_cvt_pk_bf16_f32 v40, v40, v41
	v_cvt_pk_bf16_f32 v41, v56, v57
	global_store_dwordx4 v[50:51], v[38:41], off
	v_lshlrev_b32_e32 v46, 16, v190
	v_and_b32_e32 v47, 0xffff0000, v190
	v_lshlrev_b32_e32 v48, 16, v191
	v_and_b32_e32 v49, 0xffff0000, v191
	v_lshlrev_b32_e32 v54, 16, v192
	v_and_b32_e32 v55, 0xffff0000, v192
	v_lshlrev_b32_e32 v56, 16, v193
	v_and_b32_e32 v57, 0xffff0000, v193
	v_lshlrev_b32_e32 v52, 16, v194
	v_and_b32_e32 v38, 0xffff0000, v194
	v_lshlrev_b32_e32 v53, 16, v195
	v_and_b32_e32 v58, 0xffff0000, v195
	v_lshlrev_b32_e32 v59, 16, v196
	v_and_b32_e32 v60, 0xffff0000, v196
	v_lshlrev_b32_e32 v61, 16, v197
	v_and_b32_e32 v62, 0xffff0000, v197
	v_sub_f32_e32 v39, v38, v47
	v_sub_f32_e32 v38, v52, v46
	v_sub_f32_e32 v41, v58, v49
	v_sub_f32_e32 v40, v53, v48
	v_pk_fma_f32 v[32:33], v[32:33], v[40:41], v[48:49]
	v_pk_fma_f32 v[30:31], v[30:31], v[38:39], v[46:47]
	v_sub_f32_e32 v39, v60, v55
	v_sub_f32_e32 v38, v59, v54
	v_sub_f32_e32 v41, v62, v57
	v_sub_f32_e32 v40, v61, v56
	v_pk_fma_f32 v[40:41], v[28:29], v[40:41], v[56:57]
	v_pk_fma_f32 v[28:29], v[26:27], v[38:39], v[54:55]
	v_cvt_pk_bf16_f32 v26, v30, v31
	v_cvt_pk_bf16_f32 v27, v32, v33
	s_nop 0
	v_cvt_pk_bf16_f32 v28, v28, v29
	v_cvt_pk_bf16_f32 v29, v40, v41
	global_store_dwordx4 v[50:51], v[26:29], off offset:256
	s_nop 1
	v_add_u32_e32 v26, 0xb0, v162
	v_ashrrev_i32_e32 v27, 31, v26
	v_lshlrev_b64 v[28:29], 11, v[26:27]
	v_mad_i64_i32 v[26:27], s[60:61], v26, s27, v[160:161]
	v_lshl_add_u64 v[26:27], v[26:27], 0, v[158:159]
	v_add_co_u32_e32 v26, vcc, s9, v26
	v_lshl_add_u64 v[28:29], s[56:57], 0, v[28:29]
	s_nop 0
	v_addc_co_u32_e32 v27, vcc, 0, v27, vcc
	v_lshl_add_u64 v[28:29], v[28:29], 0, v[158:159]
	global_load_dwordx4 v[30:33], v[26:27], off
	global_load_dwordx4 v[46:49], v[28:29], off
	global_load_dwordx4 v[190:193], v[26:27], off offset:256
	global_load_dwordx4 v[194:197], v[28:29], off offset:256
	s_mov_b64 s[60:61], -1
	s_and_b64 vcc, exec, s[36:37]
	s_waitcnt vmcnt(0)
	v_lshlrev_b32_e32 v38, 16, v30
	v_and_b32_e32 v39, 0xffff0000, v30
	v_lshlrev_b32_e32 v40, 16, v31
	v_and_b32_e32 v41, 0xffff0000, v31
	v_lshlrev_b32_e32 v50, 16, v46
	v_and_b32_e32 v46, 0xffff0000, v46
	v_lshlrev_b32_e32 v51, 16, v47
	v_and_b32_e32 v47, 0xffff0000, v47
	v_lshlrev_b32_e32 v30, 16, v32
	v_and_b32_e32 v31, 0xffff0000, v32
	v_lshlrev_b32_e32 v32, 16, v33
	v_and_b32_e32 v33, 0xffff0000, v33
	v_lshlrev_b32_e32 v52, 16, v48
	v_and_b32_e32 v48, 0xffff0000, v48
	v_lshlrev_b32_e32 v53, 16, v49
	v_and_b32_e32 v49, 0xffff0000, v49
	v_sub_f32_e32 v35, v46, v39
	v_sub_f32_e32 v34, v50, v38
	v_sub_f32_e32 v37, v47, v41
	v_sub_f32_e32 v36, v51, v40
	v_pk_fma_f32 v[16:17], v[16:17], v[36:37], v[40:41]
	v_pk_fma_f32 v[14:15], v[14:15], v[34:35], v[38:39]
	v_sub_f32_e32 v35, v48, v31
	v_sub_f32_e32 v34, v52, v30
	v_sub_f32_e32 v37, v49, v33
	v_sub_f32_e32 v36, v53, v32
	v_pk_fma_f32 v[32:33], v[12:13], v[36:37], v[32:33]
	v_pk_fma_f32 v[12:13], v[10:11], v[34:35], v[30:31]
	v_cvt_pk_bf16_f32 v10, v14, v15
	v_cvt_pk_bf16_f32 v11, v16, v17
	s_nop 0
	v_cvt_pk_bf16_f32 v12, v12, v13
	v_cvt_pk_bf16_f32 v13, v32, v33
	global_store_dwordx4 v[26:27], v[10:13], off
	v_lshlrev_b32_e32 v14, 16, v190
	v_and_b32_e32 v15, 0xffff0000, v190
	v_lshlrev_b32_e32 v16, 16, v191
	v_and_b32_e32 v17, 0xffff0000, v191
	v_lshlrev_b32_e32 v30, 16, v192
	v_and_b32_e32 v31, 0xffff0000, v192
	v_lshlrev_b32_e32 v32, 16, v193
	v_and_b32_e32 v33, 0xffff0000, v193
	v_lshlrev_b32_e32 v28, 16, v194
	v_and_b32_e32 v10, 0xffff0000, v194
	v_lshlrev_b32_e32 v29, 16, v195
	v_and_b32_e32 v34, 0xffff0000, v195
	v_lshlrev_b32_e32 v35, 16, v196
	v_and_b32_e32 v36, 0xffff0000, v196
	v_lshlrev_b32_e32 v37, 16, v197
	v_and_b32_e32 v38, 0xffff0000, v197
	v_sub_f32_e32 v11, v10, v15
	v_sub_f32_e32 v10, v28, v14
	v_sub_f32_e32 v13, v34, v17
	v_sub_f32_e32 v12, v29, v16
	v_pk_fma_f32 v[8:9], v[8:9], v[12:13], v[16:17]
	v_pk_fma_f32 v[6:7], v[6:7], v[10:11], v[14:15]
	v_sub_f32_e32 v11, v36, v31
	v_sub_f32_e32 v10, v35, v30
	v_sub_f32_e32 v13, v38, v33
	v_sub_f32_e32 v12, v37, v32
	v_pk_fma_f32 v[12:13], v[4:5], v[12:13], v[32:33]
	v_pk_fma_f32 v[4:5], v[2:3], v[10:11], v[30:31]
	v_cvt_pk_bf16_f32 v2, v6, v7
	v_cvt_pk_bf16_f32 v3, v8, v9
	s_nop 0
	v_cvt_pk_bf16_f32 v4, v4, v5
	v_cvt_pk_bf16_f32 v5, v12, v13
	global_store_dwordx4 v[26:27], v[2:5], off offset:256
	s_cbranch_vccnz .LBB0_750
	s_andn2_b64 vcc, exec, s[44:45]
	s_cbranch_vccnz .LBB0_749
	s_barrier
	s_branch .LBB0_749

; __device__ __forceinline__ void unpk8(const u32x4 w, f32x4& a, f32x4& b) { a = (f32x4){bflo(w.x), bfhi(w.x), bflo(w.y), bfhi(w.y)}; b = (f32x4){bflo(w.z), bfhi(w.z), bflo(w.w), bfhi(w.w)}; }
; __device__ __forceinline__ u32x4 pk8(const f32x4 a, const f32x4 b) { u32x4 w; w.x = cvt_pk_bf16(a[0], a[1]); w.y = cvt_pk_bf16(a[2], a[3]); w.z = cvt_pk_bf16(b[0], b[1]); w.w = cvt_pk_bf16(b[2], b[3]); return w; }
;     __device__ __forceinline__ void operator()(const f32x4 (&acc)[2][2][4][2], const Unit& u, int wr, int wc, int fr, int fq) const {
;         const int row0 = u.pm * BM + wr * 64 + fr, col0 = u.pn * 256 + wc * 32 + 8 * fq;
; #pragma unroll
;         for (int ai = 0; ai < 2; ++ai) { u32x4 gv[4][2], pv[4][2];
; #pragma unroll
;             for (int m = 0; m < 4; ++m) { const size_t row = (size_t)(row0 + ai * HALF + m * 16);
; #pragma unroll
;                 for (int bj = 0; bj < 2; ++bj) { const int c = col0 + bj * HALF; gv[m][bj] = *(const u32x4*)(sg + row * 2048 + (SECOND ? 0 : 1024) + c);
;                     if (SECOND) pv[m][bj] = *(const u32x4*)(m2 + row * 2048 + c); } }
; #pragma unroll
;             for (int m = 0; m < 4; ++m) { const size_t row = (size_t)(row0 + ai * HALF + m * 16);
; #pragma unroll
;                 for (int bj = 0; bj < 2; ++bj) { const int c = col0 + bj * HALF;
;                     f32x4 g0, g1; unpk8(gv[m][bj], g0, g1);
;                     f32x4 v0 = g0 * acc[ai][bj][m][0], v1 = g1 * acc[ai][bj][m][1];
;                     if (SECOND) { f32x4 p0, p1; unpk8(pv[m][bj], p0, p1); v0 = v0 + p0; v1 = v1 + p1; *(u32x4*)(o + row * 1024 + c) = pk8(v0, v1); }
;                     else *(u32x4*)(m2 + row * 2048 + c) = pk8(v0, v1); } } }
.LBB0_857:
	v_lshl_add_u32 v130, s91, 8, v1
	v_ashrrev_i32_e32 v131, 31, v130
	v_lshlrev_b64 v[164:165], 12, v[130:131]
	v_lshl_add_u64 v[132:133], s[2:3], 0, v[164:165]
	v_lshl_or_b32 v162, s90, 9, v174
	v_mov_b32_e32 v163, v0
	v_lshl_add_u64 v[132:133], v[132:133], 0, v[162:163]
	global_load_dwordx4 v[176:179], v[132:133], off offset:2048
	global_load_dwordx4 v[180:183], v[132:133], off offset:2304
	v_or_b32_e32 v132, 16, v130
	v_ashrrev_i32_e32 v133, 31, v132
	v_lshlrev_b64 v[170:171], 12, v[132:133]
	v_lshl_add_u64 v[132:133], s[2:3], 0, v[170:171]
	v_lshl_add_u64 v[132:133], v[132:133], 0, v[162:163]
	global_load_dwordx4 v[184:187], v[132:133], off offset:2048
	global_load_dwordx4 v[146:149], v[132:133], off offset:2304
	v_or_b32_e32 v132, 32, v130
	v_ashrrev_i32_e32 v133, 31, v132
	v_lshlrev_b64 v[168:169], 12, v[132:133]
	v_lshl_add_u64 v[132:133], s[2:3], 0, v[168:169]
	v_lshl_add_u64 v[132:133], v[132:133], 0, v[162:163]
	global_load_dwordx4 v[142:145], v[132:133], off offset:2048
	global_load_dwordx4 v[134:137], v[132:133], off offset:2304
	v_or_b32_e32 v130, 48, v130
	v_ashrrev_i32_e32 v131, 31, v130
	v_lshlrev_b64 v[166:167], 12, v[130:131]
	v_lshl_add_u64 v[130:131], s[2:3], 0, v[166:167]
	v_lshl_add_u64 v[130:131], v[130:131], 0, v[162:163]
	global_load_dwordx4 v[138:141], v[130:131], off offset:2048
	global_load_dwordx4 v[130:133], v[130:131], off offset:2304
	s_mov_b64 s[46:47], 0x80000
	s_mov_b64 s[72:73], -1
	s_and_b64 vcc, exec, s[40:41]
	s_waitcnt vmcnt(0)
	v_lshlrev_b32_e32 v188, 16, v176
	v_and_b32_e32 v189, 0xffff0000, v176
	v_lshlrev_b32_e32 v176, 16, v177
	v_and_b32_e32 v177, 0xffff0000, v177
	v_lshlrev_b32_e32 v190, 16, v178
	v_and_b32_e32 v191, 0xffff0000, v178
	v_pk_mul_f32 v[124:125], v[124:125], v[176:177]
	v_pk_mul_f32 v[122:123], v[122:123], v[188:189]
	v_pk_mul_f32 v[126:127], v[126:127], v[190:191]
	v_lshlrev_b32_e32 v178, 16, v179
	v_and_b32_e32 v179, 0xffff0000, v179
	v_cvt_pk_bf16_f32 v122, v122, v123
	v_cvt_pk_bf16_f32 v123, v124, v125
	v_cvt_pk_bf16_f32 v124, v126, v127
	v_lshl_add_u64 v[126:127], s[54:55], 0, v[164:165]
	v_pk_mul_f32 v[128:129], v[128:129], v[178:179]
	v_lshl_add_u64 v[126:127], v[126:127], 0, v[162:163]
	v_cvt_pk_bf16_f32 v125, v128, v129
	global_store_dwordx4 v[126:127], v[122:125], off
	v_lshlrev_b32_e32 v128, 16, v182
	v_and_b32_e32 v129, 0xffff0000, v182
	v_lshlrev_b32_e32 v122, 16, v180
	v_and_b32_e32 v123, 0xffff0000, v180
	v_lshlrev_b32_e32 v124, 16, v181
	v_and_b32_e32 v125, 0xffff0000, v181
	v_lshlrev_b32_e32 v176, 16, v183
	v_and_b32_e32 v177, 0xffff0000, v183
	v_pk_mul_f32 v[120:121], v[120:121], v[124:125]
	v_pk_mul_f32 v[118:119], v[118:119], v[122:123]
	v_pk_mul_f32 v[122:123], v[116:117], v[176:177]
	v_pk_mul_f32 v[116:117], v[114:115], v[128:129]
	v_cvt_pk_bf16_f32 v114, v118, v119
	v_cvt_pk_bf16_f32 v115, v120, v121
	v_lshlrev_b32_e32 v118, 16, v186
	v_cvt_pk_bf16_f32 v116, v116, v117
	v_cvt_pk_bf16_f32 v117, v122, v123
	global_store_dwordx4 v[126:127], v[114:117], off offset:256
	v_and_b32_e32 v119, 0xffff0000, v186
	v_lshlrev_b32_e32 v120, 16, v187
	v_lshlrev_b32_e32 v114, 16, v184
	v_and_b32_e32 v115, 0xffff0000, v184
	v_lshlrev_b32_e32 v116, 16, v185
	v_and_b32_e32 v117, 0xffff0000, v185
	v_and_b32_e32 v121, 0xffff0000, v187
	v_pk_mul_f32 v[110:111], v[110:111], v[114:115]
	v_pk_mul_f32 v[106:107], v[106:107], v[118:119]
	v_pk_mul_f32 v[112:113], v[112:113], v[116:117]
	v_pk_mul_f32 v[114:115], v[108:109], v[120:121]
	v_cvt_pk_bf16_f32 v108, v110, v111
	v_cvt_pk_bf16_f32 v109, v112, v113
	v_cvt_pk_bf16_f32 v110, v106, v107
	v_lshl_add_u64 v[106:107], s[54:55], 0, v[170:171]
	v_cvt_pk_bf16_f32 v111, v114, v115
	v_lshl_add_u64 v[106:107], v[106:107], 0, v[162:163]
	global_store_dwordx4 v[106:107], v[108:111], off
	v_lshlrev_b32_e32 v112, 16, v148
	v_and_b32_e32 v113, 0xffff0000, v148
	v_lshlrev_b32_e32 v108, 16, v146
	v_and_b32_e32 v109, 0xffff0000, v146
	v_lshlrev_b32_e32 v110, 16, v147
	v_and_b32_e32 v111, 0xffff0000, v147
	v_lshlrev_b32_e32 v114, 16, v149
	v_and_b32_e32 v115, 0xffff0000, v149
	v_pk_mul_f32 v[104:105], v[104:105], v[110:111]
	v_pk_mul_f32 v[102:103], v[102:103], v[108:109]
	v_pk_mul_f32 v[108:109], v[100:101], v[114:115]
	v_pk_mul_f32 v[100:101], v[98:99], v[112:113]
	v_cvt_pk_bf16_f32 v98, v102, v103
	v_cvt_pk_bf16_f32 v99, v104, v105
	v_lshlrev_b32_e32 v102, 16, v144
	v_cvt_pk_bf16_f32 v100, v100, v101
	v_cvt_pk_bf16_f32 v101, v108, v109
	global_store_dwordx4 v[106:107], v[98:101], off offset:256
	v_and_b32_e32 v103, 0xffff0000, v144
	v_lshlrev_b32_e32 v104, 16, v145
	v_lshlrev_b32_e32 v98, 16, v142
	v_and_b32_e32 v99, 0xffff0000, v142
	v_and_b32_e32 v105, 0xffff0000, v145
	v_pk_mul_f32 v[94:95], v[94:95], v[98:99]
	v_lshlrev_b32_e32 v100, 16, v143
	v_and_b32_e32 v101, 0xffff0000, v143
	v_pk_mul_f32 v[98:99], v[92:93], v[104:105]
	v_pk_mul_f32 v[92:93], v[90:91], v[102:103]
	v_cvt_pk_bf16_f32 v90, v94, v95
	v_lshl_add_u64 v[94:95], s[54:55], 0, v[168:169]
	v_pk_mul_f32 v[96:97], v[96:97], v[100:101]
	v_lshl_add_u64 v[94:95], v[94:95], 0, v[162:163]
	v_cvt_pk_bf16_f32 v91, v96, v97
	v_cvt_pk_bf16_f32 v92, v92, v93
	v_cvt_pk_bf16_f32 v93, v98, v99
	global_store_dwordx4 v[94:95], v[90:93], off
	v_lshlrev_b32_e32 v96, 16, v136
	v_and_b32_e32 v97, 0xffff0000, v136
	v_lshlrev_b32_e32 v90, 16, v134
	v_and_b32_e32 v91, 0xffff0000, v134
	v_lshlrev_b32_e32 v92, 16, v135
	v_and_b32_e32 v93, 0xffff0000, v135
	v_lshlrev_b32_e32 v98, 16, v137
	v_and_b32_e32 v99, 0xffff0000, v137
	v_pk_mul_f32 v[88:89], v[88:89], v[92:93]
	v_pk_mul_f32 v[86:87], v[86:87], v[90:91]
	v_pk_mul_f32 v[90:91], v[84:85], v[98:99]
	v_pk_mul_f32 v[84:85], v[82:83], v[96:97]
; __device__ __forceinline__ void unpk8(const u32x4 w, f32x4& a, f32x4& b) { a = (f32x4){bflo(w.x), bfhi(w.x), bflo(w.y), bfhi(w.y)}; b = (f32x4){bflo(w.z), bfhi(w.z), bflo(w.w), bfhi(w.w)}; }
; __device__ __forceinline__ u32x4 pk8(const f32x4 a, const f32x4 b) { u32x4 w; w.x = cvt_pk_bf16(a[0], a[1]); w.y = cvt_pk_bf16(a[2], a[3]); w.z = cvt_pk_bf16(b[0], b[1]); w.w = cvt_pk_bf16(b[2], b[3]); return w; }
;     __device__ __forceinline__ void operator()(const f32x4 (&acc)[2][2][4][2], const Unit& u, int wr, int wc, int fr, int fq) const {
;     ...
;                 for (int bj = 0; bj < 2; ++bj) { const int c = col0 + bj * HALF; gv[m][bj] = *(const u32x4*)(sg + row * 2048 + (SECOND ? 0 : 1024) + c);
;                     if (SECOND) pv[m][bj] = *(const u32x4*)(m2 + row * 2048 + c); } }
; #pragma unroll
;             for (int m = 0; m < 4; ++m) { const size_t row = (size_t)(row0 + ai * HALF + m * 16);
; #pragma unroll
;                 for (int bj = 0; bj < 2; ++bj) { const int c = col0 + bj * HALF;
;                     f32x4 g0, g1; unpk8(gv[m][bj], g0, g1);
;                     f32x4 v0 = g0 * acc[ai][bj][m][0], v1 = g1 * acc[ai][bj][m][1];
;                     if (SECOND) { f32x4 p0, p1; unpk8(pv[m][bj], p0, p1); v0 = v0 + p0; v1 = v1 + p1; *(u32x4*)(o + row * 1024 + c) = pk8(v0, v1); }
;                     else *(u32x4*)(m2 + row * 2048 + c) = pk8(v0, v1); } } }
	v_cvt_pk_bf16_f32 v82, v86, v87
	v_cvt_pk_bf16_f32 v83, v88, v89
	v_lshlrev_b32_e32 v86, 16, v140
	v_cvt_pk_bf16_f32 v84, v84, v85
	v_cvt_pk_bf16_f32 v85, v90, v91
	global_store_dwordx4 v[94:95], v[82:85], off offset:256
	v_and_b32_e32 v87, 0xffff0000, v140
	v_lshlrev_b32_e32 v88, 16, v141
	v_lshlrev_b32_e32 v82, 16, v138
	v_and_b32_e32 v83, 0xffff0000, v138
	v_and_b32_e32 v89, 0xffff0000, v141
	v_pk_mul_f32 v[78:79], v[78:79], v[82:83]
	v_lshlrev_b32_e32 v84, 16, v139
	v_and_b32_e32 v85, 0xffff0000, v139
	v_pk_mul_f32 v[82:83], v[76:77], v[88:89]
	v_pk_mul_f32 v[76:77], v[74:75], v[86:87]
	v_cvt_pk_bf16_f32 v74, v78, v79
	v_lshl_add_u64 v[78:79], s[54:55], 0, v[166:167]
	v_pk_mul_f32 v[80:81], v[80:81], v[84:85]
	v_lshl_add_u64 v[78:79], v[78:79], 0, v[162:163]
	v_cvt_pk_bf16_f32 v75, v80, v81
	v_cvt_pk_bf16_f32 v76, v76, v77
	v_cvt_pk_bf16_f32 v77, v82, v83
	global_store_dwordx4 v[78:79], v[74:77], off
	v_lshlrev_b32_e32 v80, 16, v132
	v_and_b32_e32 v81, 0xffff0000, v132
	v_lshlrev_b32_e32 v74, 16, v130
	v_and_b32_e32 v75, 0xffff0000, v130
	v_lshlrev_b32_e32 v76, 16, v131
	v_and_b32_e32 v77, 0xffff0000, v131
	v_lshlrev_b32_e32 v82, 16, v133
	v_and_b32_e32 v83, 0xffff0000, v133
	v_pk_mul_f32 v[72:73], v[72:73], v[76:77]
	v_pk_mul_f32 v[70:71], v[70:71], v[74:75]
	v_pk_mul_f32 v[74:75], v[68:69], v[82:83]
	v_pk_mul_f32 v[68:69], v[66:67], v[80:81]
	v_cvt_pk_bf16_f32 v66, v70, v71
	v_cvt_pk_bf16_f32 v67, v72, v73
	v_lshl_add_u64 v[100:101], v[164:165], 0, s[46:47]
	v_cvt_pk_bf16_f32 v68, v68, v69
	v_cvt_pk_bf16_f32 v69, v74, v75
	global_store_dwordx4 v[78:79], v[66:69], off offset:256
	s_mov_b64 s[46:47], 0x90000
	v_lshl_add_u64 v[102:103], v[164:165], 0, s[46:47]
	v_lshl_add_u64 v[66:67], s[2:3], 0, v[100:101]
	v_lshl_add_u64 v[66:67], v[66:67], 0, v[162:163]
	global_load_dwordx4 v[76:79], v[66:67], off offset:2048
	global_load_dwordx4 v[80:83], v[66:67], off offset:2304
	v_lshl_add_u64 v[66:67], s[2:3], 0, v[102:103]
	v_lshl_add_u64 v[66:67], v[66:67], 0, v[162:163]
	global_load_dwordx4 v[84:87], v[66:67], off offset:2048
	global_load_dwordx4 v[88:91], v[66:67], off offset:2304
	s_mov_b64 s[46:47], 0xa0000
	v_lshl_add_u64 v[104:105], v[164:165], 0, s[46:47]
	v_lshl_add_u64 v[66:67], s[2:3], 0, v[104:105]
	v_lshl_add_u64 v[66:67], v[66:67], 0, v[162:163]
	global_load_dwordx4 v[92:95], v[66:67], off offset:2048
	global_load_dwordx4 v[96:99], v[66:67], off offset:2304
	s_mov_b64 s[46:47], 0xb0000
	v_lshl_add_u64 v[74:75], v[164:165], 0, s[46:47]
	v_lshl_add_u64 v[66:67], s[2:3], 0, v[74:75]
	v_lshl_add_u64 v[66:67], v[66:67], 0, v[162:163]
	global_load_dwordx4 v[70:73], v[66:67], off offset:2048
	global_load_dwordx4 v[66:69], v[66:67], off offset:2304
	s_waitcnt vmcnt(0)
; __device__ __forceinline__ void unpk8(const u32x4 w, f32x4& a, f32x4& b) { a = (f32x4){bflo(w.x), bfhi(w.x), bflo(w.y), bfhi(w.y)}; b = (f32x4){bflo(w.z), bfhi(w.z), bflo(w.w), bfhi(w.w)}; }
; __device__ __forceinline__ u32x4 pk8(const f32x4 a, const f32x4 b) { u32x4 w; w.x = cvt_pk_bf16(a[0], a[1]); w.y = cvt_pk_bf16(a[2], a[3]); w.z = cvt_pk_bf16(b[0], b[1]); w.w = cvt_pk_bf16(b[2], b[3]); return w; }
; #define PG8_BAR __builtin_amdgcn_s_barrier()
;     __device__ __forceinline__ void operator()(const f32x4 (&acc)[2][2][4][2], const Unit& u, int wr, int wc, int fr, int fq) const {
;     ...
;             for (int m = 0; m < 4; ++m) { const size_t row = (size_t)(row0 + ai * HALF + m * 16);
; #pragma unroll
;                 for (int bj = 0; bj < 2; ++bj) { const int c = col0 + bj * HALF;
;                     f32x4 g0, g1; unpk8(gv[m][bj], g0, g1);
;                     f32x4 v0 = g0 * acc[ai][bj][m][0], v1 = g1 * acc[ai][bj][m][1];
;                     if (SECOND) { f32x4 p0, p1; unpk8(pv[m][bj], p0, p1); v0 = v0 + p0; v1 = v1 + p1; *(u32x4*)(o + row * 1024 + c) = pk8(v0, v1); }
;                     else *(u32x4*)(m2 + row * 2048 + c) = pk8(v0, v1); } } }
; template <class Epi, class Sched, bool ALIGN_EPI = false, bool SP2 = false>
; __device__ __forceinline__ void gemm_phase(PG8_LAS unsigned char* lds, const Gemm g, const Sched& S, const Epi& E, const int wave0) {
;     ...
;         if constexpr (ALIGN_EPI) { if (wr == 0) PG8_BAR; }
;         if constexpr (!Epi::AFTER_DRAIN) { E(acc, cur, wr, wc, fr, fq); S.done(cur); }
;         if (!has_next) break;
; #pragma unroll
;         for (int a = 0; a < 2; ++a)
; #pragma unroll
;             for (int b = 0; b < 2; ++b)
; #pragma unroll
;                 for (int m = 0; m < 4; ++m)
; #pragma unroll
;                     for (int n = 0; n < 2; ++n) acc[a][b][m][n] = (f32x4){0.f, 0.f, 0.f, 0.f};
;         cur = nxt; cA = nA; cB = nB; ++ui;
;         if constexpr (ALIGN_EPI) { if (wr == 1) PG8_BAR; }
	v_lshlrev_b32_e32 v106, 16, v76
	v_and_b32_e32 v107, 0xffff0000, v76
	v_lshlrev_b32_e32 v76, 16, v77
	v_and_b32_e32 v77, 0xffff0000, v77
	v_lshlrev_b32_e32 v108, 16, v78
	v_and_b32_e32 v109, 0xffff0000, v78
	v_lshlrev_b32_e32 v78, 16, v79
	v_and_b32_e32 v79, 0xffff0000, v79
	v_pk_mul_f32 v[62:63], v[62:63], v[106:107]
	v_pk_mul_f32 v[64:65], v[64:65], v[76:77]
	v_pk_mul_f32 v[76:77], v[60:61], v[78:79]
	v_pk_mul_f32 v[60:61], v[58:59], v[108:109]
	v_cvt_pk_bf16_f32 v58, v62, v63
	v_lshl_add_u64 v[62:63], s[54:55], 0, v[100:101]
	v_cvt_pk_bf16_f32 v59, v64, v65
	v_cvt_pk_bf16_f32 v60, v60, v61
	v_cvt_pk_bf16_f32 v61, v76, v77
	v_lshl_add_u64 v[62:63], v[62:63], 0, v[162:163]
	global_store_dwordx4 v[62:63], v[58:61], off
	v_lshlrev_b32_e32 v64, 16, v82
	v_and_b32_e32 v65, 0xffff0000, v82
	v_lshlrev_b32_e32 v58, 16, v80
	v_and_b32_e32 v59, 0xffff0000, v80
	v_lshlrev_b32_e32 v60, 16, v81
	v_and_b32_e32 v61, 0xffff0000, v81
	v_lshlrev_b32_e32 v76, 16, v83
	v_and_b32_e32 v77, 0xffff0000, v83
	v_pk_mul_f32 v[56:57], v[56:57], v[60:61]
	v_pk_mul_f32 v[54:55], v[54:55], v[58:59]
	v_pk_mul_f32 v[58:59], v[52:53], v[76:77]
	v_pk_mul_f32 v[52:53], v[50:51], v[64:65]
	v_cvt_pk_bf16_f32 v50, v54, v55
	v_cvt_pk_bf16_f32 v51, v56, v57
	v_lshlrev_b32_e32 v54, 16, v86
	v_cvt_pk_bf16_f32 v52, v52, v53
	v_cvt_pk_bf16_f32 v53, v58, v59
	global_store_dwordx4 v[62:63], v[50:53], off offset:256
	v_and_b32_e32 v55, 0xffff0000, v86
	v_lshlrev_b32_e32 v56, 16, v87
	v_lshlrev_b32_e32 v50, 16, v84
	v_and_b32_e32 v51, 0xffff0000, v84
	v_and_b32_e32 v57, 0xffff0000, v87
	v_pk_mul_f32 v[46:47], v[46:47], v[50:51]
	v_lshlrev_b32_e32 v52, 16, v85
	v_and_b32_e32 v53, 0xffff0000, v85
	v_pk_mul_f32 v[50:51], v[44:45], v[56:57]
	v_pk_mul_f32 v[44:45], v[42:43], v[54:55]
	v_cvt_pk_bf16_f32 v42, v46, v47
	v_lshl_add_u64 v[46:47], s[54:55], 0, v[102:103]
	v_pk_mul_f32 v[48:49], v[48:49], v[52:53]
	v_lshl_add_u64 v[46:47], v[46:47], 0, v[162:163]
	v_cvt_pk_bf16_f32 v43, v48, v49
	v_cvt_pk_bf16_f32 v44, v44, v45
	v_cvt_pk_bf16_f32 v45, v50, v51
	global_store_dwordx4 v[46:47], v[42:45], off
	v_lshlrev_b32_e32 v48, 16, v90
	v_and_b32_e32 v49, 0xffff0000, v90
	v_lshlrev_b32_e32 v42, 16, v88
	v_and_b32_e32 v43, 0xffff0000, v88
	v_lshlrev_b32_e32 v44, 16, v89
	v_and_b32_e32 v45, 0xffff0000, v89
	v_lshlrev_b32_e32 v50, 16, v91
	v_and_b32_e32 v51, 0xffff0000, v91
	v_pk_mul_f32 v[40:41], v[40:41], v[44:45]
	v_pk_mul_f32 v[38:39], v[38:39], v[42:43]
	v_pk_mul_f32 v[42:43], v[36:37], v[50:51]
	v_pk_mul_f32 v[36:37], v[34:35], v[48:49]
	v_cvt_pk_bf16_f32 v34, v38, v39
	v_cvt_pk_bf16_f32 v35, v40, v41
	v_lshlrev_b32_e32 v38, 16, v94
	v_cvt_pk_bf16_f32 v36, v36, v37
	v_cvt_pk_bf16_f32 v37, v42, v43
	global_store_dwordx4 v[46:47], v[34:37], off offset:256
	v_and_b32_e32 v39, 0xffff0000, v94
	v_lshlrev_b32_e32 v40, 16, v95
	v_lshlrev_b32_e32 v34, 16, v92
	v_and_b32_e32 v35, 0xffff0000, v92
	v_and_b32_e32 v41, 0xffff0000, v95
	v_pk_mul_f32 v[30:31], v[30:31], v[34:35]
	v_lshlrev_b32_e32 v36, 16, v93
	v_and_b32_e32 v37, 0xffff0000, v93
	v_pk_mul_f32 v[34:35], v[28:29], v[40:41]
	v_pk_mul_f32 v[28:29], v[26:27], v[38:39]
	v_cvt_pk_bf16_f32 v26, v30, v31
	v_lshl_add_u64 v[30:31], s[54:55], 0, v[104:105]
	v_pk_mul_f32 v[32:33], v[32:33], v[36:37]
	v_lshl_add_u64 v[30:31], v[30:31], 0, v[162:163]
	v_cvt_pk_bf16_f32 v27, v32, v33
	v_cvt_pk_bf16_f32 v28, v28, v29
	v_cvt_pk_bf16_f32 v29, v34, v35
	global_store_dwordx4 v[30:31], v[26:29], off
	v_lshlrev_b32_e32 v32, 16, v98
	v_and_b32_e32 v33, 0xffff0000, v98
	v_lshlrev_b32_e32 v26, 16, v96
	v_and_b32_e32 v27, 0xffff0000, v96
	v_lshlrev_b32_e32 v28, 16, v97
	v_and_b32_e32 v29, 0xffff0000, v97
	v_lshlrev_b32_e32 v34, 16, v99
	v_and_b32_e32 v35, 0xffff0000, v99
	v_pk_mul_f32 v[24:25], v[24:25], v[28:29]
	v_pk_mul_f32 v[22:23], v[22:23], v[26:27]
	v_pk_mul_f32 v[26:27], v[20:21], v[34:35]
	v_pk_mul_f32 v[20:21], v[18:19], v[32:33]
	v_cvt_pk_bf16_f32 v18, v22, v23
	v_cvt_pk_bf16_f32 v19, v24, v25
	v_lshlrev_b32_e32 v22, 16, v72
	v_cvt_pk_bf16_f32 v20, v20, v21
	v_cvt_pk_bf16_f32 v21, v26, v27
	global_store_dwordx4 v[30:31], v[18:21], off offset:256
	v_and_b32_e32 v23, 0xffff0000, v72
	v_lshlrev_b32_e32 v24, 16, v73
	v_lshlrev_b32_e32 v18, 16, v70
	v_and_b32_e32 v19, 0xffff0000, v70
	v_and_b32_e32 v25, 0xffff0000, v73
	v_pk_mul_f32 v[14:15], v[14:15], v[18:19]
	v_lshlrev_b32_e32 v20, 16, v71
	v_and_b32_e32 v21, 0xffff0000, v71
	v_pk_mul_f32 v[18:19], v[12:13], v[24:25]
	v_pk_mul_f32 v[12:13], v[10:11], v[22:23]
	v_cvt_pk_bf16_f32 v10, v14, v15
	v_lshl_add_u64 v[14:15], s[54:55], 0, v[74:75]
	v_pk_mul_f32 v[16:17], v[16:17], v[20:21]
	v_lshl_add_u64 v[14:15], v[14:15], 0, v[162:163]
	v_cvt_pk_bf16_f32 v11, v16, v17
	v_cvt_pk_bf16_f32 v12, v12, v13
	v_cvt_pk_bf16_f32 v13, v18, v19
	global_store_dwordx4 v[14:15], v[10:13], off
	v_lshlrev_b32_e32 v16, 16, v68
	v_and_b32_e32 v17, 0xffff0000, v68
	v_lshlrev_b32_e32 v10, 16, v66
	v_and_b32_e32 v11, 0xffff0000, v66
	v_lshlrev_b32_e32 v18, 16, v69
	v_and_b32_e32 v19, 0xffff0000, v69
	v_lshlrev_b32_e32 v12, 16, v67
	v_and_b32_e32 v13, 0xffff0000, v67
	v_pk_mul_f32 v[6:7], v[6:7], v[10:11]
	v_pk_mul_f32 v[10:11], v[4:5], v[18:19]
	v_pk_mul_f32 v[4:5], v[2:3], v[16:17]
	v_pk_mul_f32 v[8:9], v[8:9], v[12:13]
	v_cvt_pk_bf16_f32 v2, v6, v7
	s_nop 0
	v_cvt_pk_bf16_f32 v3, v8, v9
	v_cvt_pk_bf16_f32 v4, v4, v5
	v_cvt_pk_bf16_f32 v5, v10, v11
	global_store_dwordx4 v[14:15], v[2:5], off offset:256
	s_cbranch_vccnz .LBB0_846
	s_andn2_b64 vcc, exec, s[44:45]
	s_cbranch_vccnz .LBB0_845
	s_barrier
	s_branch .LBB0_845

; __device__ __forceinline__ void cvt8_chunk(const float* src, unsigned char* dst, size_t chunk, int lane, float sc) {
;     const f32x4* s = (const f32x4*)(src + chunk * 512) + lane * 2; const f32x4 a = s[0] * sc, b = s[1] * sc;
;     int w0 = 0, w1 = 0;
;     w0 = __builtin_amdgcn_cvt_pk_fp8_f32(a.x, a.y, w0, false); w0 = __builtin_amdgcn_cvt_pk_fp8_f32(a.z, a.w, w0, true);
;     w1 = __builtin_amdgcn_cvt_pk_fp8_f32(b.x, b.y, w1, false); w1 = __builtin_amdgcn_cvt_pk_fp8_f32(b.z, b.w, w1, true);
;     *(v2u*)(dst + chunk * 512 + lane * 8) = (v2u){(unsigned)w0, (unsigned)w1};
; __device__ __forceinline__ void prep_phase(Frame& F, const Args& a, int layer, int blk, int nblk_, int part) {
;     ...
;             if (r < n2) { cvt8_chunk(ut, (unsigned char*)(db + DB_U), r, lane, 256.f); continue; } r -= n2;
.Lcv_2_orig:
	v_lshl_add_u64 v[6:7], v[2:3], 4, s[36:37]
	s_lshl_b64 s[36:37], s[22:23], 9
	s_lshl_b64 s[22:23], s[22:23], 11
	v_lshl_add_u64 v[10:11], v[6:7], 0, s[22:23]
	global_load_dwordx4 v[6:9], v[10:11], off offset:16
	global_load_dwordx4 v[10:13], v[10:11], off
	v_mov_b32_e32 v16, v0
	v_mov_b32_e32 v17, v0
	v_lshl_add_u64 v[14:15], v[4:5], 0, s[38:39]
	s_waitcnt vmcnt(0)
	v_pk_mul_f32 v[6:7], v[6:7], s[20:21] op_sel_hi:[1,0]
	v_pk_mul_f32 v[10:11], v[10:11], s[20:21] op_sel_hi:[1,0]
	v_cvt_pk_fp8_f32 v17, v6, v7
	v_cvt_pk_fp8_f32 v16, v10, v11
	v_pk_mul_f32 v[12:13], v[12:13], s[20:21] op_sel_hi:[1,0]
	v_pk_mul_f32 v[8:9], v[8:9], s[20:21] op_sel_hi:[1,0]
	v_readlane_b32 s20, v254, 44
	v_cvt_pk_fp8_f32 v16, v12, v13 op_sel:[0,0,1]
	v_cvt_pk_fp8_f32 v17, v8, v9 op_sel:[0,0,1]
	v_readlane_b32 s21, v254, 45
	s_add_u32 s2, s2, s20
	s_addc_u32 s3, s3, s21
	v_lshl_add_u64 v[6:7], v[14:15], 0, s[36:37]
	s_cmp_lt_i32 s2, 0x10000
	global_store_dwordx2 v[6:7], v[16:17], off
	s_cbranch_scc0 .LBB0_1197

; __device__ __forceinline__ u32x4 pk8(const f32x4 a, const f32x4 b) { u32x4 w; w.x = cvt_pk_bf16(a[0], a[1]); w.y = cvt_pk_bf16(a[2], a[3]); w.z = cvt_pk_bf16(b[0], b[1]); w.w = cvt_pk_bf16(b[2], b[3]); return w; }
; __device__ __forceinline__ void cvt_chunk(const float* src, bf16* dst, size_t chunk, int lane) {
;     const f32x4* s = (const f32x4*)(src + chunk * 512) + lane * 2; const f32x4 a = s[0], b = s[1];
;     *(v4u*)(dst + chunk * 512 + lane * 8) = pk8(a, b);
; }
; __device__ __forceinline__ void prep_phase(Frame& F, const Args& a, int layer, int blk, int nblk_, int part) {
;     ...
;         for (int it = gw; it < ntot; it += NGW) {
;             int r = it;
;             if (r < n2) { cvt8_chunk(ut, (unsigned char*)(db + DB_U), r, lane, 256.f); continue; } r -= n2;
;             if (r < n2) { cvt8_chunk(vt, (unsigned char*)(db + DB_V), r, lane, 64.f); continue; } r -= n2;
;             if (r < n4) { cvt_chunk(pin, (bf16*)(db + DB_PB), r, lane); continue; } r -= n4;
;             if (r < n1) { cvt_chunk(keys, (bf16*)(db + DB_KEYS), r, lane); continue; } r -= n1;
;             {
;                 const int e0 = r * 512 + lane * 8, tq = (e0 >> 7) & 127, p0 = e0 & 127;
;                 const f32x4* s = (const f32x4*)(gws + e0); f32x4 x0 = s[0], x1 = s[1];
; #pragma unroll
;                 for (int j = 0; j < 4; ++j) { if (p0 + j > tq) x0[j] = 0.f; if (p0 + 4 + j > tq) x1[j] = 0.f; }
;                 *(v4u*)((bf16*)(db + DB_GMW) + e0) = pk8(x0, x1);
.LBB0_1292:
	s_add_i32 s22, s5, 0x8000
	s_cmpk_gt_i32 s22, 0x7fff
	s_mov_b64 s[22:23], -1
	s_cbranch_scc0 .LBB0_1306
	s_cmpk_gt_u32 s5, 0x7fff
	s_cbranch_scc0 .LBB0_1303
	s_add_i32 s22, s5, 0xffff8000
	s_cmpk_gt_u32 s22, 0x3fff
	s_mov_b64 s[22:23], -1
	s_cbranch_scc0 .LBB0_1300
	s_add_i32 s22, s5, 0xffff4000
	s_cmpk_gt_u32 s22, 0x1ff
	s_mov_b64 s[22:23], -1
	s_cbranch_scc0 .LBB0_1297
	v_add_u32_e32 v36, s36, v24
	v_ashrrev_i32_e32 v37, 31, v36
	v_lshl_add_u64 v[30:31], v[36:37], 2, s[0:1]
	global_load_dwordx4 v[26:29], v[30:31], off offset:16
	global_load_dwordx4 v[30:33], v[30:31], off
	v_bfe_u32 v25, v36, 7, 7
	v_cmp_gt_u32_e32 vcc, v1, v25
	v_mov_b32_e32 v34, s31
	s_mov_b64 s[22:23], 0
	s_waitcnt vmcnt(0)
	v_cndmask_b32_e32 v35, v32, v32, vcc
	v_cndmask_b32_e32 v38, v33, v33, vcc
	v_cndmask_b32_e32 v39, v30, v34, vcc
	v_cmp_gt_u32_e32 vcc, v18, v25
	s_nop 1
	v_cndmask_b32_e32 v34, v26, v34, vcc
	v_cndmask_b32_e32 v26, v29, v29, vcc
	v_cndmask_b32_e32 v28, v28, v28, vcc
	v_cndmask_b32_e32 v27, v27, v27, vcc
	v_cmp_lt_u32_e32 vcc, v1, v25
	s_nop 1
	v_cndmask_b32_e32 v29, v39, v30, vcc
	v_cndmask_b32_e32 v30, v38, v33, vcc
	v_cndmask_b32_e32 v32, v35, v32, vcc
	v_cndmask_b32_e32 v31, 0, v31, vcc
	v_cmp_le_u32_e32 vcc, v19, v25
	s_nop 1
	v_cndmask_b32_e32 v33, 0, v27, vcc
	v_cmp_le_u32_e32 vcc, v20, v25
	s_nop 1
	v_cndmask_b32_e32 v27, 0, v32, vcc
	v_cmp_le_u32_e32 vcc, v21, v25
	s_nop 1
	v_cndmask_b32_e32 v32, 0, v28, vcc
	v_cmp_le_u32_e32 vcc, v22, v25
	s_nop 1
	v_cndmask_b32_e32 v28, 0, v30, vcc
	v_cmp_le_u32_e32 vcc, v23, v25
	s_nop 1
	v_cndmask_b32_e32 v25, 0, v26, vcc
	v_cvt_pk_bf16_f32 v26, v29, v31
	v_lshl_add_u64 v[30:31], v[36:37], 1, s[2:3]
	v_cvt_pk_bf16_f32 v27, v27, v28
	v_cvt_pk_bf16_f32 v28, v34, v33
	v_cvt_pk_bf16_f32 v29, v32, v25
	global_store_dwordx4 v[30:31], v[26:29], off
.LBB0_1297:
	s_andn2_b64 vcc, exec, s[22:23]
	s_cbranch_vccnz .LBB0_1299
	v_readlane_b32 s22, v254, 30
	s_add_i32 s22, s22, s36
	s_add_i32 s30, s22, 0xfd800000
	v_lshl_add_u64 v[30:31], s[30:31], 2, v[6:7]
	global_load_dwordx4 v[26:29], v[30:31], off
	global_load_dwordx4 v[30:33], v[30:31], off offset:16
	s_waitcnt vmcnt(0)
	v_cvt_pk_bf16_f32 v26, v26, v27
	v_cvt_pk_bf16_f32 v27, v28, v29
	v_cvt_pk_bf16_f32 v28, v30, v31
	v_lshl_add_u64 v[30:31], s[30:31], 1, v[8:9]
	v_cvt_pk_bf16_f32 v29, v32, v33
	global_store_dwordx4 v[30:31], v[26:29], off

; __device__ __forceinline__ u32x4 pk8(const f32x4 a, const f32x4 b) { u32x4 w; w.x = cvt_pk_bf16(a[0], a[1]); w.y = cvt_pk_bf16(a[2], a[3]); w.z = cvt_pk_bf16(b[0], b[1]); w.w = cvt_pk_bf16(b[2], b[3]); return w; }
; __device__ __forceinline__ void cvt_chunk(const float* src, bf16* dst, size_t chunk, int lane) {
;     const f32x4* s = (const f32x4*)(src + chunk * 512) + lane * 2; const f32x4 a = s[0], b = s[1];
;     *(v4u*)(dst + chunk * 512 + lane * 8) = pk8(a, b);
; }
; __device__ __forceinline__ void prep_phase(Frame& F, const Args& a, int layer, int blk, int nblk_, int part) {
;     ...
;             if (r < n4) { cvt_chunk(pin, (bf16*)(db + DB_PB), r, lane); continue; } r -= n4;
.Lcv_p_orig:
	v_readlane_b32 s22, v254, 30
	s_add_i32 s22, s22, s36
	s_add_i32 s30, s22, 0xfe000000
	v_lshl_add_u64 v[30:31], s[30:31], 2, v[10:11]
	global_load_dwordx4 v[26:29], v[30:31], off
	global_load_dwordx4 v[30:33], v[30:31], off offset:16
	s_waitcnt vmcnt(0)
	v_cvt_pk_bf16_f32 v26, v26, v27
	v_cvt_pk_bf16_f32 v27, v28, v29
	v_cvt_pk_bf16_f32 v28, v30, v31
	v_lshl_add_u64 v[30:31], s[30:31], 1, v[12:13]
	v_cvt_pk_bf16_f32 v29, v32, v33
	global_store_dwordx4 v[30:31], v[26:29], off

; __device__ __forceinline__ void cvt8_chunk(const float* src, unsigned char* dst, size_t chunk, int lane, float sc) {
;     const f32x4* s = (const f32x4*)(src + chunk * 512) + lane * 2; const f32x4 a = s[0] * sc, b = s[1] * sc;
;     int w0 = 0, w1 = 0;
;     w0 = __builtin_amdgcn_cvt_pk_fp8_f32(a.x, a.y, w0, false); w0 = __builtin_amdgcn_cvt_pk_fp8_f32(a.z, a.w, w0, true);
;     w1 = __builtin_amdgcn_cvt_pk_fp8_f32(b.x, b.y, w1, false); w1 = __builtin_amdgcn_cvt_pk_fp8_f32(b.z, b.w, w1, true);
;     *(v2u*)(dst + chunk * 512 + lane * 8) = (v2u){(unsigned)w0, (unsigned)w1};
; __device__ __forceinline__ void prep_phase(Frame& F, const Args& a, int layer, int blk, int nblk_, int part) {
;     ...
;             if (r < n2) { cvt8_chunk(vt, (unsigned char*)(db + DB_V), r, lane, 64.f); continue; } r -= n2;
.Lcv_v_orig:
	v_readlane_b32 s22, v254, 30
	s_add_i32 s22, s22, s36
	s_add_i32 s30, s22, 0xff000000
	v_lshl_add_u64 v[30:31], s[30:31], 2, v[14:15]
	global_load_dwordx4 v[26:29], v[30:31], off offset:16
	global_load_dwordx4 v[30:33], v[30:31], off
	s_mov_b32 s22, 0x42800000
	v_mov_b32_e32 v34, v0
	v_mov_b32_e32 v35, v0
	s_waitcnt vmcnt(0)
	v_pk_mul_f32 v[26:27], v[26:27], s[22:23] op_sel_hi:[1,0]
	v_pk_mul_f32 v[30:31], v[30:31], s[22:23] op_sel_hi:[1,0]
	v_cvt_pk_fp8_f32 v35, v26, v27
	v_cvt_pk_fp8_f32 v34, v30, v31
	v_pk_mul_f32 v[32:33], v[32:33], s[22:23] op_sel_hi:[1,0]
	v_pk_mul_f32 v[28:29], v[28:29], s[22:23] op_sel_hi:[1,0]
	v_lshl_add_u64 v[26:27], v[16:17], 0, s[30:31]
	v_cvt_pk_fp8_f32 v34, v32, v33 op_sel:[0,0,1]
	v_cvt_pk_fp8_f32 v35, v28, v29 op_sel:[0,0,1]
	global_store_dwordx2 v[26:27], v[34:35], off

; __device__ __forceinline__ void cvt8_chunk(const float* src, unsigned char* dst, size_t chunk, int lane, float sc) {
;     const f32x4* s = (const f32x4*)(src + chunk * 512) + lane * 2; const f32x4 a = s[0] * sc, b = s[1] * sc;
;     int w0 = 0, w1 = 0;
;     w0 = __builtin_amdgcn_cvt_pk_fp8_f32(a.x, a.y, w0, false); w0 = __builtin_amdgcn_cvt_pk_fp8_f32(a.z, a.w, w0, true);
;     w1 = __builtin_amdgcn_cvt_pk_fp8_f32(b.x, b.y, w1, false); w1 = __builtin_amdgcn_cvt_pk_fp8_f32(b.z, b.w, w1, true);
;     *(v2u*)(dst + chunk * 512 + lane * 8) = (v2u){(unsigned)w0, (unsigned)w1};
; __device__ __forceinline__ void prep_phase(Frame& F, const Args& a, int layer, int blk, int nblk_, int part) {
;     ...
;             if (r < n2) { cvt8_chunk(ut, (unsigned char*)(db + DB_U), r, lane, 256.f); continue; } r -= n2;
.Lcv_u_orig:
	v_lshl_add_u64 v[30:31], s[20:21], 0, v[4:5]
	global_load_dwordx4 v[26:29], v[30:31], off offset:16
	global_load_dwordx4 v[30:33], v[30:31], off
	v_mov_b32_e32 v34, v0
	v_mov_b32_e32 v35, v0
	s_waitcnt vmcnt(0)
	v_pk_mul_f32 v[26:27], v[26:27], s[8:9] op_sel_hi:[1,0]
	v_pk_mul_f32 v[30:31], v[30:31], s[8:9] op_sel_hi:[1,0]
	v_cvt_pk_fp8_f32 v35, v26, v27
	v_cvt_pk_fp8_f32 v34, v30, v31
	v_pk_mul_f32 v[32:33], v[32:33], s[8:9] op_sel_hi:[1,0]
	v_pk_mul_f32 v[28:29], v[28:29], s[8:9] op_sel_hi:[1,0]
	v_cvt_pk_fp8_f32 v34, v32, v33 op_sel:[0,0,1]
	v_cvt_pk_fp8_f32 v35, v28, v29 op_sel:[0,0,1]
	global_store_dwordx2 v[2:3], v[34:35], off
	s_branch .LBB0_1291

; __device__ __forceinline__ void unpk8(const u32x4 w, f32x4& a, f32x4& b) { a = (f32x4){bflo(w.x), bfhi(w.x), bflo(w.y), bfhi(w.y)}; b = (f32x4){bflo(w.z), bfhi(w.z), bflo(w.w), bfhi(w.w)}; }
; __device__ __forceinline__ u32x4 pk8(const f32x4 a, const f32x4 b) { u32x4 w; w.x = cvt_pk_bf16(a[0], a[1]); w.y = cvt_pk_bf16(a[2], a[3]); w.z = cvt_pk_bf16(b[0], b[1]); w.w = cvt_pk_bf16(b[2], b[3]); return w; }
;     __device__ __forceinline__ void operator()(const f32x4 (&acc)[2][2][4][2], const Unit& u, int wr, int wc, int fr, int fq) const {
;         const int row0 = u.pm * BM + wr * 64 + fr, col0 = u.pn * 256 + wc * 32 + 8 * fq;
; #pragma unroll
;         for (int ai = 0; ai < 2; ++ai) { u32x4 gv[4][2], pv[4][2];
; #pragma unroll
;             for (int m = 0; m < 4; ++m) { const size_t row = (size_t)(row0 + ai * HALF + m * 16);
; #pragma unroll
;                 for (int bj = 0; bj < 2; ++bj) { const int c = col0 + bj * HALF; gv[m][bj] = *(const u32x4*)(sg + row * 2048 + (SECOND ? 0 : 1024) + c);
;                     if (SECOND) pv[m][bj] = *(const u32x4*)(m2 + row * 2048 + c); } }
; #pragma unroll
;             for (int m = 0; m < 4; ++m) { const size_t row = (size_t)(row0 + ai * HALF + m * 16);
; #pragma unroll
;                 for (int bj = 0; bj < 2; ++bj) { const int c = col0 + bj * HALF;
;                     f32x4 g0, g1; unpk8(gv[m][bj], g0, g1);
;                     f32x4 v0 = g0 * acc[ai][bj][m][0], v1 = g1 * acc[ai][bj][m][1];
;                     if (SECOND) { f32x4 p0, p1; unpk8(pv[m][bj], p0, p1); v0 = v0 + p0; v1 = v1 + p1; *(u32x4*)(o + row * 1024 + c) = pk8(v0, v1); }
;                     else *(u32x4*)(m2 + row * 2048 + c) = pk8(v0, v1); } } }
.LBB0_1425:
	v_lshl_add_u32 v200, s90, 8, v1
	v_lshl_or_b32 v130, s89, 8, v227
	v_ashrrev_i32_e32 v201, 31, v200
	v_ashrrev_i32_e32 v131, 31, v130
	v_lshlrev_b64 v[132:133], 12, v[200:201]
	v_lshl_add_u64 v[134:135], s[46:47], 0, v[132:133]
	v_lshlrev_b64 v[198:199], 1, v[130:131]
	v_lshl_add_u64 v[132:133], s[52:53], 0, v[132:133]
	v_lshl_add_u64 v[130:131], v[134:135], 0, v[198:199]
	global_load_dwordx4 v[230:233], v[130:131], off
	v_lshl_add_u64 v[132:133], v[132:133], 0, v[198:199]
	global_load_dwordx4 v[238:241], v[132:133], off
	global_load_dwordx4 v[182:185], v[130:131], off offset:256
	global_load_dwordx4 v[178:181], v[132:133], off offset:256
	v_or_b32_e32 v130, 16, v200
	v_ashrrev_i32_e32 v131, 31, v130
	v_lshlrev_b64 v[206:207], 11, v[130:131]
	v_lshlrev_b64 v[130:131], 12, v[130:131]
	v_lshl_add_u64 v[132:133], s[46:47], 0, v[130:131]
	v_lshl_add_u64 v[130:131], s[52:53], 0, v[130:131]
	v_lshl_add_u64 v[132:133], v[132:133], 0, v[198:199]
	global_load_dwordx4 v[174:177], v[132:133], off
	v_lshl_add_u64 v[130:131], v[130:131], 0, v[198:199]
	global_load_dwordx4 v[170:173], v[130:131], off
	global_load_dwordx4 v[166:169], v[132:133], off offset:256
	global_load_dwordx4 v[158:161], v[130:131], off offset:256
	v_or_b32_e32 v130, 32, v200
	v_ashrrev_i32_e32 v131, 31, v130
	v_lshlrev_b64 v[204:205], 11, v[130:131]
	v_lshlrev_b64 v[130:131], 12, v[130:131]
	v_lshl_add_u64 v[132:133], s[46:47], 0, v[130:131]
	v_lshl_add_u64 v[130:131], s[52:53], 0, v[130:131]
	v_lshl_add_u64 v[132:133], v[132:133], 0, v[198:199]
	global_load_dwordx4 v[162:165], v[132:133], off
	v_lshl_add_u64 v[130:131], v[130:131], 0, v[198:199]
	global_load_dwordx4 v[154:157], v[130:131], off
	global_load_dwordx4 v[142:145], v[132:133], off offset:256
	global_load_dwordx4 v[138:141], v[130:131], off offset:256
	v_or_b32_e32 v130, 48, v200
	v_ashrrev_i32_e32 v131, 31, v130
	v_lshlrev_b64 v[202:203], 11, v[130:131]
	v_lshlrev_b64 v[130:131], 12, v[130:131]
	v_lshl_add_u64 v[132:133], s[46:47], 0, v[130:131]
	v_lshl_add_u64 v[132:133], v[132:133], 0, v[198:199]
	v_lshl_add_u64 v[130:131], s[52:53], 0, v[130:131]
	global_load_dwordx4 v[150:153], v[132:133], off
	v_lshl_add_u64 v[130:131], v[130:131], 0, v[198:199]
	global_load_dwordx4 v[146:149], v[130:131], off
	global_load_dwordx4 v[134:137], v[132:133], off offset:256
	global_load_dwordx4 v[130:133], v[130:131], off offset:256
	v_lshlrev_b64 v[224:225], 11, v[200:201]
	s_mov_b64 s[70:71], -1
	s_and_b64 vcc, exec, s[40:41]
	s_waitcnt vmcnt(0)
	v_lshlrev_b32_e32 v246, 16, v238
	v_lshlrev_b32_e32 v234, 16, v230
	v_and_b32_e32 v235, 0xffff0000, v230
	v_lshlrev_b32_e32 v230, 16, v231
	v_and_b32_e32 v231, 0xffff0000, v231
	v_lshlrev_b32_e32 v248, 16, v232
	v_and_b32_e32 v249, 0xffff0000, v232
	v_and_b32_e32 v247, 0xffff0000, v238
	v_lshlrev_b32_e32 v238, 16, v239
	v_and_b32_e32 v239, 0xffff0000, v239
	v_lshlrev_b32_e32 v236, 16, v240
	v_and_b32_e32 v237, 0xffff0000, v240
	v_pk_fma_f32 v[124:125], v[124:125], v[230:231], v[238:239]
	v_pk_fma_f32 v[122:123], v[122:123], v[234:235], v[246:247]
	v_pk_fma_f32 v[126:127], v[126:127], v[248:249], v[236:237]
	v_lshlrev_b32_e32 v232, 16, v233
	v_and_b32_e32 v233, 0xffff0000, v233
	v_lshlrev_b32_e32 v240, 16, v241
	v_and_b32_e32 v241, 0xffff0000, v241
	v_cvt_pk_bf16_f32 v122, v122, v123
	v_cvt_pk_bf16_f32 v123, v124, v125
	v_cvt_pk_bf16_f32 v124, v126, v127
	v_lshl_add_u64 v[126:127], s[54:55], 0, v[224:225]
	v_pk_fma_f32 v[128:129], v[128:129], v[232:233], v[240:241]
	v_lshl_add_u64 v[126:127], v[126:127], 0, v[198:199]
	v_cvt_pk_bf16_f32 v125, v128, v129
	global_store_dwordx4 v[126:127], v[122:125], off
	v_lshlrev_b32_e32 v128, 16, v184
	v_and_b32_e32 v129, 0xffff0000, v184
	v_lshlrev_b32_e32 v122, 16, v182
	v_and_b32_e32 v123, 0xffff0000, v182
	v_lshlrev_b32_e32 v124, 16, v183
	v_and_b32_e32 v125, 0xffff0000, v183
	v_lshlrev_b32_e32 v182, 16, v185
	v_and_b32_e32 v183, 0xffff0000, v185
	v_lshlrev_b32_e32 v184, 16, v178
	v_and_b32_e32 v185, 0xffff0000, v178
	v_lshlrev_b32_e32 v178, 16, v179
	v_and_b32_e32 v179, 0xffff0000, v179
	v_lshlrev_b32_e32 v224, 16, v180
	v_and_b32_e32 v225, 0xffff0000, v180
	v_lshlrev_b32_e32 v180, 16, v181
	v_and_b32_e32 v181, 0xffff0000, v181
	v_pk_fma_f32 v[120:121], v[120:121], v[124:125], v[178:179]
	v_pk_fma_f32 v[118:119], v[118:119], v[122:123], v[184:185]
	v_pk_fma_f32 v[122:123], v[116:117], v[182:183], v[180:181]
	v_pk_fma_f32 v[116:117], v[114:115], v[128:129], v[224:225]
	v_cvt_pk_bf16_f32 v114, v118, v119
	v_cvt_pk_bf16_f32 v115, v120, v121
	v_lshlrev_b32_e32 v118, 16, v176
	v_cvt_pk_bf16_f32 v116, v116, v117
	v_cvt_pk_bf16_f32 v117, v122, v123
	global_store_dwordx4 v[126:127], v[114:117], off offset:256
	v_lshlrev_b32_e32 v122, 16, v170
	v_and_b32_e32 v123, 0xffff0000, v170
	v_lshlrev_b32_e32 v114, 16, v174
	v_and_b32_e32 v115, 0xffff0000, v174
	v_and_b32_e32 v119, 0xffff0000, v176
	v_lshlrev_b32_e32 v120, 16, v177
	v_and_b32_e32 v121, 0xffff0000, v177
	v_lshlrev_b32_e32 v126, 16, v172
	v_and_b32_e32 v127, 0xffff0000, v172
	v_lshlrev_b32_e32 v128, 16, v173
	v_and_b32_e32 v129, 0xffff0000, v173
	v_pk_fma_f32 v[110:111], v[110:111], v[114:115], v[122:123]
	v_lshlrev_b32_e32 v116, 16, v175
	v_and_b32_e32 v117, 0xffff0000, v175
	v_lshlrev_b32_e32 v124, 16, v171
	v_and_b32_e32 v125, 0xffff0000, v171
	v_pk_fma_f32 v[114:115], v[108:109], v[120:121], v[128:129]
	v_pk_fma_f32 v[108:109], v[106:107], v[118:119], v[126:127]
	v_cvt_pk_bf16_f32 v106, v110, v111
	v_lshl_add_u64 v[110:111], s[54:55], 0, v[206:207]
	v_pk_fma_f32 v[112:113], v[112:113], v[116:117], v[124:125]
	v_lshl_add_u64 v[110:111], v[110:111], 0, v[198:199]
	v_cvt_pk_bf16_f32 v107, v112, v113
; __device__ __forceinline__ void unpk8(const u32x4 w, f32x4& a, f32x4& b) { a = (f32x4){bflo(w.x), bfhi(w.x), bflo(w.y), bfhi(w.y)}; b = (f32x4){bflo(w.z), bfhi(w.z), bflo(w.w), bfhi(w.w)}; }
; __device__ __forceinline__ u32x4 pk8(const f32x4 a, const f32x4 b) { u32x4 w; w.x = cvt_pk_bf16(a[0], a[1]); w.y = cvt_pk_bf16(a[2], a[3]); w.z = cvt_pk_bf16(b[0], b[1]); w.w = cvt_pk_bf16(b[2], b[3]); return w; }
;     __device__ __forceinline__ void operator()(const f32x4 (&acc)[2][2][4][2], const Unit& u, int wr, int wc, int fr, int fq) const {
;     ...
;         for (int ai = 0; ai < 2; ++ai) { u32x4 gv[4][2], pv[4][2];
; #pragma unroll
;             for (int m = 0; m < 4; ++m) { const size_t row = (size_t)(row0 + ai * HALF + m * 16);
; #pragma unroll
;                 for (int bj = 0; bj < 2; ++bj) { const int c = col0 + bj * HALF; gv[m][bj] = *(const u32x4*)(sg + row * 2048 + (SECOND ? 0 : 1024) + c);
;                     if (SECOND) pv[m][bj] = *(const u32x4*)(m2 + row * 2048 + c); } }
;     ...
;             for (int m = 0; m < 4; ++m) { const size_t row = (size_t)(row0 + ai * HALF + m * 16);
; #pragma unroll
;                 for (int bj = 0; bj < 2; ++bj) { const int c = col0 + bj * HALF;
;                     f32x4 g0, g1; unpk8(gv[m][bj], g0, g1);
;                     f32x4 v0 = g0 * acc[ai][bj][m][0], v1 = g1 * acc[ai][bj][m][1];
;                     if (SECOND) { f32x4 p0, p1; unpk8(pv[m][bj], p0, p1); v0 = v0 + p0; v1 = v1 + p1; *(u32x4*)(o + row * 1024 + c) = pk8(v0, v1); }
;                     else *(u32x4*)(m2 + row * 2048 + c) = pk8(v0, v1); } } }
	v_cvt_pk_bf16_f32 v108, v108, v109
	v_cvt_pk_bf16_f32 v109, v114, v115
	global_store_dwordx4 v[110:111], v[106:109], off
	v_lshlrev_b32_e32 v112, 16, v168
	v_and_b32_e32 v113, 0xffff0000, v168
	v_lshlrev_b32_e32 v106, 16, v166
	v_and_b32_e32 v107, 0xffff0000, v166
	v_lshlrev_b32_e32 v108, 16, v167
	v_and_b32_e32 v109, 0xffff0000, v167
	v_lshlrev_b32_e32 v114, 16, v169
	v_and_b32_e32 v115, 0xffff0000, v169
	v_lshlrev_b32_e32 v116, 16, v158
	v_and_b32_e32 v117, 0xffff0000, v158
	v_lshlrev_b32_e32 v118, 16, v159
	v_and_b32_e32 v119, 0xffff0000, v159
	v_lshlrev_b32_e32 v120, 16, v160
	v_and_b32_e32 v121, 0xffff0000, v160
	v_lshlrev_b32_e32 v122, 16, v161
	v_and_b32_e32 v123, 0xffff0000, v161
	v_pk_fma_f32 v[104:105], v[104:105], v[108:109], v[118:119]
	v_pk_fma_f32 v[102:103], v[102:103], v[106:107], v[116:117]
	v_pk_fma_f32 v[106:107], v[100:101], v[114:115], v[122:123]
	v_pk_fma_f32 v[100:101], v[98:99], v[112:113], v[120:121]
	v_cvt_pk_bf16_f32 v98, v102, v103
	v_cvt_pk_bf16_f32 v99, v104, v105
	v_lshlrev_b32_e32 v102, 16, v164
	v_cvt_pk_bf16_f32 v100, v100, v101
	v_cvt_pk_bf16_f32 v101, v106, v107
	global_store_dwordx4 v[110:111], v[98:101], off offset:256
	v_lshlrev_b32_e32 v106, 16, v154
	v_and_b32_e32 v107, 0xffff0000, v154
	v_lshlrev_b32_e32 v98, 16, v162
	v_and_b32_e32 v99, 0xffff0000, v162
	v_and_b32_e32 v103, 0xffff0000, v164
	v_lshlrev_b32_e32 v104, 16, v165
	v_and_b32_e32 v105, 0xffff0000, v165
	v_lshlrev_b32_e32 v110, 16, v156
	v_and_b32_e32 v111, 0xffff0000, v156
	v_lshlrev_b32_e32 v112, 16, v157
	v_and_b32_e32 v113, 0xffff0000, v157
	v_pk_fma_f32 v[94:95], v[94:95], v[98:99], v[106:107]
	v_lshlrev_b32_e32 v100, 16, v163
	v_and_b32_e32 v101, 0xffff0000, v163
	v_lshlrev_b32_e32 v108, 16, v155
	v_and_b32_e32 v109, 0xffff0000, v155
	v_pk_fma_f32 v[98:99], v[92:93], v[104:105], v[112:113]
	v_pk_fma_f32 v[92:93], v[90:91], v[102:103], v[110:111]
	v_cvt_pk_bf16_f32 v90, v94, v95
	v_lshl_add_u64 v[94:95], s[54:55], 0, v[204:205]
	v_pk_fma_f32 v[96:97], v[96:97], v[100:101], v[108:109]
	v_lshl_add_u64 v[94:95], v[94:95], 0, v[198:199]
	v_cvt_pk_bf16_f32 v91, v96, v97
	v_cvt_pk_bf16_f32 v92, v92, v93
	v_cvt_pk_bf16_f32 v93, v98, v99
	global_store_dwordx4 v[94:95], v[90:93], off
	v_lshlrev_b32_e32 v96, 16, v144
	v_and_b32_e32 v97, 0xffff0000, v144
	v_lshlrev_b32_e32 v90, 16, v142
	v_and_b32_e32 v91, 0xffff0000, v142
	v_lshlrev_b32_e32 v92, 16, v143
	v_and_b32_e32 v93, 0xffff0000, v143
	v_lshlrev_b32_e32 v98, 16, v145
	v_and_b32_e32 v99, 0xffff0000, v145
	v_lshlrev_b32_e32 v100, 16, v138
	v_and_b32_e32 v101, 0xffff0000, v138
	v_lshlrev_b32_e32 v102, 16, v139
	v_and_b32_e32 v103, 0xffff0000, v139
	v_lshlrev_b32_e32 v104, 16, v140
	v_and_b32_e32 v105, 0xffff0000, v140
	v_lshlrev_b32_e32 v106, 16, v141
	v_and_b32_e32 v107, 0xffff0000, v141
	v_pk_fma_f32 v[88:89], v[88:89], v[92:93], v[102:103]
	v_pk_fma_f32 v[86:87], v[86:87], v[90:91], v[100:101]
	v_pk_fma_f32 v[90:91], v[84:85], v[98:99], v[106:107]
	v_pk_fma_f32 v[84:85], v[82:83], v[96:97], v[104:105]
	v_cvt_pk_bf16_f32 v82, v86, v87
	v_cvt_pk_bf16_f32 v83, v88, v89
	v_lshlrev_b32_e32 v86, 16, v152
	v_cvt_pk_bf16_f32 v84, v84, v85
	v_cvt_pk_bf16_f32 v85, v90, v91
	global_store_dwordx4 v[94:95], v[82:85], off offset:256
	v_lshlrev_b32_e32 v90, 16, v146
	v_and_b32_e32 v91, 0xffff0000, v146
	v_lshlrev_b32_e32 v82, 16, v150
	v_and_b32_e32 v83, 0xffff0000, v150
	v_and_b32_e32 v87, 0xffff0000, v152
	v_lshlrev_b32_e32 v88, 16, v153
	v_and_b32_e32 v89, 0xffff0000, v153
	v_lshlrev_b32_e32 v94, 16, v148
	v_and_b32_e32 v95, 0xffff0000, v148
	v_lshlrev_b32_e32 v96, 16, v149
	v_and_b32_e32 v97, 0xffff0000, v149
	v_pk_fma_f32 v[78:79], v[78:79], v[82:83], v[90:91]
	v_lshlrev_b32_e32 v84, 16, v151
	v_and_b32_e32 v85, 0xffff0000, v151
	v_lshlrev_b32_e32 v92, 16, v147
	v_and_b32_e32 v93, 0xffff0000, v147
	v_pk_fma_f32 v[82:83], v[76:77], v[88:89], v[96:97]
	v_pk_fma_f32 v[76:77], v[74:75], v[86:87], v[94:95]
	v_cvt_pk_bf16_f32 v74, v78, v79
	v_lshl_add_u64 v[78:79], s[54:55], 0, v[202:203]
	v_pk_fma_f32 v[80:81], v[80:81], v[84:85], v[92:93]
	v_lshl_add_u64 v[78:79], v[78:79], 0, v[198:199]
	v_cvt_pk_bf16_f32 v75, v80, v81
	v_cvt_pk_bf16_f32 v76, v76, v77
	v_cvt_pk_bf16_f32 v77, v82, v83
	global_store_dwordx4 v[78:79], v[74:77], off
	v_lshlrev_b32_e32 v80, 16, v136
	v_and_b32_e32 v81, 0xffff0000, v136
	v_lshlrev_b32_e32 v74, 16, v134
	v_and_b32_e32 v75, 0xffff0000, v134
	v_lshlrev_b32_e32 v82, 16, v137
	v_and_b32_e32 v83, 0xffff0000, v137
	v_lshlrev_b32_e32 v84, 16, v130
	v_and_b32_e32 v85, 0xffff0000, v130
	v_lshlrev_b32_e32 v88, 16, v132
	v_and_b32_e32 v89, 0xffff0000, v132
	v_lshlrev_b32_e32 v90, 16, v133
	v_and_b32_e32 v91, 0xffff0000, v133
	v_lshlrev_b32_e32 v76, 16, v135
	v_and_b32_e32 v77, 0xffff0000, v135
	v_lshlrev_b32_e32 v86, 16, v131
	v_and_b32_e32 v87, 0xffff0000, v131
	v_pk_fma_f32 v[70:71], v[70:71], v[74:75], v[84:85]
	v_pk_fma_f32 v[74:75], v[68:69], v[82:83], v[90:91]
	v_pk_fma_f32 v[68:69], v[66:67], v[80:81], v[88:89]
	v_cvt_pk_bf16_f32 v66, v70, v71
	v_pk_fma_f32 v[72:73], v[72:73], v[76:77], v[86:87]
	s_nop 0
	v_cvt_pk_bf16_f32 v67, v72, v73
	v_cvt_pk_bf16_f32 v68, v68, v69
	v_cvt_pk_bf16_f32 v69, v74, v75
	global_store_dwordx4 v[78:79], v[66:69], off offset:256
	s_nop 1
	v_add_u32_e32 v66, 0x80, v200
	v_ashrrev_i32_e32 v67, 31, v66
	v_lshlrev_b64 v[136:137], 11, v[66:67]
	v_lshlrev_b64 v[66:67], 12, v[66:67]
	v_lshl_add_u64 v[68:69], s[46:47], 0, v[66:67]
	v_lshl_add_u64 v[66:67], s[52:53], 0, v[66:67]
	v_lshl_add_u64 v[68:69], v[68:69], 0, v[198:199]
	global_load_dwordx4 v[112:115], v[68:69], off
	v_lshl_add_u64 v[66:67], v[66:67], 0, v[198:199]
	global_load_dwordx4 v[116:119], v[66:67], off
; __device__ __forceinline__ void unpk8(const u32x4 w, f32x4& a, f32x4& b) { a = (f32x4){bflo(w.x), bfhi(w.x), bflo(w.y), bfhi(w.y)}; b = (f32x4){bflo(w.z), bfhi(w.z), bflo(w.w), bfhi(w.w)}; }
; __device__ __forceinline__ u32x4 pk8(const f32x4 a, const f32x4 b) { u32x4 w; w.x = cvt_pk_bf16(a[0], a[1]); w.y = cvt_pk_bf16(a[2], a[3]); w.z = cvt_pk_bf16(b[0], b[1]); w.w = cvt_pk_bf16(b[2], b[3]); return w; }
;     __device__ __forceinline__ void operator()(const f32x4 (&acc)[2][2][4][2], const Unit& u, int wr, int wc, int fr, int fq) const {
;     ...
;         for (int ai = 0; ai < 2; ++ai) { u32x4 gv[4][2], pv[4][2];
; #pragma unroll
;             for (int m = 0; m < 4; ++m) { const size_t row = (size_t)(row0 + ai * HALF + m * 16);
; #pragma unroll
;                 for (int bj = 0; bj < 2; ++bj) { const int c = col0 + bj * HALF; gv[m][bj] = *(const u32x4*)(sg + row * 2048 + (SECOND ? 0 : 1024) + c);
;                     if (SECOND) pv[m][bj] = *(const u32x4*)(m2 + row * 2048 + c); } }
; #pragma unroll
;             for (int m = 0; m < 4; ++m) { const size_t row = (size_t)(row0 + ai * HALF + m * 16);
; #pragma unroll
;                 for (int bj = 0; bj < 2; ++bj) { const int c = col0 + bj * HALF;
;                     f32x4 g0, g1; unpk8(gv[m][bj], g0, g1);
;                     f32x4 v0 = g0 * acc[ai][bj][m][0], v1 = g1 * acc[ai][bj][m][1];
;                     if (SECOND) { f32x4 p0, p1; unpk8(pv[m][bj], p0, p1); v0 = v0 + p0; v1 = v1 + p1; *(u32x4*)(o + row * 1024 + c) = pk8(v0, v1); }
;                     else *(u32x4*)(m2 + row * 2048 + c) = pk8(v0, v1); } } }
	global_load_dwordx4 v[120:123], v[68:69], off offset:256
	global_load_dwordx4 v[124:127], v[66:67], off offset:256
	v_add_u32_e32 v66, 0x90, v200
	v_ashrrev_i32_e32 v67, 31, v66
	v_lshlrev_b64 v[110:111], 11, v[66:67]
	v_lshlrev_b64 v[66:67], 12, v[66:67]
	v_lshl_add_u64 v[68:69], s[46:47], 0, v[66:67]
	v_lshl_add_u64 v[66:67], s[52:53], 0, v[66:67]
	v_lshl_add_u64 v[68:69], v[68:69], 0, v[198:199]
	global_load_dwordx4 v[128:131], v[68:69], off
	v_lshl_add_u64 v[66:67], v[66:67], 0, v[198:199]
	global_load_dwordx4 v[132:135], v[66:67], off
	global_load_dwordx4 v[102:105], v[68:69], off offset:256
	global_load_dwordx4 v[98:101], v[66:67], off offset:256
	v_add_u32_e32 v66, 0xa0, v200
	v_ashrrev_i32_e32 v67, 31, v66
	v_lshlrev_b64 v[108:109], 11, v[66:67]
	v_lshlrev_b64 v[66:67], 12, v[66:67]
	v_lshl_add_u64 v[68:69], s[46:47], 0, v[66:67]
	v_lshl_add_u64 v[66:67], s[52:53], 0, v[66:67]
	v_lshl_add_u64 v[68:69], v[68:69], 0, v[198:199]
	global_load_dwordx4 v[94:97], v[68:69], off
	v_lshl_add_u64 v[66:67], v[66:67], 0, v[198:199]
	global_load_dwordx4 v[90:93], v[66:67], off
	global_load_dwordx4 v[86:89], v[68:69], off offset:256
	global_load_dwordx4 v[82:85], v[66:67], off offset:256
	v_add_u32_e32 v66, 0xb0, v200
	v_ashrrev_i32_e32 v67, 31, v66
	v_lshlrev_b64 v[106:107], 11, v[66:67]
	v_lshlrev_b64 v[66:67], 12, v[66:67]
	v_lshl_add_u64 v[68:69], s[46:47], 0, v[66:67]
	v_lshl_add_u64 v[68:69], v[68:69], 0, v[198:199]
	v_lshl_add_u64 v[66:67], s[52:53], 0, v[66:67]
	global_load_dwordx4 v[78:81], v[68:69], off
	v_lshl_add_u64 v[66:67], v[66:67], 0, v[198:199]
	global_load_dwordx4 v[74:77], v[66:67], off
	global_load_dwordx4 v[70:73], v[68:69], off offset:256
	global_load_dwordx4 v[66:69], v[66:67], off offset:256
	s_waitcnt vmcnt(0)
	v_lshlrev_b32_e32 v138, 16, v112
	v_and_b32_e32 v139, 0xffff0000, v112
	v_lshlrev_b32_e32 v142, 16, v116
	v_and_b32_e32 v143, 0xffff0000, v116
	v_lshlrev_b32_e32 v112, 16, v113
	v_and_b32_e32 v113, 0xffff0000, v113
	v_lshlrev_b32_e32 v140, 16, v114
	v_and_b32_e32 v141, 0xffff0000, v114
	v_lshlrev_b32_e32 v114, 16, v115
	v_and_b32_e32 v115, 0xffff0000, v115
	v_lshlrev_b32_e32 v116, 16, v117
	v_and_b32_e32 v117, 0xffff0000, v117
	v_lshlrev_b32_e32 v144, 16, v118
	v_and_b32_e32 v145, 0xffff0000, v118
	v_lshlrev_b32_e32 v118, 16, v119
	v_and_b32_e32 v119, 0xffff0000, v119
	v_pk_fma_f32 v[62:63], v[62:63], v[138:139], v[142:143]
	v_pk_fma_f32 v[64:65], v[64:65], v[112:113], v[116:117]
	v_pk_fma_f32 v[112:113], v[60:61], v[114:115], v[118:119]
	v_pk_fma_f32 v[60:61], v[58:59], v[140:141], v[144:145]
	v_cvt_pk_bf16_f32 v58, v62, v63
	v_lshl_add_u64 v[62:63], s[54:55], 0, v[136:137]
	v_cvt_pk_bf16_f32 v59, v64, v65
	v_cvt_pk_bf16_f32 v60, v60, v61
	v_cvt_pk_bf16_f32 v61, v112, v113
	v_lshl_add_u64 v[62:63], v[62:63], 0, v[198:199]
	global_store_dwordx4 v[62:63], v[58:61], off
	v_lshlrev_b32_e32 v64, 16, v122
	v_and_b32_e32 v65, 0xffff0000, v122
	v_lshlrev_b32_e32 v58, 16, v120
	v_and_b32_e32 v59, 0xffff0000, v120
	v_lshlrev_b32_e32 v60, 16, v121
	v_and_b32_e32 v61, 0xffff0000, v121
	v_lshlrev_b32_e32 v112, 16, v123
	v_and_b32_e32 v113, 0xffff0000, v123
	v_lshlrev_b32_e32 v114, 16, v124
	v_and_b32_e32 v115, 0xffff0000, v124
	v_lshlrev_b32_e32 v116, 16, v125
	v_and_b32_e32 v117, 0xffff0000, v125
	v_lshlrev_b32_e32 v118, 16, v126
	v_and_b32_e32 v119, 0xffff0000, v126
	v_lshlrev_b32_e32 v120, 16, v127
	v_and_b32_e32 v121, 0xffff0000, v127
	v_pk_fma_f32 v[56:57], v[56:57], v[60:61], v[116:117]
	v_pk_fma_f32 v[54:55], v[54:55], v[58:59], v[114:115]
	v_pk_fma_f32 v[58:59], v[52:53], v[112:113], v[120:121]
	v_pk_fma_f32 v[52:53], v[50:51], v[64:65], v[118:119]
	v_cvt_pk_bf16_f32 v50, v54, v55
	v_cvt_pk_bf16_f32 v51, v56, v57
	v_lshlrev_b32_e32 v54, 16, v130
	v_cvt_pk_bf16_f32 v52, v52, v53
	v_cvt_pk_bf16_f32 v53, v58, v59
	global_store_dwordx4 v[62:63], v[50:53], off offset:256
	v_lshlrev_b32_e32 v58, 16, v132
	v_and_b32_e32 v59, 0xffff0000, v132
	v_lshlrev_b32_e32 v50, 16, v128
	v_and_b32_e32 v51, 0xffff0000, v128
	v_and_b32_e32 v55, 0xffff0000, v130
	v_lshlrev_b32_e32 v56, 16, v131
	v_and_b32_e32 v57, 0xffff0000, v131
	v_lshlrev_b32_e32 v62, 16, v134
	v_and_b32_e32 v63, 0xffff0000, v134
	v_lshlrev_b32_e32 v64, 16, v135
	v_and_b32_e32 v65, 0xffff0000, v135
	v_pk_fma_f32 v[46:47], v[46:47], v[50:51], v[58:59]
	v_lshlrev_b32_e32 v52, 16, v129
	v_and_b32_e32 v53, 0xffff0000, v129
	v_lshlrev_b32_e32 v60, 16, v133
	v_and_b32_e32 v61, 0xffff0000, v133
	v_pk_fma_f32 v[50:51], v[44:45], v[56:57], v[64:65]
	v_pk_fma_f32 v[44:45], v[42:43], v[54:55], v[62:63]
	v_cvt_pk_bf16_f32 v42, v46, v47
	v_lshl_add_u64 v[46:47], s[54:55], 0, v[110:111]
	v_pk_fma_f32 v[48:49], v[48:49], v[52:53], v[60:61]
	v_lshl_add_u64 v[46:47], v[46:47], 0, v[198:199]
	v_cvt_pk_bf16_f32 v43, v48, v49
	v_cvt_pk_bf16_f32 v44, v44, v45
	v_cvt_pk_bf16_f32 v45, v50, v51
	global_store_dwordx4 v[46:47], v[42:45], off
	v_lshlrev_b32_e32 v48, 16, v104
	v_and_b32_e32 v49, 0xffff0000, v104
; __device__ __forceinline__ void unpk8(const u32x4 w, f32x4& a, f32x4& b) { a = (f32x4){bflo(w.x), bfhi(w.x), bflo(w.y), bfhi(w.y)}; b = (f32x4){bflo(w.z), bfhi(w.z), bflo(w.w), bfhi(w.w)}; }
; __device__ __forceinline__ u32x4 pk8(const f32x4 a, const f32x4 b) { u32x4 w; w.x = cvt_pk_bf16(a[0], a[1]); w.y = cvt_pk_bf16(a[2], a[3]); w.z = cvt_pk_bf16(b[0], b[1]); w.w = cvt_pk_bf16(b[2], b[3]); return w; }
; #define PG8_BAR __builtin_amdgcn_s_barrier()
;     __device__ __forceinline__ void operator()(const f32x4 (&acc)[2][2][4][2], const Unit& u, int wr, int wc, int fr, int fq) const {
;     ...
;             for (int m = 0; m < 4; ++m) { const size_t row = (size_t)(row0 + ai * HALF + m * 16);
; #pragma unroll
;                 for (int bj = 0; bj < 2; ++bj) { const int c = col0 + bj * HALF;
;                     f32x4 g0, g1; unpk8(gv[m][bj], g0, g1);
;                     f32x4 v0 = g0 * acc[ai][bj][m][0], v1 = g1 * acc[ai][bj][m][1];
;                     if (SECOND) { f32x4 p0, p1; unpk8(pv[m][bj], p0, p1); v0 = v0 + p0; v1 = v1 + p1; *(u32x4*)(o + row * 1024 + c) = pk8(v0, v1); }
;                     else *(u32x4*)(m2 + row * 2048 + c) = pk8(v0, v1); } } }
; template <class Epi, class Sched, bool ALIGN_EPI = false, bool SP2 = false>
; __device__ __forceinline__ void gemm_phase(PG8_LAS unsigned char* lds, const Gemm g, const Sched& S, const Epi& E, const int wave0) {
;     ...
;         if constexpr (ALIGN_EPI) { if (wr == 0) PG8_BAR; }
;         if constexpr (!Epi::AFTER_DRAIN) { E(acc, cur, wr, wc, fr, fq); S.done(cur); }
;         if (!has_next) break;
; #pragma unroll
;         for (int a = 0; a < 2; ++a)
; #pragma unroll
;             for (int b = 0; b < 2; ++b)
; #pragma unroll
;                 for (int m = 0; m < 4; ++m)
; #pragma unroll
;                     for (int n = 0; n < 2; ++n) acc[a][b][m][n] = (f32x4){0.f, 0.f, 0.f, 0.f};
;         cur = nxt; cA = nA; cB = nB; ++ui;
;         if constexpr (ALIGN_EPI) { if (wr == 1) PG8_BAR; }
	v_lshlrev_b32_e32 v42, 16, v102
	v_and_b32_e32 v43, 0xffff0000, v102
	v_lshlrev_b32_e32 v44, 16, v103
	v_and_b32_e32 v45, 0xffff0000, v103
	v_lshlrev_b32_e32 v50, 16, v105
	v_and_b32_e32 v51, 0xffff0000, v105
	v_lshlrev_b32_e32 v52, 16, v98
	v_and_b32_e32 v53, 0xffff0000, v98
	v_lshlrev_b32_e32 v54, 16, v99
	v_and_b32_e32 v55, 0xffff0000, v99
	v_lshlrev_b32_e32 v56, 16, v100
	v_and_b32_e32 v57, 0xffff0000, v100
	v_lshlrev_b32_e32 v58, 16, v101
	v_and_b32_e32 v59, 0xffff0000, v101
	v_pk_fma_f32 v[40:41], v[40:41], v[44:45], v[54:55]
	v_pk_fma_f32 v[38:39], v[38:39], v[42:43], v[52:53]
	v_pk_fma_f32 v[42:43], v[36:37], v[50:51], v[58:59]
	v_pk_fma_f32 v[36:37], v[34:35], v[48:49], v[56:57]
	v_cvt_pk_bf16_f32 v34, v38, v39
	v_cvt_pk_bf16_f32 v35, v40, v41
	v_lshlrev_b32_e32 v38, 16, v96
	v_cvt_pk_bf16_f32 v36, v36, v37
	v_cvt_pk_bf16_f32 v37, v42, v43
	global_store_dwordx4 v[46:47], v[34:37], off offset:256
	v_lshlrev_b32_e32 v42, 16, v90
	v_and_b32_e32 v43, 0xffff0000, v90
	v_lshlrev_b32_e32 v34, 16, v94
	v_and_b32_e32 v35, 0xffff0000, v94
	v_and_b32_e32 v39, 0xffff0000, v96
	v_lshlrev_b32_e32 v40, 16, v97
	v_and_b32_e32 v41, 0xffff0000, v97
	v_lshlrev_b32_e32 v46, 16, v92
	v_and_b32_e32 v47, 0xffff0000, v92
	v_lshlrev_b32_e32 v48, 16, v93
	v_and_b32_e32 v49, 0xffff0000, v93
	v_pk_fma_f32 v[30:31], v[30:31], v[34:35], v[42:43]
	v_lshlrev_b32_e32 v36, 16, v95
	v_and_b32_e32 v37, 0xffff0000, v95
	v_lshlrev_b32_e32 v44, 16, v91
	v_and_b32_e32 v45, 0xffff0000, v91
	v_pk_fma_f32 v[34:35], v[28:29], v[40:41], v[48:49]
	v_pk_fma_f32 v[28:29], v[26:27], v[38:39], v[46:47]
	v_cvt_pk_bf16_f32 v26, v30, v31
	v_lshl_add_u64 v[30:31], s[54:55], 0, v[108:109]
	v_pk_fma_f32 v[32:33], v[32:33], v[36:37], v[44:45]
	v_lshl_add_u64 v[30:31], v[30:31], 0, v[198:199]
	v_cvt_pk_bf16_f32 v27, v32, v33
	v_cvt_pk_bf16_f32 v28, v28, v29
	v_cvt_pk_bf16_f32 v29, v34, v35
	global_store_dwordx4 v[30:31], v[26:29], off
	v_lshlrev_b32_e32 v32, 16, v88
	v_and_b32_e32 v33, 0xffff0000, v88
	v_lshlrev_b32_e32 v26, 16, v86
	v_and_b32_e32 v27, 0xffff0000, v86
	v_lshlrev_b32_e32 v28, 16, v87
	v_and_b32_e32 v29, 0xffff0000, v87
	v_lshlrev_b32_e32 v34, 16, v89
	v_and_b32_e32 v35, 0xffff0000, v89
	v_lshlrev_b32_e32 v36, 16, v82
	v_and_b32_e32 v37, 0xffff0000, v82
	v_lshlrev_b32_e32 v38, 16, v83
	v_and_b32_e32 v39, 0xffff0000, v83
	v_lshlrev_b32_e32 v40, 16, v84
	v_and_b32_e32 v41, 0xffff0000, v84
	v_lshlrev_b32_e32 v42, 16, v85
	v_and_b32_e32 v43, 0xffff0000, v85
	v_pk_fma_f32 v[24:25], v[24:25], v[28:29], v[38:39]
	v_pk_fma_f32 v[22:23], v[22:23], v[26:27], v[36:37]
	v_pk_fma_f32 v[26:27], v[20:21], v[34:35], v[42:43]
	v_pk_fma_f32 v[20:21], v[18:19], v[32:33], v[40:41]
	v_cvt_pk_bf16_f32 v18, v22, v23
	v_cvt_pk_bf16_f32 v19, v24, v25
	v_lshlrev_b32_e32 v22, 16, v80
	v_cvt_pk_bf16_f32 v20, v20, v21
	v_cvt_pk_bf16_f32 v21, v26, v27
	global_store_dwordx4 v[30:31], v[18:21], off offset:256
	v_lshlrev_b32_e32 v26, 16, v74
	v_and_b32_e32 v27, 0xffff0000, v74
	v_lshlrev_b32_e32 v18, 16, v78
	v_and_b32_e32 v19, 0xffff0000, v78
	v_and_b32_e32 v23, 0xffff0000, v80
	v_lshlrev_b32_e32 v24, 16, v81
	v_and_b32_e32 v25, 0xffff0000, v81
	v_lshlrev_b32_e32 v30, 16, v76
	v_and_b32_e32 v31, 0xffff0000, v76
	v_lshlrev_b32_e32 v32, 16, v77
	v_and_b32_e32 v33, 0xffff0000, v77
	v_pk_fma_f32 v[14:15], v[14:15], v[18:19], v[26:27]
	v_lshlrev_b32_e32 v20, 16, v79
	v_and_b32_e32 v21, 0xffff0000, v79
	v_lshlrev_b32_e32 v28, 16, v75
	v_and_b32_e32 v29, 0xffff0000, v75
	v_pk_fma_f32 v[18:19], v[12:13], v[24:25], v[32:33]
	v_pk_fma_f32 v[12:13], v[10:11], v[22:23], v[30:31]
	v_cvt_pk_bf16_f32 v10, v14, v15
	v_lshl_add_u64 v[14:15], s[54:55], 0, v[106:107]
	v_pk_fma_f32 v[16:17], v[16:17], v[20:21], v[28:29]
	v_lshl_add_u64 v[14:15], v[14:15], 0, v[198:199]
	v_cvt_pk_bf16_f32 v11, v16, v17
	v_cvt_pk_bf16_f32 v12, v12, v13
	v_cvt_pk_bf16_f32 v13, v18, v19
	global_store_dwordx4 v[14:15], v[10:13], off
	v_lshlrev_b32_e32 v16, 16, v72
	v_and_b32_e32 v17, 0xffff0000, v72
	v_lshlrev_b32_e32 v10, 16, v70
	v_and_b32_e32 v11, 0xffff0000, v70
	v_lshlrev_b32_e32 v18, 16, v73
	v_and_b32_e32 v19, 0xffff0000, v73
	v_lshlrev_b32_e32 v20, 16, v66
	v_and_b32_e32 v21, 0xffff0000, v66
	v_lshlrev_b32_e32 v24, 16, v68
	v_and_b32_e32 v25, 0xffff0000, v68
	v_lshlrev_b32_e32 v26, 16, v69
	v_and_b32_e32 v27, 0xffff0000, v69
	v_lshlrev_b32_e32 v12, 16, v71
	v_and_b32_e32 v13, 0xffff0000, v71
	v_lshlrev_b32_e32 v22, 16, v67
	v_and_b32_e32 v23, 0xffff0000, v67
	v_pk_fma_f32 v[6:7], v[6:7], v[10:11], v[20:21]
	v_pk_fma_f32 v[10:11], v[4:5], v[18:19], v[26:27]
	v_pk_fma_f32 v[4:5], v[2:3], v[16:17], v[24:25]
	v_pk_fma_f32 v[8:9], v[8:9], v[12:13], v[22:23]
	v_cvt_pk_bf16_f32 v2, v6, v7
	s_nop 0
	v_cvt_pk_bf16_f32 v3, v8, v9
	v_cvt_pk_bf16_f32 v4, v4, v5
	v_cvt_pk_bf16_f32 v5, v10, v11
	global_store_dwordx4 v[14:15], v[2:5], off offset:256
	s_cbranch_vccnz .LBB0_1408
	s_andn2_b64 vcc, exec, s[38:39]
	s_cbranch_vccnz .LBB0_1407
	s_barrier
	s_branch .LBB0_1407

;     __device__ __forceinline__ void operator()(const f32x4 (&acc)[2][2][4][2], const Unit& u, int wr, int wc, int fr, int fq) const {
;         const int row0 = u.pm * BM + wr * 64 + fr, col0 = u.pn * 256 + wc * 32 + 4 * fq;
; #pragma unroll
;         for (int ai = 0; ai < 2; ++ai) { f32x4 hv[4][2][2];
; #pragma unroll
;             for (int m = 0; m < 4; ++m) { const float* rowp = h + (size_t)(row0 + ai * HALF + m * 16) * 1024 + col0;
; #pragma unroll
;                 for (int bj = 0; bj < 2; ++bj)
; #pragma unroll
;                     for (int n = 0; n < 2; ++n) hv[m][bj][n] = *(const f32x4*)(rowp + bj * HALF + n * 16); }
; #pragma unroll
;             for (int m = 0; m < 4; ++m) { float* rowp = h + (size_t)(row0 + ai * HALF + m * 16) * 1024 + col0;
; #pragma unroll
;                 for (int bj = 0; bj < 2; ++bj)
; #pragma unroll
;                     for (int n = 0; n < 2; ++n) *(f32x4*)(rowp + bj * HALF + n * 16) = hv[m][bj][n] + acc[ai][bj][m][n]; } }
;     }
.LBB0_1505:
	v_lshl_or_b32 v142, s77, 8, v155
	v_lshl_add_u32 v152, s82, 8, v1
	v_ashrrev_i32_e32 v143, 31, v142
	v_lshlrev_b64 v[142:143], 2, v[142:143]
	v_ashrrev_i32_e32 v153, 31, v152
	v_lshl_add_u64 v[144:145], s[24:25], 0, v[142:143]
	v_lshlrev_b64 v[146:147], 12, v[152:153]
	v_or_b32_e32 v170, 16, v152
	v_lshl_add_u64 v[166:167], v[144:145], 0, v[146:147]
	v_ashrrev_i32_e32 v171, 31, v170
	global_load_dwordx4 v[148:151], v[166:167], off
	global_load_dwordx4 v[158:161], v[166:167], off offset:64
	global_load_dwordx4 v[162:165], v[166:167], off offset:512
	global_load_dwordx4 v[166:169], v[166:167], off offset:576
	v_lshlrev_b64 v[206:207], 12, v[170:171]
	v_or_b32_e32 v186, 32, v152
	v_lshl_add_u64 v[182:183], v[144:145], 0, v[206:207]
	v_ashrrev_i32_e32 v187, 31, v186
	global_load_dwordx4 v[170:173], v[182:183], off
	global_load_dwordx4 v[174:177], v[182:183], off offset:64
	global_load_dwordx4 v[178:181], v[182:183], off offset:512
	global_load_dwordx4 v[182:185], v[182:183], off offset:576
	v_lshlrev_b64 v[238:239], 12, v[186:187]
	v_or_b32_e32 v152, 48, v152
	v_lshl_add_u64 v[198:199], v[144:145], 0, v[238:239]
	v_ashrrev_i32_e32 v153, 31, v152
	global_load_dwordx4 v[186:189], v[198:199], off
	global_load_dwordx4 v[190:193], v[198:199], off offset:64
	global_load_dwordx4 v[194:197], v[198:199], off offset:512
	global_load_dwordx4 v[198:201], v[198:199], off offset:576
	v_lshlrev_b64 v[152:153], 12, v[152:153]
	v_lshl_add_u64 v[232:233], v[144:145], 0, v[152:153]
	global_load_dwordx4 v[202:205], v[232:233], off
	global_load_dwordx4 v[224:227], v[232:233], off offset:64
	global_load_dwordx4 v[228:231], v[232:233], off offset:512
	global_load_dwordx4 v[232:235], v[232:233], off offset:576
	v_lshl_add_u64 v[240:241], s[24:25], 0, v[146:147]
	v_lshl_add_u64 v[240:241], v[240:241], 0, v[142:143]
	s_mov_b64 s[44:45], 0x80000
	s_mov_b64 s[56:57], -1
	s_and_b64 vcc, exec, s[38:39]
	s_waitcnt vmcnt(0)
	v_pk_add_f32 v[124:125], v[124:125], v[150:151]
	v_pk_add_f32 v[122:123], v[122:123], v[148:149]
	global_store_dwordx4 v[240:241], v[122:125], off
	v_pk_add_f32 v[116:117], v[116:117], v[168:169]
	v_pk_add_f32 v[114:115], v[114:115], v[166:167]
	global_store_dwordx4 v[240:241], v[114:117], off offset:576
	v_pk_add_f32 v[124:125], v[128:129], v[160:161]
	v_pk_add_f32 v[122:123], v[126:127], v[158:159]
	v_lshl_add_u64 v[114:115], s[24:25], 0, v[206:207]
	v_lshl_add_u64 v[114:115], v[114:115], 0, v[142:143]
	v_pk_add_f32 v[100:101], v[100:101], v[184:185]
	v_pk_add_f32 v[98:99], v[98:99], v[182:183]
	global_store_dwordx4 v[114:115], v[98:101], off offset:576
	v_pk_add_f32 v[84:85], v[84:85], v[200:201]
	v_pk_add_f32 v[82:83], v[82:83], v[198:199]
	v_lshl_add_u64 v[98:99], s[24:25], 0, v[238:239]
	v_lshl_add_u64 v[98:99], v[98:99], 0, v[142:143]
	global_store_dwordx4 v[98:99], v[82:85], off offset:576
	v_pk_add_f32 v[120:121], v[120:121], v[164:165]
	v_pk_add_f32 v[118:119], v[118:119], v[162:163]
	v_lshl_add_u64 v[82:83], s[24:25], 0, v[152:153]
	v_pk_add_f32 v[112:113], v[112:113], v[172:173]
	v_pk_add_f32 v[110:111], v[110:111], v[170:171]
	v_pk_add_f32 v[108:109], v[108:109], v[176:177]
	v_pk_add_f32 v[106:107], v[106:107], v[174:175]
	v_pk_add_f32 v[104:105], v[104:105], v[180:181]
	v_pk_add_f32 v[102:103], v[102:103], v[178:179]
	v_pk_add_f32 v[96:97], v[96:97], v[188:189]
	v_pk_add_f32 v[94:95], v[94:95], v[186:187]
	v_pk_add_f32 v[92:93], v[92:93], v[192:193]
	v_pk_add_f32 v[90:91], v[90:91], v[190:191]
	v_pk_add_f32 v[88:89], v[88:89], v[196:197]
	v_pk_add_f32 v[86:87], v[86:87], v[194:195]
	v_lshl_add_u64 v[82:83], v[82:83], 0, v[142:143]
	v_pk_add_f32 v[80:81], v[80:81], v[204:205]
	v_pk_add_f32 v[78:79], v[78:79], v[202:203]
	v_pk_add_f32 v[76:77], v[76:77], v[226:227]
	v_pk_add_f32 v[74:75], v[74:75], v[224:225]
	v_pk_add_f32 v[72:73], v[72:73], v[230:231]
	v_pk_add_f32 v[70:71], v[70:71], v[228:229]
	v_pk_add_f32 v[68:69], v[68:69], v[234:235]
	v_pk_add_f32 v[66:67], v[66:67], v[232:233]
	v_lshl_add_u64 v[152:153], v[146:147], 0, s[44:45]
	global_store_dwordx4 v[240:241], v[122:125], off offset:64
	global_store_dwordx4 v[240:241], v[118:121], off offset:512
	global_store_dwordx4 v[114:115], v[110:113], off
	global_store_dwordx4 v[114:115], v[106:109], off offset:64
	global_store_dwordx4 v[114:115], v[102:105], off offset:512
	global_store_dwordx4 v[98:99], v[94:97], off
	global_store_dwordx4 v[98:99], v[90:93], off offset:64
	global_store_dwordx4 v[98:99], v[86:89], off offset:512
	global_store_dwordx4 v[82:83], v[78:81], off
	global_store_dwordx4 v[82:83], v[74:77], off offset:64
	global_store_dwordx4 v[82:83], v[70:73], off offset:512
	global_store_dwordx4 v[82:83], v[66:69], off offset:576
	s_mov_b64 s[44:45], 0x90000
	v_lshl_add_u64 v[150:151], v[146:147], 0, s[44:45]
	v_lshl_add_u64 v[66:67], v[144:145], 0, v[152:153]
	global_load_dwordx4 v[110:113], v[66:67], off
	global_load_dwordx4 v[106:109], v[66:67], off offset:64
	global_load_dwordx4 v[102:105], v[66:67], off offset:512
	global_load_dwordx4 v[94:97], v[66:67], off offset:576
	v_lshl_add_u64 v[66:67], v[144:145], 0, v[150:151]
	s_mov_b64 s[44:45], 0xa0000
	global_load_dwordx4 v[98:101], v[66:67], off
	global_load_dwordx4 v[90:93], v[66:67], off offset:64
	global_load_dwordx4 v[82:85], v[66:67], off offset:512
	global_load_dwordx4 v[74:77], v[66:67], off offset:576
	v_lshl_add_u64 v[148:149], v[146:147], 0, s[44:45]
	v_lshl_add_u64 v[66:67], v[144:145], 0, v[148:149]
	s_mov_b64 s[44:45], 0xb0000
	global_load_dwordx4 v[86:89], v[66:67], off
	global_load_dwordx4 v[78:81], v[66:67], off offset:64
	global_load_dwordx4 v[70:73], v[66:67], off offset:512
	global_load_dwordx4 v[66:69], v[66:67], off offset:576
	v_lshl_add_u64 v[146:147], v[146:147], 0, s[44:45]
	v_lshl_add_u64 v[126:127], v[144:145], 0, v[146:147]
	global_load_dwordx4 v[122:125], v[126:127], off
	global_load_dwordx4 v[118:121], v[126:127], off offset:64
	global_load_dwordx4 v[114:117], v[126:127], off offset:512
	global_load_dwordx4 v[126:129], v[126:127], off offset:576
	v_lshl_add_u64 v[144:145], s[24:25], 0, v[152:153]
	v_lshl_add_u64 v[144:145], v[144:145], 0, v[142:143]
	s_waitcnt vmcnt(0)
; #define PG8_BAR __builtin_amdgcn_s_barrier()
;     __device__ __forceinline__ void operator()(const f32x4 (&acc)[2][2][4][2], const Unit& u, int wr, int wc, int fr, int fq) const {
;     ...
;             for (int m = 0; m < 4; ++m) { float* rowp = h + (size_t)(row0 + ai * HALF + m * 16) * 1024 + col0;
; #pragma unroll
;                 for (int bj = 0; bj < 2; ++bj)
; #pragma unroll
;                     for (int n = 0; n < 2; ++n) *(f32x4*)(rowp + bj * HALF + n * 16) = hv[m][bj][n] + acc[ai][bj][m][n]; } }
;     }
; template <class Epi, class Sched, bool ALIGN_EPI = false, bool SP2 = false>
; __device__ __forceinline__ void gemm_phase(PG8_LAS unsigned char* lds, const Gemm g, const Sched& S, const Epi& E, const int wave0) {
;     ...
;         if constexpr (ALIGN_EPI) { if (wr == 0) PG8_BAR; }
;         if constexpr (!Epi::AFTER_DRAIN) { E(acc, cur, wr, wc, fr, fq); S.done(cur); }
;         if (!has_next) break;
; #pragma unroll
;         for (int a = 0; a < 2; ++a)
; #pragma unroll
;             for (int b = 0; b < 2; ++b)
; #pragma unroll
;                 for (int m = 0; m < 4; ++m)
; #pragma unroll
;                     for (int n = 0; n < 2; ++n) acc[a][b][m][n] = (f32x4){0.f, 0.f, 0.f, 0.f};
;         cur = nxt; cA = nA; cB = nB; ++ui;
;         if constexpr (ALIGN_EPI) { if (wr == 1) PG8_BAR; }
	v_pk_add_f32 v[64:65], v[64:65], v[112:113]
	v_pk_add_f32 v[62:63], v[62:63], v[110:111]
	v_pk_add_f32 v[60:61], v[60:61], v[108:109]
	v_pk_add_f32 v[52:53], v[52:53], v[96:97]
	v_pk_add_f32 v[50:51], v[50:51], v[94:95]
	global_store_dwordx4 v[144:145], v[50:53], off offset:576
	v_pk_add_f32 v[36:37], v[36:37], v[76:77]
	v_pk_add_f32 v[34:35], v[34:35], v[74:75]
	v_lshl_add_u64 v[50:51], s[24:25], 0, v[150:151]
	v_lshl_add_u64 v[50:51], v[50:51], 0, v[142:143]
	global_store_dwordx4 v[50:51], v[34:37], off offset:576
	v_pk_add_f32 v[20:21], v[20:21], v[68:69]
	v_pk_add_f32 v[18:19], v[18:19], v[66:67]
	v_lshl_add_u64 v[34:35], s[24:25], 0, v[148:149]
	v_lshl_add_u64 v[34:35], v[34:35], 0, v[142:143]
	global_store_dwordx4 v[34:35], v[18:21], off offset:576
	v_pk_add_f32 v[58:59], v[58:59], v[106:107]
	v_pk_add_f32 v[56:57], v[56:57], v[104:105]
	v_lshl_add_u64 v[18:19], s[24:25], 0, v[146:147]
	v_pk_add_f32 v[54:55], v[54:55], v[102:103]
	v_pk_add_f32 v[48:49], v[48:49], v[100:101]
	v_pk_add_f32 v[46:47], v[46:47], v[98:99]
	v_pk_add_f32 v[44:45], v[44:45], v[92:93]
	v_pk_add_f32 v[42:43], v[42:43], v[90:91]
	v_pk_add_f32 v[40:41], v[40:41], v[84:85]
	v_pk_add_f32 v[38:39], v[38:39], v[82:83]
	v_pk_add_f32 v[32:33], v[32:33], v[88:89]
	v_pk_add_f32 v[30:31], v[30:31], v[86:87]
	v_pk_add_f32 v[28:29], v[28:29], v[80:81]
	v_pk_add_f32 v[26:27], v[26:27], v[78:79]
	v_pk_add_f32 v[24:25], v[24:25], v[72:73]
	v_pk_add_f32 v[22:23], v[22:23], v[70:71]
	v_lshl_add_u64 v[18:19], v[18:19], 0, v[142:143]
	v_pk_add_f32 v[16:17], v[16:17], v[124:125]
	v_pk_add_f32 v[14:15], v[14:15], v[122:123]
	v_pk_add_f32 v[12:13], v[12:13], v[120:121]
	v_pk_add_f32 v[10:11], v[10:11], v[118:119]
	v_pk_add_f32 v[8:9], v[8:9], v[116:117]
	v_pk_add_f32 v[6:7], v[6:7], v[114:115]
	v_pk_add_f32 v[4:5], v[4:5], v[128:129]
	v_pk_add_f32 v[2:3], v[2:3], v[126:127]
	global_store_dwordx4 v[144:145], v[62:65], off
	global_store_dwordx4 v[144:145], v[58:61], off offset:64
	global_store_dwordx4 v[144:145], v[54:57], off offset:512
	global_store_dwordx4 v[50:51], v[46:49], off
	global_store_dwordx4 v[50:51], v[42:45], off offset:64
	global_store_dwordx4 v[50:51], v[38:41], off offset:512
	global_store_dwordx4 v[34:35], v[30:33], off
	global_store_dwordx4 v[34:35], v[26:29], off offset:64
	global_store_dwordx4 v[34:35], v[22:25], off offset:512
	global_store_dwordx4 v[18:19], v[14:17], off
	global_store_dwordx4 v[18:19], v[10:13], off offset:64
	global_store_dwordx4 v[18:19], v[6:9], off offset:512
	global_store_dwordx4 v[18:19], v[2:5], off offset:576
	s_cbranch_vccnz .LBB0_1488
	s_andn2_b64 vcc, exec, s[42:43]
	s_cbranch_vccnz .LBB0_1487
	s_barrier
	s_branch .LBB0_1487

; __device__ __forceinline__ void norm_row_n2x2(const float* hrow0, const float* hrow1, const float* g, bf16* o0, bf16* o1, unsigned char* e0, unsigned char* e1, int lane) {
;     const f32x4* x0 = (const f32x4*)hrow0 + lane; const f32x4* x1 = (const f32x4*)hrow1 + lane; f32x4 v[2][4]; float s0 = 0.f, s1 = 0.f;
; #pragma unroll
;     for (int j = 0; j < 4; ++j) { v[0][j] = x0[64 * j]; v[1][j] = x1[64 * j]; }
; #pragma unroll
;     for (int j = 0; j < 4; ++j) { s0 += (v[0][j].x * v[0][j].x + v[0][j].y * v[0][j].y) + (v[0][j].z * v[0][j].z + v[0][j].w * v[0][j].w);
;                                   s1 += (v[1][j].x * v[1][j].x + v[1][j].y * v[1][j].y) + (v[1][j].z * v[1][j].z + v[1][j].w * v[1][j].w); }
;     const float r0 = 1.f / sqrtf(wave_sum(s0) * (1.f / D) + 1e-6f), r1 = 1.f / sqrtf(wave_sum(s1) * (1.f / D) + 1e-6f);
.LBB0_1565:
	v_lshl_add_u64 v[2:3], s[2:3], 0, v[34:35]
	v_lshl_add_u64 v[4:5], s[6:7], 0, v[34:35]
	global_load_dwordx4 v[30:33], v[2:3], off
	global_load_dwordx4 v[26:29], v[4:5], off
	global_load_dwordx4 v[22:25], v[2:3], off offset:1024
	global_load_dwordx4 v[18:21], v[4:5], off offset:1024
	global_load_dwordx4 v[14:17], v[2:3], off offset:2048
	global_load_dwordx4 v[10:13], v[4:5], off offset:2048
	global_load_dwordx4 v[6:9], v[2:3], off offset:3072
	global_load_dwordx4 v[2:5], v[4:5], off offset:3072
	s_add_i32 s5, s5, s82
	s_add_u32 s6, s6, s22
	s_addc_u32 s7, s7, s23
	s_add_u32 s2, s2, s22
	s_addc_u32 s3, s3, s23
	s_cmpk_gt_i32 s5, 0x3fff
	s_waitcnt vmcnt(7)
	v_mul_f32_e32 v1, v31, v31
	v_mul_f32_e32 v70, v33, v33
	v_fmac_f32_e32 v1, v30, v30
	v_fmac_f32_e32 v70, v32, v32
	v_add_f32_e32 v1, v1, v70
	s_waitcnt vmcnt(6)
	v_mul_f32_e32 v70, v27, v27
	v_mul_f32_e32 v71, v29, v29
	v_fmac_f32_e32 v70, v26, v26
	v_fmac_f32_e32 v71, v28, v28
	v_add_f32_e32 v70, v70, v71
	s_waitcnt vmcnt(5)
	v_mul_f32_e32 v71, v23, v23
	v_mul_f32_e32 v72, v25, v25
	v_fmac_f32_e32 v71, v22, v22
	v_fmac_f32_e32 v72, v24, v24
	v_add_f32_e32 v71, v71, v72
	v_add_f32_e32 v1, v1, v71
	s_waitcnt vmcnt(4)
	v_mul_f32_e32 v71, v19, v19
	v_mul_f32_e32 v72, v21, v21
	v_fmac_f32_e32 v71, v18, v18
	v_fmac_f32_e32 v72, v20, v20
	v_add_f32_e32 v71, v71, v72
	v_add_f32_e32 v70, v70, v71
	s_waitcnt vmcnt(3)
	v_mul_f32_e32 v71, v15, v15
	v_mul_f32_e32 v72, v17, v17
	v_fmac_f32_e32 v71, v14, v14
	v_fmac_f32_e32 v72, v16, v16
	v_add_f32_e32 v71, v71, v72
	v_add_f32_e32 v1, v1, v71
	s_waitcnt vmcnt(2)
	v_mul_f32_e32 v71, v11, v11
	v_mul_f32_e32 v72, v13, v13
	v_fmac_f32_e32 v71, v10, v10
	v_fmac_f32_e32 v72, v12, v12
	v_add_f32_e32 v71, v71, v72
	v_add_f32_e32 v70, v70, v71
	s_waitcnt vmcnt(1)
	v_mul_f32_e32 v71, v7, v7
	v_mul_f32_e32 v72, v9, v9
	v_fmac_f32_e32 v71, v6, v6
	v_fmac_f32_e32 v72, v8, v8
	v_add_f32_e32 v71, v71, v72
	v_add_f32_e32 v1, v1, v71
	s_waitcnt vmcnt(0)
	v_mul_f32_e32 v71, v3, v3
	v_mul_f32_e32 v72, v5, v5
	v_add_f32_dpp v1, v1, v1 quad_perm:[1,0,3,2] row_mask:0xf bank_mask:0xf bound_ctrl:1
	v_fmac_f32_e32 v71, v2, v2
	v_fmac_f32_e32 v72, v4, v4
	v_add_f32_dpp v1, v1, v1 quad_perm:[2,3,0,1] row_mask:0xf bank_mask:0xf bound_ctrl:1
	v_add_f32_e32 v71, v71, v72
	v_add_f32_e32 v71, v70, v71
	v_add_f32_dpp v1, v1, v1 row_half_mirror row_mask:0xf bank_mask:0xf bound_ctrl:1
	s_nop 1
	v_add_f32_dpp v1, v1, v1 row_mirror row_mask:0xf bank_mask:0xf bound_ctrl:1
	v_mov_b32_e32 v70, v1
	s_nop 1
	v_permlane16_swap_b32_e32 v1, v70
	v_add_f32_e32 v1, v1, v70
	v_mov_b32_e32 v70, v1
	s_nop 1
	v_permlane32_swap_b32_e32 v1, v70
	v_add_f32_e32 v1, v1, v70
	v_fmamk_f32 v1, v1, 0x3a800000, v244
	v_cmp_gt_f32_e32 vcc, s69, v1
	v_mul_f32_e32 v70, 0x4f800000, v1
	s_nop 0
	v_cndmask_b32_e32 v1, v1, v70, vcc
	v_sqrt_f32_e32 v70, v1
	s_nop 0
	v_add_u32_e32 v72, -1, v70
	v_fma_f32 v73, -v72, v70, v1
	v_cmp_ge_f32_e64 s[38:39], 0, v73
	v_add_u32_e32 v73, 1, v70
	s_nop 0
	v_cndmask_b32_e64 v72, v70, v72, s[38:39]
	v_fma_f32 v70, -v73, v70, v1
	v_cmp_lt_f32_e64 s[38:39], 0, v70
	s_nop 1
	v_cndmask_b32_e64 v70, v72, v73, s[38:39]
	v_mul_f32_e32 v72, 0x37800000, v70
	v_cndmask_b32_e32 v70, v70, v72, vcc
	v_cmp_class_f32_e32 vcc, v1, v242
	s_nop 1
	v_cndmask_b32_e32 v1, v70, v1, vcc
	v_div_scale_f32 v70, s[20:21], v1, v1, 1.0
	v_rcp_f32_e32 v72, v70
	s_nop 0
	v_fma_f32 v73, -v70, v72, 1.0
	v_fmac_f32_e32 v72, v73, v72
	v_div_scale_f32 v73, vcc, 1.0, v1, 1.0
	v_mul_f32_e32 v74, v73, v72
	v_fma_f32 v75, -v70, v74, v73
	v_fmac_f32_e32 v74, v75, v72
	v_fma_f32 v70, -v70, v74, v73
	v_div_fmas_f32 v70, v70, v72, v74
	v_div_fixup_f32 v70, v70, v1, 1.0
	v_add_f32_dpp v1, v71, v71 quad_perm:[1,0,3,2] row_mask:0xf bank_mask:0xf bound_ctrl:1
	s_nop 1
	v_add_f32_dpp v1, v1, v1 quad_perm:[2,3,0,1] row_mask:0xf bank_mask:0xf bound_ctrl:1
	s_nop 1
	v_add_f32_dpp v1, v1, v1 row_half_mirror row_mask:0xf bank_mask:0xf bound_ctrl:1
	s_nop 1
	v_add_f32_dpp v1, v1, v1 row_mirror row_mask:0xf bank_mask:0xf bound_ctrl:1
	v_mov_b32_e32 v71, v1
	s_nop 1
	v_permlane16_swap_b32_e32 v1, v71
	v_add_f32_e32 v1, v1, v71
	v_mov_b32_e32 v71, v1
	s_nop 1
	v_permlane32_swap_b32_e32 v1, v71
	v_add_f32_e32 v1, v1, v71
	v_fmamk_f32 v1, v1, 0x3a800000, v244
	v_cmp_gt_f32_e32 vcc, s69, v1
	v_mul_f32_e32 v71, 0x4f800000, v1
	s_nop 0
	v_cndmask_b32_e32 v1, v1, v71, vcc
	v_sqrt_f32_e32 v71, v1
	s_nop 0
	v_add_u32_e32 v72, -1, v71
	v_fma_f32 v73, -v72, v71, v1
	v_cmp_ge_f32_e64 s[38:39], 0, v73
	v_add_u32_e32 v73, 1, v71
	s_nop 0
	v_cndmask_b32_e64 v72, v71, v72, s[38:39]
	v_fma_f32 v71, -v73, v71, v1
	v_cmp_lt_f32_e64 s[38:39], 0, v71
	s_nop 1
	v_cndmask_b32_e64 v71, v72, v73, s[38:39]
	v_mul_f32_e32 v72, 0x37800000, v71
	v_cndmask_b32_e32 v71, v71, v72, vcc
	v_cmp_class_f32_e32 vcc, v1, v242
	s_nop 1
	v_cndmask_b32_e32 v1, v71, v1, vcc
	v_div_scale_f32 v71, s[20:21], v1, v1, 1.0
	v_rcp_f32_e32 v72, v71
	s_nop 0
	v_fma_f32 v73, -v71, v72, 1.0
	v_fmac_f32_e32 v72, v73, v72
	v_div_scale_f32 v73, vcc, 1.0, v1, 1.0
	v_mul_f32_e32 v74, v73, v72
	v_fma_f32 v75, -v71, v74, v73
	v_fmac_f32_e32 v74, v75, v72
	v_fma_f32 v71, -v71, v74, v73
	v_div_fmas_f32 v71, v71, v72, v74
	v_mov_b64_e32 v[74:75], v[100:101]
	v_mov_b64_e32 v[76:77], v[102:103]
	v_div_fixup_f32 v72, v71, v1, 1.0
	v_pk_mul_f32 v[30:31], v[30:31], v[70:71] op_sel_hi:[1,0]
	v_pk_mul_f32 v[32:33], v[32:33], v[70:71] op_sel_hi:[1,0]
	v_pk_mul_f32 v[26:27], v[26:27], v[72:73] op_sel_hi:[1,0]
	v_pk_mul_f32 v[28:29], v[28:29], v[72:73] op_sel_hi:[1,0]
	v_mov_b32_e32 v71, v0
	v_mov_b32_e32 v1, v0
	v_pk_mul_f32 v[18:19], v[18:19], v[72:73] op_sel_hi:[1,0]
; __device__ __forceinline__ unsigned cvt_pk_bf16(float lo, float hi) { unsigned r; asm volatile("v_cvt_pk_bf16_f32 %0, %1, %2" : "=v"(r) : "v"(lo), "v"(hi)); return r; }
; __device__ __forceinline__ void norm_row_n2x2(const float* hrow0, const float* hrow1, const float* g, bf16* o0, bf16* o1, unsigned char* e0, unsigned char* e1, int lane) {
;     ...
;     for (int j = 0; j < 4; ++j) { const f32x4 gv = ((const f32x4*)g)[lane + 64 * j]; const f32x4 a = v[0][j] * r0 * gv, b = v[1][j] * r1 * gv;
;         *(v2u*)(o0 + 4 * (lane + 64 * j)) = (v2u){cvt_pk_bf16(a.x, a.y), cvt_pk_bf16(a.z, a.w)}; *(v2u*)(o1 + 4 * (lane + 64 * j)) = (v2u){cvt_pk_bf16(b.x, b.y), cvt_pk_bf16(b.z, b.w)};
;         { const f32x4 a8 = a * 16.f, b8 = b * 16.f; int wa = 0, wb = 0;
;           wa = __builtin_amdgcn_cvt_pk_fp8_f32(a8.x, a8.y, wa, false); wa = __builtin_amdgcn_cvt_pk_fp8_f32(a8.z, a8.w, wa, true); wb = __builtin_amdgcn_cvt_pk_fp8_f32(b8.x, b8.y, wb, false); wb = __builtin_amdgcn_cvt_pk_fp8_f32(b8.z, b8.w, wb, true);
;           *(unsigned*)(e0 + 4 * (lane + 64 * j)) = (unsigned)wa; *(unsigned*)(e1 + 4 * (lane + 64 * j)) = (unsigned)wb; } }
	v_pk_mul_f32 v[20:21], v[20:21], v[72:73] op_sel_hi:[1,0]
	v_pk_mul_f32 v[10:11], v[10:11], v[72:73] op_sel_hi:[1,0]
	v_pk_mul_f32 v[12:13], v[12:13], v[72:73] op_sel_hi:[1,0]
	v_pk_mul_f32 v[2:3], v[2:3], v[72:73] op_sel_hi:[1,0]
	v_pk_mul_f32 v[4:5], v[4:5], v[72:73] op_sel_hi:[1,0]
	v_pk_mul_f32 v[30:31], v[74:75], v[30:31]
	v_pk_mul_f32 v[32:33], v[76:77], v[32:33]
	v_pk_mul_f32 v[28:29], v[76:77], v[28:29]
	v_pk_mul_f32 v[26:27], v[74:75], v[26:27]
	v_cvt_pk_bf16_f32 v74, v30, v31
	v_lshl_add_u64 v[76:77], s[0:1], 0, v[58:59]
	v_pk_mul_f32 v[30:31], v[30:31], s[10:11] op_sel_hi:[1,0]
	v_cvt_pk_bf16_f32 v75, v32, v33
	global_store_dwordx2 v[76:77], v[74:75], off
	v_cvt_pk_bf16_f32 v74, v26, v27
	v_pk_mul_f32 v[26:27], v[26:27], s[10:11] op_sel_hi:[1,0]
	v_cvt_pk_fp8_f32 v71, v30, v31
	v_cvt_pk_fp8_f32 v1, v26, v27
	v_pk_mul_f32 v[32:33], v[32:33], s[10:11] op_sel_hi:[1,0]
	v_cvt_pk_bf16_f32 v75, v28, v29
	v_pk_mul_f32 v[28:29], v[28:29], s[10:11] op_sel_hi:[1,0]
	v_cvt_pk_fp8_f32 v71, v32, v33 op_sel:[0,0,1]
	v_cvt_pk_fp8_f32 v1, v28, v29 op_sel:[0,0,1]
	v_lshl_add_u64 v[76:77], s[0:1], 0, v[40:41]
	v_lshl_add_u64 v[26:27], s[0:1], 0, v[66:67]
	global_store_dwordx2 v[76:77], v[74:75], off
	global_store_dword v[26:27], v71, off
	v_lshl_add_u64 v[26:27], s[0:1], 0, v[48:49]
	global_store_dword v[26:27], v1, off
	v_mov_b64_e32 v[26:27], v[104:105]
	v_mov_b64_e32 v[28:29], v[106:107]
	v_pk_mul_f32 v[22:23], v[22:23], v[70:71] op_sel_hi:[1,0]
	v_pk_mul_f32 v[24:25], v[24:25], v[70:71] op_sel_hi:[1,0]
	v_mov_b32_e32 v1, v0
	v_pk_mul_f32 v[14:15], v[14:15], v[70:71] op_sel_hi:[1,0]
	v_pk_mul_f32 v[16:17], v[16:17], v[70:71] op_sel_hi:[1,0]
	v_pk_mul_f32 v[6:7], v[6:7], v[70:71] op_sel_hi:[1,0]
	v_pk_mul_f32 v[8:9], v[8:9], v[70:71] op_sel_hi:[1,0]
	v_lshl_add_u64 v[40:41], v[40:41], 0, s[54:55]
	v_lshl_add_u64 v[48:49], v[48:49], 0, s[96:97]
	v_lshl_add_u64 v[58:59], v[58:59], 0, s[54:55]
	v_lshl_add_u64 v[66:67], v[66:67], 0, s[96:97]
	v_pk_mul_f32 v[22:23], v[22:23], v[26:27]
	v_pk_mul_f32 v[24:25], v[24:25], v[28:29]
	v_pk_mul_f32 v[20:21], v[20:21], v[28:29]
	v_pk_mul_f32 v[18:19], v[18:19], v[26:27]
	v_cvt_pk_bf16_f32 v26, v22, v23
	v_lshl_add_u64 v[28:29], s[0:1], 0, v[60:61]
	v_pk_mul_f32 v[22:23], v[22:23], s[10:11] op_sel_hi:[1,0]
	v_cvt_pk_bf16_f32 v27, v24, v25
	global_store_dwordx2 v[28:29], v[26:27], off
	v_cvt_pk_bf16_f32 v26, v18, v19
	v_pk_mul_f32 v[18:19], v[18:19], s[10:11] op_sel_hi:[1,0]
	v_cvt_pk_fp8_f32 v1, v22, v23
	v_mov_b32_e32 v22, v0
	v_cvt_pk_fp8_f32 v22, v18, v19
	v_pk_mul_f32 v[24:25], v[24:25], s[10:11] op_sel_hi:[1,0]
	v_cvt_pk_bf16_f32 v27, v20, v21
	v_pk_mul_f32 v[20:21], v[20:21], s[10:11] op_sel_hi:[1,0]
	v_cvt_pk_fp8_f32 v1, v24, v25 op_sel:[0,0,1]
	v_cvt_pk_fp8_f32 v22, v20, v21 op_sel:[0,0,1]
	v_lshl_add_u64 v[28:29], s[0:1], 0, v[42:43]
	v_lshl_add_u64 v[18:19], s[0:1], 0, v[68:69]
	global_store_dwordx2 v[28:29], v[26:27], off
	global_store_dword v[18:19], v1, off
	v_lshl_add_u64 v[18:19], s[0:1], 0, v[50:51]
	global_store_dword v[18:19], v22, off
	v_mov_b64_e32 v[18:19], v[108:109]
	v_mov_b64_e32 v[20:21], v[110:111]
	v_mov_b32_e32 v1, v0
	v_lshl_add_u64 v[42:43], v[42:43], 0, s[54:55]
	v_lshl_add_u64 v[50:51], v[50:51], 0, s[96:97]
	v_lshl_add_u64 v[60:61], v[60:61], 0, s[54:55]
	v_lshl_add_u64 v[68:69], v[68:69], 0, s[96:97]
	v_pk_mul_f32 v[14:15], v[14:15], v[18:19]
	v_pk_mul_f32 v[16:17], v[16:17], v[20:21]
	v_pk_mul_f32 v[12:13], v[12:13], v[20:21]
	v_pk_mul_f32 v[10:11], v[10:11], v[18:19]
	v_cvt_pk_bf16_f32 v18, v14, v15
	v_lshl_add_u64 v[20:21], s[0:1], 0, v[62:63]
	v_pk_mul_f32 v[14:15], v[14:15], s[10:11] op_sel_hi:[1,0]
	v_cvt_pk_bf16_f32 v19, v16, v17
	global_store_dwordx2 v[20:21], v[18:19], off
	v_cvt_pk_bf16_f32 v18, v10, v11
	v_pk_mul_f32 v[10:11], v[10:11], s[10:11] op_sel_hi:[1,0]
	v_cvt_pk_fp8_f32 v1, v14, v15
	v_mov_b32_e32 v14, v0
	v_cvt_pk_fp8_f32 v14, v10, v11
	v_pk_mul_f32 v[16:17], v[16:17], s[10:11] op_sel_hi:[1,0]
	v_cvt_pk_bf16_f32 v19, v12, v13
	v_pk_mul_f32 v[12:13], v[12:13], s[10:11] op_sel_hi:[1,0]
	v_cvt_pk_fp8_f32 v1, v16, v17 op_sel:[0,0,1]
	v_cvt_pk_fp8_f32 v14, v12, v13 op_sel:[0,0,1]
	v_lshl_add_u64 v[20:21], s[0:1], 0, v[44:45]
	v_lshl_add_u64 v[10:11], s[0:1], 0, v[56:57]
	global_store_dwordx2 v[20:21], v[18:19], off
	global_store_dword v[10:11], v1, off
	v_lshl_add_u64 v[10:11], s[0:1], 0, v[52:53]
	global_store_dword v[10:11], v14, off
	v_mov_b64_e32 v[10:11], v[112:113]
	v_mov_b64_e32 v[12:13], v[114:115]
	v_mov_b32_e32 v1, v0
	v_lshl_add_u64 v[44:45], v[44:45], 0, s[54:55]
	v_lshl_add_u64 v[52:53], v[52:53], 0, s[96:97]
	v_lshl_add_u64 v[56:57], v[56:57], 0, s[96:97]
	v_lshl_add_u64 v[62:63], v[62:63], 0, s[54:55]
	v_pk_mul_f32 v[6:7], v[6:7], v[10:11]
	v_pk_mul_f32 v[8:9], v[8:9], v[12:13]
	v_pk_mul_f32 v[4:5], v[4:5], v[12:13]
	v_pk_mul_f32 v[2:3], v[2:3], v[10:11]
	v_cvt_pk_bf16_f32 v10, v6, v7
	v_lshl_add_u64 v[12:13], s[0:1], 0, v[64:65]
	v_pk_mul_f32 v[6:7], v[6:7], s[10:11] op_sel_hi:[1,0]
	v_cvt_pk_bf16_f32 v11, v8, v9
	global_store_dwordx2 v[12:13], v[10:11], off
	v_cvt_pk_bf16_f32 v10, v2, v3
	v_pk_mul_f32 v[2:3], v[2:3], s[10:11] op_sel_hi:[1,0]
	v_cvt_pk_fp8_f32 v1, v6, v7
	v_mov_b32_e32 v6, v0
	v_cvt_pk_fp8_f32 v6, v2, v3
	v_pk_mul_f32 v[8:9], v[8:9], s[10:11] op_sel_hi:[1,0]
	v_cvt_pk_bf16_f32 v11, v4, v5
	v_pk_mul_f32 v[4:5], v[4:5], s[10:11] op_sel_hi:[1,0]
	v_cvt_pk_fp8_f32 v1, v8, v9 op_sel:[0,0,1]
	v_cvt_pk_fp8_f32 v6, v4, v5 op_sel:[0,0,1]
	v_lshl_add_u64 v[12:13], s[0:1], 0, v[46:47]
	v_lshl_add_u64 v[2:3], s[0:1], 0, v[38:39]
	global_store_dwordx2 v[12:13], v[10:11], off
	global_store_dword v[2:3], v1, off
	v_lshl_add_u64 v[2:3], s[0:1], 0, v[54:55]
	v_lshl_add_u64 v[38:39], v[38:39], 0, s[96:97]
	v_lshl_add_u64 v[46:47], v[46:47], 0, s[54:55]
	v_lshl_add_u64 v[54:55], v[54:55], 0, s[96:97]
	v_lshl_add_u64 v[64:65], v[64:65], 0, s[54:55]
	global_store_dword v[2:3], v6, off
	s_cbranch_scc0 .LBB0_1565

; #define LAS __attribute__((address_space(3)))
; #define K_FETCH(J) do { _Pragma("unroll") for (int _i = 0; _i < 4; ++_i) { const int _pc = tid + 512 * _i, _rr = _pc >> 4, _c16 = _pc & 15; ktn[_i] = *(const v4u*)(KEYS + (size_t)(J) * 16384 + _rr * 128 + _c16 * 8); } \
;         _Pragma("unroll") for (int _kk = 0; _kk < 4; ++_kk) qfn[_kk] = *(const bf16x8*)(Q + trow * 2048 + (J) * 128 + 32 * _kk + 8 * fq); } while (0)
; #define K_STORE(J) do { _Pragma("unroll") for (int _i = 0; _i < 4; ++_i) { const int _pc = tid + 512 * _i, _rr = _pc >> 4, _c16 = _pc & 15; *(LAS v4u*)(sKey + ((J) & 1) * 128 * TP + _rr * TP + _c16 * 8) = ktn[_i]; } } while (0)
; __device__ __forceinline__ void peer_unit(Frame& F, const Args& a, int layer, int unit, bool last) {
;     ...
;     LAS bf16* sKey = (LAS bf16*)F.lds;
;     LAS unsigned* sLT = (LAS unsigned*)(F.lds + 2 * 128 * TP * 2) + wave * 512;
;     const bf16* Q = (const bf16*)(F.ws + WS_Q); const bf16* KEYS = (const bf16*)(F.ws + WS_DB + (size_t)(layer & 1) * DB_SET + DB_KEYS); v2u* SEL = (v2u*)(F.ws + WS_SEL);
;     const size_t trow = t0 + wave * 16 + fr;
;     constexpr float KOFF = 32.f;
;     v4u ktn[4]; bf16x8 qfn[4];
;     ...
;     for (int krep = 0; krep < REP_K; ++krep) {
;     __syncthreads();
;     K_FETCH(0); K_STORE(0);
;     bf16x8 qf[4];
; #pragma unroll
;     for (int kk = 0; kk < 4; ++kk) qf[kk] = qfn[kk];
;     __syncthreads();
.LBB0_1703:
	s_ashr_i32 s3, s2, 31
	s_lshl_b64 s[0:1], s[2:3], 7
	s_waitcnt vmcnt(14)
	v_mbcnt_lo_u32_b32 v74, -1, 0
	v_mbcnt_hi_u32_b32 v74, -1, v74
	s_add_u32 s6, s18, s76
	s_addc_u32 s7, s19, 0
	v_add_u32_e32 v38, s27, v74
	s_add_u32 s0, s0, s74
	v_lshlrev_b32_e32 v1, 3, v38
	s_waitcnt vmcnt(0)
	v_and_b32_e32 v150, 15, v74
	s_addc_u32 s1, s1, 0
	v_lshlrev_b32_e32 v2, 4, v38
	v_and_b32_e32 v52, 0xffffff80, v1
	v_ashrrev_i32_e32 v1, 4, v74
	v_or_b32_e32 v36, s0, v150
	v_mov_b32_e32 v37, s1
	v_and_b32_e32 v34, 0xf0, v2
	v_mov_b32_e32 v35, v0
	v_lshlrev_b64 v[18:19], 12, v[36:37]
	v_lshlrev_b32_e32 v20, 3, v1
	v_lshl_add_u64 v[2:3], s[6:7], 0, v[34:35]
	s_mov_b64 s[6:7], 0x3400000
	v_ashrrev_i32_e32 v21, 31, v20
	v_lshl_add_u64 v[18:19], s[18:19], 0, v[18:19]
	v_lshl_add_u64 v[50:51], v[2:3], 0, s[6:7]
	v_add_u32_e32 v54, 0x1000, v52
	v_add_u32_e32 v56, 0x2000, v52
	v_add_u32_e32 v58, 0x3000, v52
	v_lshl_add_u64 v[18:19], v[20:21], 1, v[18:19]
	s_mov_b64 s[6:7], 0x1a400000
	s_mov_b32 s3, 0x1a400000
	v_ashrrev_i32_e32 v53, 31, v52
	v_ashrrev_i32_e32 v55, 31, v54
	v_ashrrev_i32_e32 v57, 31, v56
	v_ashrrev_i32_e32 v59, 31, v58
	v_lshl_add_u64 v[60:61], v[18:19], 0, s[6:7]
	v_add_co_u32_e32 v18, vcc, s3, v18
	v_lshl_add_u64 v[2:3], v[52:53], 1, v[50:51]
	v_lshl_add_u64 v[6:7], v[54:55], 1, v[50:51]
	v_lshl_add_u64 v[10:11], v[56:57], 1, v[50:51]
	v_lshl_add_u64 v[14:15], v[58:59], 1, v[50:51]
	v_addc_co_u32_e32 v19, vcc, 0, v19, vcc
	s_barrier
	global_load_dwordx4 v[2:5], v[2:3], off
	global_load_dwordx4 v[6:9], v[6:7], off
	global_load_dwordx4 v[10:13], v[10:11], off
	v_and_b32_e32 v35, 32, v74
	global_load_dwordx4 v[14:17], v[14:15], off
	global_load_dwordx4 v[18:21], v[18:19], off
	global_load_dwordx4 v[22:25], v[60:61], off offset:64
	global_load_dwordx4 v[26:29], v[60:61], off offset:128
	global_load_dwordx4 v[30:33], v[60:61], off offset:192
	v_and_b32_e32 v40, 16, v74
	v_cmp_eq_u32_e64 s[38:39], 0, v35
	v_cmp_eq_u32_e64 s[40:41], 0, v40
	v_lshrrev_b32_e32 v35, 4, v38
	v_add_u32_e32 v40, 0x200, v38
	v_add_u32_e32 v41, 0x400, v38
	v_add_u32_e32 v38, 0x600, v38
	s_movk_i32 s5, 0x110
	v_mul_lo_u32 v77, v35, s5
	v_lshrrev_b32_e32 v35, 4, v40
	v_lshrrev_b32_e32 v40, 4, v41
	v_lshrrev_b32_e32 v38, 4, v38
	v_add_u32_e32 v78, 0, v34
	v_mul_lo_u32 v79, v35, s5
	v_mul_lo_u32 v80, v40, s5
	v_mul_lo_u32 v81, v38, s5
	s_add_u32 s44, s18, 0x22400000
	v_and_b32_e32 v39, -16, v74
	v_mul_u32_u24_e32 v42, 0x110, v150
	v_add_u32_e32 v38, v78, v77
	v_add_u32_e32 v40, v78, v79
	v_add_u32_e32 v41, v78, v80
	v_add_u32_e32 v43, v78, v81
	v_lshlrev_b64 v[34:35], 10, v[36:37]
	s_addc_u32 s45, s19, 0
	v_lshlrev_b32_e32 v76, 2, v1
	v_lshl_add_u64 v[62:63], s[44:45], 0, v[34:35]
	v_add3_u32 v113, 0, v39, v42
	s_mov_b32 s3, 0
	v_lshl_add_u32 v75, v150, 7, s33
	v_add_u32_e32 v82, 16, v76
	v_add_u32_e32 v83, 32, v76
	v_add_u32_e32 v84, 48, v76
	v_add_u32_e32 v85, 64, v76
	v_add_u32_e32 v86, 0x50, v76
	s_waitcnt vmcnt(7)
	ds_write_b128 v38, v[2:5]
	s_waitcnt vmcnt(6)
	ds_write_b128 v40, v[6:9]
	s_waitcnt vmcnt(5)
	ds_write_b128 v41, v[10:13]
	s_waitcnt vmcnt(4)
	ds_write_b128 v43, v[14:17]
	s_waitcnt vmcnt(3)
	v_mov_b64_e32 v[36:37], v[20:21]
	s_waitcnt vmcnt(2)
	v_mov_b64_e32 v[40:41], v[24:25]
	s_waitcnt vmcnt(1)
	v_mov_b64_e32 v[44:45], v[28:29]
	s_waitcnt vmcnt(0)
	v_mov_b64_e32 v[48:49], v[32:33]
	v_add_u32_e32 v87, 0x60, v76
	v_add_u32_e32 v88, 0x70, v76
	v_cmp_gt_u32_e64 s[42:43], 16, v74
	v_or_b32_e32 v89, 1, v76
	v_or_b32_e32 v90, 2, v76
	v_or_b32_e32 v91, 3, v76
	v_add_u32_e32 v92, 17, v76
	v_add_u32_e32 v93, 18, v76
	v_add_u32_e32 v94, 19, v76
	v_add_u32_e32 v95, 33, v76
	v_add_u32_e32 v96, 34, v76
	v_add_u32_e32 v97, 35, v76
	v_add_u32_e32 v98, 49, v76
	v_add_u32_e32 v99, 50, v76
	v_add_u32_e32 v100, 51, v76
	v_add_u32_e32 v101, 0x41, v76
	v_add_u32_e32 v102, 0x42, v76
	v_add_u32_e32 v103, 0x43, v76
	v_add_u32_e32 v104, 0x51, v76
	v_add_u32_e32 v105, 0x52, v76
	v_add_u32_e32 v106, 0x53, v76
	v_add_u32_e32 v107, 0x61, v76
	v_add_u32_e32 v108, 0x62, v76
	v_add_u32_e32 v109, 0x63, v76
	v_add_u32_e32 v110, 0x71, v76
	v_add_u32_e32 v111, 0x72, v76
	v_add_u32_e32 v112, 0x73, v76
	v_mov_b64_e32 v[34:35], v[18:19]
	v_mov_b64_e32 v[38:39], v[22:23]
	v_mov_b64_e32 v[42:43], v[26:27]
	v_mov_b64_e32 v[46:47], v[30:31]
	s_waitcnt lgkmcnt(0)
	s_barrier
	s_branch .LBB0_1705

; #define K_FETCH(J) do { _Pragma("unroll") for (int _i = 0; _i < 4; ++_i) { const int _pc = tid + 512 * _i, _rr = _pc >> 4, _c16 = _pc & 15; ktn[_i] = *(const v4u*)(KEYS + (size_t)(J) * 16384 + _rr * 128 + _c16 * 8); } \
;         _Pragma("unroll") for (int _kk = 0; _kk < 4; ++_kk) qfn[_kk] = *(const bf16x8*)(Q + trow * 2048 + (J) * 128 + 32 * _kk + 8 * fq); } while (0)
; __device__ __forceinline__ void peer_unit(Frame& F, const Args& a, int layer, int unit, bool last) {
;     ...
;     for (int hd = 0; hd < 8; ++hd) {
;         for (int p = 0; p < 2; ++p) {
;             const int jp = hd * 2 + p;
;             if (jp + 1 < 16) K_FETCH(jp + 1);
.LBB0_1707:
	s_or_b32 s5, s55, s48
	s_add_i32 s54, s5, 1
	s_cmp_lt_u32 s5, 15
	s_cselect_b64 s[52:53], -1, 0
	s_cmp_gt_u32 s5, 14
	s_cbranch_scc1 .LBB0_1709
	s_lshl_b32 s30, s54, 15
	s_waitcnt vmcnt(5)
	v_lshl_add_u64 v[10:11], v[50:51], 0, s[30:31]
	s_lshl_b32 s30, s54, 8
	v_lshl_add_u64 v[2:3], v[52:53], 1, v[10:11]
	v_lshl_add_u64 v[6:7], v[54:55], 1, v[10:11]
	v_lshl_add_u64 v[12:13], v[56:57], 1, v[10:11]
	s_waitcnt vmcnt(4)
	v_lshl_add_u64 v[14:15], v[58:59], 1, v[10:11]
	s_waitcnt vmcnt(0)
	v_lshl_add_u64 v[46:47], v[60:61], 0, s[30:31]
	global_load_dwordx4 v[2:5], v[2:3], off
	global_load_dwordx4 v[6:9], v[6:7], off
	global_load_dwordx4 v[10:13], v[12:13], off
	global_load_dwordx4 v[14:17], v[14:15], off
	global_load_dwordx4 v[34:37], v[46:47], off
	global_load_dwordx4 v[38:41], v[46:47], off offset:64
	global_load_dwordx4 v[42:45], v[46:47], off offset:128
	global_load_dwordx4 v[46:49], v[46:47], off offset:192
